# speedup vs baseline: 1.0124x; 1.0059x over previous
.LBB2_13:
	s_or_b64 exec, exec, s[10:11]
	v_mfma_f32_16x16x32_f16 v[92:95], v[42:45], v[34:37], 0
	v_cvt_f32_f16_e32 v89, v24
	v_lshlrev_b32_e32 v52, 3, v107
	s_movk_i32 s0, 0x50
	v_mfma_f32_16x16x32_f16 v[34:37], v[38:41], v[34:37], 0
	v_cvt_f32_f16_e32 v49, v108
	s_nop 2
	v_add_f32_e32 v24, v92, v134
	v_min_f32_e32 v46, 0x42a00000, v24
	v_mul_f32_e32 v46, 0x3fb8aa3b, v46
	v_exp_f32_e32 v46, v46
	v_add_f32_e32 v48, v93, v134
	v_min_f32_e32 v50, 0x42a00000, v48
	v_mul_f32_e32 v50, 0x3fb8aa3b, v50
	v_add_f32_e32 v46, 1.0, v46
	v_log_f32_e32 v46, v46
	v_exp_f32_e32 v50, v50
	v_add_f32_e32 v56, v95, v134
	v_min_f32_e32 v58, 0x42a00000, v56
	v_mul_f32_e32 v46, 0x3f317218, v46
	v_max_f32_e32 v24, v24, v46
	v_add_f32_e32 v46, 1.0, v50
	v_add_f32_e32 v50, v94, v134
	v_min_f32_e32 v54, 0x42a00000, v50
	v_mul_f32_e32 v54, 0x3fb8aa3b, v54
	v_exp_f32_e32 v54, v54
	v_mul_f32_e32 v58, 0x3fb8aa3b, v58
	v_exp_f32_e32 v58, v58
	v_log_f32_e32 v46, v46
	v_add_f32_e32 v54, 1.0, v54
	v_log_f32_e32 v54, v54
	v_add_f32_e32 v58, 1.0, v58
	v_log_f32_e32 v58, v58
	v_mul_f32_e32 v46, 0x3f317218, v46
	v_mfma_f32_16x16x32_f16 v[92:95], v[42:45], v[30:33], 0
	v_max_f32_e32 v46, v48, v46
	v_mul_f32_e32 v48, 0x3f317218, v54
	v_max_f32_e32 v48, v50, v48
	v_mul_f32_e32 v50, 0x3f317218, v58
	v_max_f32_e32 v50, v56, v50
	v_cvt_pk_f16_f32 v97, v48, v50
	s_nop 1
	v_add_f32_e32 v48, v92, v133
	v_min_f32_e32 v50, 0x42a00000, v48
	v_mul_f32_e32 v50, 0x3fb8aa3b, v50
	v_exp_f32_e32 v50, v50
	v_cvt_pk_f16_f32 v96, v24, v46
	v_add_f32_e32 v58, v95, v133
	v_min_f32_e32 v60, 0x42a00000, v58
	v_add_f32_e32 v46, 1.0, v50
	v_add_f32_e32 v50, v93, v133
	v_min_f32_e32 v54, 0x42a00000, v50
	v_log_f32_e32 v46, v46
	v_mul_f32_e32 v54, 0x3fb8aa3b, v54
	v_exp_f32_e32 v54, v54
	v_mul_f32_e32 v60, 0x3fb8aa3b, v60
	v_mul_f32_e32 v46, 0x3f317218, v46
	v_max_f32_e32 v46, v48, v46
	v_add_f32_e32 v48, 1.0, v54
	v_add_f32_e32 v54, v94, v133
	v_min_f32_e32 v56, 0x42a00000, v54
	v_mul_f32_e32 v56, 0x3fb8aa3b, v56
	v_exp_f32_e32 v56, v56
	v_exp_f32_e32 v60, v60
	v_log_f32_e32 v48, v48
	s_waitcnt vmcnt(9)
	v_mfma_f32_16x16x32_f16 v[92:95], v[42:45], v[26:29], 0
	v_add_f32_e32 v56, 1.0, v56
	v_log_f32_e32 v56, v56
	v_add_f32_e32 v60, 1.0, v60
	v_log_f32_e32 v60, v60
	v_mul_f32_e32 v48, 0x3f317218, v48
	v_max_f32_e32 v48, v50, v48
	v_mul_f32_e32 v50, 0x3f317218, v56
	s_nop 0
	v_add_f32_e32 v56, v92, v131
	v_max_f32_e32 v50, v54, v50
	v_mul_f32_e32 v54, 0x3f317218, v60
	v_min_f32_e32 v60, 0x42a00000, v56
	v_mul_f32_e32 v60, 0x3fb8aa3b, v60
	v_exp_f32_e32 v60, v60
	v_mad_u32_u24 v24, v136, s0, v52
	ds_write_b64 v24, v[96:97]
	v_cvt_pk_f16_f32 v96, v46, v48
	v_add_f32_e32 v46, 1.0, v60
	v_log_f32_e32 v46, v46
	v_max_f32_e32 v54, v58, v54
	v_add_f32_e32 v48, v93, v131
	v_cvt_pk_f16_f32 v97, v50, v54
	v_min_f32_e32 v50, 0x42a00000, v48
	v_mul_f32_e32 v46, 0x3f317218, v46
	v_add_f32_e32 v54, v94, v131
	v_mul_f32_e32 v50, 0x3fb8aa3b, v50
	v_max_f32_e32 v46, v56, v46
	v_min_f32_e32 v56, 0x42a00000, v54
	v_exp_f32_e32 v50, v50
	v_mul_f32_e32 v56, 0x3fb8aa3b, v56
	v_exp_f32_e32 v56, v56
	s_waitcnt vmcnt(8)
	v_mfma_f32_16x16x32_f16 v[42:45], v[42:45], v[18:21], 0
	v_add_f32_e32 v50, 1.0, v50
	v_log_f32_e32 v50, v50
	v_add_f32_e32 v56, 1.0, v56
	v_log_f32_e32 v56, v56
	v_add_f32_e32 v58, v95, v131
	v_mul_f32_e32 v50, 0x3f317218, v50
	s_nop 1
	v_add_f32_e32 v42, v42, v121
	v_min_f32_e32 v60, 0x42a00000, v58
	v_max_f32_e32 v48, v48, v50
	v_mul_f32_e32 v50, 0x3f317218, v56
	v_min_f32_e32 v56, 0x42a00000, v42
	v_mul_f32_e32 v60, 0x3fb8aa3b, v60
	v_mul_f32_e32 v56, 0x3fb8aa3b, v56
	v_exp_f32_e32 v60, v60
	v_exp_f32_e32 v56, v56
	v_add_f32_e32 v43, v43, v121
	v_cvt_pk_f16_f32 v92, v46, v48
	v_add_f32_e32 v60, 1.0, v60
	v_add_f32_e32 v46, 1.0, v56
	v_min_f32_e32 v48, 0x42a00000, v43
	v_log_f32_e32 v60, v60
	v_log_f32_e32 v46, v46
	v_mul_f32_e32 v48, 0x3fb8aa3b, v48
	v_exp_f32_e32 v48, v48
	v_max_f32_e32 v50, v54, v50
	v_mul_f32_e32 v54, 0x3f317218, v60
	v_mul_f32_e32 v46, 0x3f317218, v46
	v_add_f32_e32 v44, v44, v121
	v_max_f32_e32 v54, v58, v54
	v_max_f32_e32 v42, v42, v46
	v_add_f32_e32 v46, 1.0, v48
	v_min_f32_e32 v48, 0x42a00000, v44
	v_add_f32_e32 v45, v45, v121
	v_cvt_pk_f16_f32 v93, v50, v54
	v_mul_f32_e32 v48, 0x3fb8aa3b, v48
	v_min_f32_e32 v50, 0x42a00000, v45
	v_exp_f32_e32 v48, v48
	v_mul_f32_e32 v50, 0x3fb8aa3b, v50
	v_exp_f32_e32 v50, v50
	v_log_f32_e32 v46, v46
	v_add_f32_e32 v48, 1.0, v48
	v_log_f32_e32 v48, v48
	v_add_f32_e32 v50, 1.0, v50
	v_log_f32_e32 v50, v50
	v_mul_f32_e32 v46, 0x3f317218, v46
	v_max_f32_e32 v46, v43, v46
	v_mul_f32_e32 v43, 0x3f317218, v48
	v_max_f32_e32 v43, v44, v43
	v_mul_f32_e32 v44, 0x3f317218, v50
	v_add_f32_e32 v34, v34, v134
	v_max_f32_e32 v44, v45, v44
	v_min_f32_e32 v45, 0x42a00000, v34
	v_mul_f32_e32 v45, 0x3fb8aa3b, v45
	v_exp_f32_e32 v45, v45
	v_add_f32_e32 v35, v35, v134
	v_cvt_pk_f16_f32 v43, v43, v44
	v_cvt_pk_f16_f32 v42, v42, v46
	v_mad_u32_u24 v44, v135, s0, v52
	v_add_f32_e32 v45, 1.0, v45
	v_min_f32_e32 v46, 0x42a00000, v35
	v_add_f32_e32 v36, v36, v134
	ds_write_b64 v24, v[96:97] offset:1280
	ds_write_b64 v24, v[92:93] offset:2560
	v_log_f32_e32 v45, v45
	v_mul_f32_e32 v46, 0x3fb8aa3b, v46
	ds_write_b64 v44, v[42:43]
	v_min_f32_e32 v43, 0x42a00000, v36
	v_exp_f32_e32 v46, v46
	v_mul_f32_e32 v43, 0x3fb8aa3b, v43
	v_exp_f32_e32 v43, v43
	v_add_f32_e32 v37, v37, v134
	v_mul_f32_e32 v42, 0x3f317218, v45
	v_min_f32_e32 v45, 0x42a00000, v37
	v_max_f32_e32 v34, v34, v42
	v_add_f32_e32 v42, 1.0, v46
	v_mul_f32_e32 v45, 0x3fb8aa3b, v45
	v_log_f32_e32 v42, v42
	v_exp_f32_e32 v45, v45
	v_add_f32_e32 v43, 1.0, v43
	v_mfma_f32_16x16x32_f16 v[30:33], v[38:41], v[30:33], 0
	v_log_f32_e32 v43, v43
	v_mul_f32_e32 v42, 0x3f317218, v42
	v_add_f32_e32 v45, 1.0, v45
	v_log_f32_e32 v45, v45
	v_max_f32_e32 v42, v35, v42
	s_nop 2
	v_add_f32_e32 v30, v30, v133
	v_mul_f32_e32 v35, 0x3f317218, v43
	v_min_f32_e32 v43, 0x42a00000, v30
	v_mul_f32_e32 v43, 0x3fb8aa3b, v43
	v_exp_f32_e32 v43, v43
	v_max_f32_e32 v35, v36, v35
	v_mul_f32_e32 v36, 0x3f317218, v45
	v_max_f32_e32 v36, v37, v36
	v_add_f32_e32 v31, v31, v133
	v_cvt_pk_f16_f32 v35, v35, v36
	v_cvt_pk_f16_f32 v34, v34, v42
	v_add_f32_e32 v36, 1.0, v43
	v_min_f32_e32 v37, 0x42a00000, v31
	v_add_f32_e32 v32, v32, v133
	v_log_f32_e32 v36, v36
	v_mul_f32_e32 v37, 0x3fb8aa3b, v37
	ds_write_b64 v24, v[34:35] offset:32
	v_min_f32_e32 v35, 0x42a00000, v32
	v_exp_f32_e32 v37, v37
	v_mul_f32_e32 v35, 0x3fb8aa3b, v35
	v_exp_f32_e32 v35, v35
	v_add_f32_e32 v33, v33, v133
	v_mul_f32_e32 v34, 0x3f317218, v36
	v_min_f32_e32 v36, 0x42a00000, v33
	v_max_f32_e32 v30, v30, v34
	v_add_f32_e32 v34, 1.0, v37
	v_mul_f32_e32 v36, 0x3fb8aa3b, v36
	v_log_f32_e32 v34, v34
	v_exp_f32_e32 v36, v36
	v_add_f32_e32 v35, 1.0, v35
	v_mfma_f32_16x16x32_f16 v[26:29], v[38:41], v[26:29], 0
	v_log_f32_e32 v35, v35
	v_mul_f32_e32 v34, 0x3f317218, v34
	v_add_f32_e32 v36, 1.0, v36
	v_log_f32_e32 v36, v36
	v_max_f32_e32 v34, v31, v34
	s_nop 2
	v_add_f32_e32 v26, v26, v131
	v_mul_f32_e32 v31, 0x3f317218, v35
	v_min_f32_e32 v35, 0x42a00000, v26
	v_mul_f32_e32 v35, 0x3fb8aa3b, v35
	v_exp_f32_e32 v35, v35
	v_max_f32_e32 v31, v32, v31
	v_mul_f32_e32 v32, 0x3f317218, v36
	v_max_f32_e32 v32, v33, v32
	v_add_f32_e32 v27, v27, v131
	v_cvt_pk_f16_f32 v31, v31, v32
	v_cvt_pk_f16_f32 v30, v30, v34
	v_add_f32_e32 v32, 1.0, v35
	v_min_f32_e32 v33, 0x42a00000, v27
	v_add_f32_e32 v28, v28, v131
	v_log_f32_e32 v32, v32
	v_mul_f32_e32 v33, 0x3fb8aa3b, v33
	ds_write_b64 v24, v[30:31] offset:1312
	v_min_f32_e32 v31, 0x42a00000, v28
	v_exp_f32_e32 v33, v33
	v_mul_f32_e32 v31, 0x3fb8aa3b, v31
	v_exp_f32_e32 v31, v31
	v_add_f32_e32 v29, v29, v131
	v_mul_f32_e32 v30, 0x3f317218, v32
	v_min_f32_e32 v32, 0x42a00000, v29
	v_max_f32_e32 v26, v26, v30
	v_add_f32_e32 v30, 1.0, v33
	v_mul_f32_e32 v32, 0x3fb8aa3b, v32
	v_log_f32_e32 v30, v30
	v_exp_f32_e32 v32, v32
	v_add_f32_e32 v31, 1.0, v31
	v_mfma_f32_16x16x32_f16 v[18:21], v[38:41], v[18:21], 0
	v_log_f32_e32 v31, v31
	v_mul_f32_e32 v30, 0x3f317218, v30
	v_add_f32_e32 v32, 1.0, v32
	v_log_f32_e32 v32, v32
	v_max_f32_e32 v30, v27, v30
	s_nop 2
	v_add_f32_e32 v18, v18, v121
	v_mul_f32_e32 v27, 0x3f317218, v31
	v_min_f32_e32 v31, 0x42a00000, v18
	v_mul_f32_e32 v31, 0x3fb8aa3b, v31
	v_exp_f32_e32 v31, v31
	v_max_f32_e32 v27, v28, v27
	v_mul_f32_e32 v28, 0x3f317218, v32
	v_max_f32_e32 v28, v29, v28
	v_add_f32_e32 v19, v19, v121
	v_cvt_pk_f16_f32 v27, v27, v28
	v_cvt_pk_f16_f32 v26, v26, v30
	v_add_f32_e32 v28, 1.0, v31
	v_min_f32_e32 v29, 0x42a00000, v19
	v_add_f32_e32 v20, v20, v121
	v_log_f32_e32 v28, v28
	v_mul_f32_e32 v29, 0x3fb8aa3b, v29
	ds_write_b64 v24, v[26:27] offset:2592
	v_min_f32_e32 v26, 0x42a00000, v20
	v_add_f32_e32 v21, v21, v121
	v_exp_f32_e32 v29, v29
	v_mul_f32_e32 v26, 0x3fb8aa3b, v26
	v_min_f32_e32 v27, 0x42a00000, v21
	v_exp_f32_e32 v26, v26
	v_mul_f32_e32 v27, 0x3fb8aa3b, v27
	v_exp_f32_e32 v27, v27
	v_mul_f32_e32 v24, 0x3f317218, v28
	v_max_f32_e32 v18, v18, v24
	v_add_f32_e32 v24, 1.0, v29
	v_log_f32_e32 v24, v24
	v_add_f32_e32 v26, 1.0, v26
	v_log_f32_e32 v26, v26
	v_add_f32_e32 v27, 1.0, v27
	v_log_f32_e32 v27, v27
	v_mul_f32_e32 v24, 0x3f317218, v24
	v_max_f32_e32 v24, v19, v24
	v_mul_f32_e32 v19, 0x3f317218, v26
	v_max_f32_e32 v19, v20, v19
	v_mul_f32_e32 v20, 0x3f317218, v27
	v_max_f32_e32 v20, v21, v20
	v_cvt_pk_f16_f32 v19, v19, v20
	v_cvt_pk_f16_f32 v18, v18, v24
	ds_write_b64 v44, v[18:19] offset:32
	v_mul_u32_u24_e32 v18, 0x50, v0
	s_waitcnt lgkmcnt(0)
	s_barrier
	ds_read_b128 v[92:95], v18
	v_cvt_f32_f16_e32 v55, v111
	v_cvt_f32_f16_e32 v59, v110
	v_cvt_f32_f16_e32 v79, v105
	v_cvt_f32_f16_e32 v82, v104
	v_cvt_f32_f16_e32 v84, v103
	v_cvt_f32_f16_e32 v86, v102
	ds_read_b128 v[96:99], v18 offset:16
	ds_read_b128 v[100:103], v18 offset:32
	ds_read_b128 v[108:111], v18 offset:48
	v_lshl_add_u64 v[104:105], s[8:9], 0, v[118:119]
	v_cvt_f32_f16_e32 v47, v113
	v_cvt_f32_f16_e32 v51, v112
	v_lshl_add_u64 v[112:113], v[104:105], 0, s[6:7]
	s_waitcnt lgkmcnt(3)
	v_cvt_f32_f16_e32 v26, v94
	v_cvt_f32_f16_sdwa v28, v94 dst_sel:DWORD dst_unused:UNUSED_PAD src0_sel:WORD_1
	v_cvt_f32_f16_e32 v30, v95
	v_cvt_f32_f16_sdwa v32, v95 dst_sel:DWORD dst_unused:UNUSED_PAD src0_sel:WORD_1
	global_store_dwordx4 v[112:113], v[92:95], off sc0 sc1
	v_cvt_f32_f16_e32 v53, v122
	v_cvt_f32_f16_e32 v57, v125
	v_lshl_add_u64 v[94:95], v[104:105], 0, s[14:15]
	s_waitcnt lgkmcnt(2)
	global_store_dwordx4 v[94:95], v[96:99], off sc0 sc1
	v_lshl_add_u64 v[94:95], v[104:105], 0, s[16:17]
	s_waitcnt lgkmcnt(1)
	global_store_dwordx4 v[94:95], v[100:103], off sc0 sc1
	v_lshl_add_u64 v[94:95], v[104:105], 0, s[18:19]
	v_cvt_f32_f16_e32 v61, v124
	v_cvt_f32_f16_e32 v63, v117
	v_cvt_f32_f16_e32 v65, v147
	v_cvt_f32_f16_e32 v67, v116
	v_cvt_f32_f16_e32 v69, v145
	v_cvt_f32_f16_e32 v71, v115
	v_cvt_f32_f16_e32 v73, v127
	v_cvt_f32_f16_e32 v75, v114
	v_cvt_f32_f16_e32 v77, v126
	v_cvt_f32_f16_e32 v81, v142
	v_cvt_f32_f16_e32 v83, v141
	v_cvt_f32_f16_e32 v85, v140
	v_cvt_f32_f16_e32 v87, v139
	v_cvt_f32_f16_e32 v25, v25
	v_cvt_f32_f16_e32 v88, v138
	v_cvt_f32_f16_e32 v90, v137
	v_cvt_f32_f16_e32 v23, v23
	v_cvt_f32_f16_e32 v91, v123
	v_cvt_f32_f16_e32 v19, v22
	v_cvt_f32_f16_sdwa v20, v92 dst_sel:DWORD dst_unused:UNUSED_PAD src0_sel:WORD_1
	v_cvt_f32_f16_e32 v22, v93
	v_cvt_f32_f16_sdwa v24, v93 dst_sel:DWORD dst_unused:UNUSED_PAD src0_sel:WORD_1
	v_cvt_f32_f16_e32 v34, v96
	v_cvt_f32_f16_sdwa v36, v96 dst_sel:DWORD dst_unused:UNUSED_PAD src0_sel:WORD_1
	v_cvt_f32_f16_e32 v38, v97
	v_cvt_f32_f16_sdwa v40, v97 dst_sel:DWORD dst_unused:UNUSED_PAD src0_sel:WORD_1
	v_cvt_f32_f16_e32 v42, v98
	v_cvt_f32_f16_sdwa v44, v98 dst_sel:DWORD dst_unused:UNUSED_PAD src0_sel:WORD_1
	v_cvt_f32_f16_e32 v46, v99
	v_cvt_f32_f16_sdwa v48, v99 dst_sel:DWORD dst_unused:UNUSED_PAD src0_sel:WORD_1
	v_cvt_f32_f16_e32 v50, v100
	v_cvt_f32_f16_sdwa v52, v100 dst_sel:DWORD dst_unused:UNUSED_PAD src0_sel:WORD_1
	v_cvt_f32_f16_e32 v54, v101
	v_cvt_f32_f16_sdwa v56, v101 dst_sel:DWORD dst_unused:UNUSED_PAD src0_sel:WORD_1
	v_cvt_f32_f16_e32 v58, v102
	v_cvt_f32_f16_sdwa v60, v102 dst_sel:DWORD dst_unused:UNUSED_PAD src0_sel:WORD_1
	v_cvt_f32_f16_e32 v62, v103
	v_cvt_f32_f16_sdwa v64, v103 dst_sel:DWORD dst_unused:UNUSED_PAD src0_sel:WORD_1
	s_waitcnt lgkmcnt(0)
	v_cvt_f32_f16_e32 v66, v108
	v_cvt_f32_f16_sdwa v68, v108 dst_sel:DWORD dst_unused:UNUSED_PAD src0_sel:WORD_1
	v_cvt_f32_f16_e32 v70, v109
	v_cvt_f32_f16_sdwa v72, v109 dst_sel:DWORD dst_unused:UNUSED_PAD src0_sel:WORD_1
	v_cvt_f32_f16_e32 v74, v110
	v_cvt_f32_f16_sdwa v76, v110 dst_sel:DWORD dst_unused:UNUSED_PAD src0_sel:WORD_1
	v_cvt_f32_f16_e32 v78, v111
	v_cvt_f32_f16_sdwa v18, v111 dst_sel:DWORD dst_unused:UNUSED_PAD src0_sel:WORD_1
	global_store_dwordx4 v[94:95], v[108:111], off sc0 sc1
	v_cvt_f32_f16_e32 v80, v92
	v_mov_b32_e32 v160, 0
	ds_read_b128 v[92:95], v160 offset:41024
	ds_read_b128 v[96:99], v160 offset:41040
	ds_read_b128 v[100:103], v160 offset:41056
	ds_read_b128 v[108:111], v160 offset:41072
	s_waitcnt lgkmcnt(0)
	ds_read_b128 v[112:115], v160 offset:41232
	ds_read_b128 v[116:119], v160 offset:41248
	ds_read_b128 v[120:123], v160 offset:41264
	ds_read_b128 v[124:127], v160 offset:41280
	s_lshr_b32 s0, s23, 5
	s_waitcnt vmcnt(11)
	v_mul_f32_e32 v104, v80, v19
	v_pk_mul_f32 v[128:129], v[104:105], v[92:93] op_sel_hi:[0,1]
	v_pk_mul_f32 v[130:131], v[104:105], v[94:95] op_sel_hi:[0,1]
	s_waitcnt vmcnt(10)
	v_pk_mul_f32 v[132:133], v[104:105], v[96:97] op_sel_hi:[0,1]
	v_pk_mul_f32 v[134:135], v[104:105], v[98:99] op_sel_hi:[0,1]
	s_waitcnt vmcnt(9)
	v_pk_mul_f32 v[136:137], v[104:105], v[100:101] op_sel_hi:[0,1]
	v_pk_mul_f32 v[138:139], v[104:105], v[102:103] op_sel_hi:[0,1]
	s_waitcnt vmcnt(8)
	v_pk_mul_f32 v[140:141], v[104:105], v[108:109] op_sel_hi:[0,1]
	v_pk_mul_f32 v[104:105], v[104:105], v[110:111] op_sel_hi:[0,1]
	s_waitcnt lgkmcnt(0)
	s_and_b32 s6, s22, 0x7ffffc0
	ds_read_b128 v[92:95], v160 offset:41440
	ds_read_b128 v[96:99], v160 offset:41456
	ds_read_b128 v[100:103], v160 offset:41472
	ds_read_b128 v[108:111], v160 offset:41488
	v_pk_mul_f32 v[142:143], v[20:21], v[14:15] op_sel_hi:[0,1]
	v_exp_f32_e32 v142, v142
	v_exp_f32_e32 v143, v143
	v_mul_f32_e32 v144, v20, v91
	v_pk_mul_f32 v[112:113], v[144:145], v[112:113] op_sel_hi:[0,1]
	v_pk_mul_f32 v[114:115], v[144:145], v[114:115] op_sel_hi:[0,1]
	v_pk_fma_f32 v[128:129], v[128:129], v[142:143], v[112:113]
	v_pk_mul_f32 v[112:113], v[20:21], v[16:17] op_sel_hi:[0,1]
	v_exp_f32_e32 v112, v112
	v_exp_f32_e32 v113, v113
	v_pk_mul_f32 v[116:117], v[144:145], v[116:117] op_sel_hi:[0,1]
	s_or_b32 s0, s0, s6
	s_lshl_b64 s[6:7], s[0:1], 14
	v_pk_fma_f32 v[130:131], v[130:131], v[112:113], v[114:115]
	v_pk_mul_f32 v[112:113], v[20:21], v[10:11] op_sel_hi:[0,1]
	v_exp_f32_e32 v112, v112
	v_exp_f32_e32 v113, v113
	v_pk_mul_f32 v[114:115], v[20:21], v[12:13] op_sel_hi:[0,1]
	v_exp_f32_e32 v114, v114
	v_exp_f32_e32 v115, v115
	v_pk_fma_f32 v[132:133], v[132:133], v[112:113], v[116:117]
	v_pk_mul_f32 v[112:113], v[144:145], v[118:119] op_sel_hi:[0,1]
	v_pk_mul_f32 v[116:117], v[144:145], v[120:121] op_sel_hi:[0,1]
	v_pk_fma_f32 v[134:135], v[134:135], v[114:115], v[112:113]
	v_pk_mul_f32 v[112:113], v[20:21], v[6:7] op_sel_hi:[0,1]
	v_exp_f32_e32 v112, v112
	v_exp_f32_e32 v113, v113
	v_pk_mul_f32 v[114:115], v[20:21], v[8:9] op_sel_hi:[0,1]
	v_exp_f32_e32 v114, v114
	v_exp_f32_e32 v115, v115
	v_pk_fma_f32 v[136:137], v[136:137], v[112:113], v[116:117]
	v_pk_mul_f32 v[112:113], v[144:145], v[122:123] op_sel_hi:[0,1]
	v_pk_mul_f32 v[116:117], v[144:145], v[124:125] op_sel_hi:[0,1]
	v_pk_fma_f32 v[138:139], v[138:139], v[114:115], v[112:113]
	v_pk_mul_f32 v[112:113], v[20:21], v[2:3] op_sel_hi:[0,1]
	v_exp_f32_e32 v112, v112
	v_exp_f32_e32 v113, v113
	v_pk_mul_f32 v[114:115], v[20:21], v[4:5] op_sel_hi:[0,1]
	v_exp_f32_e32 v114, v114
	v_exp_f32_e32 v115, v115
	v_pk_fma_f32 v[140:141], v[140:141], v[112:113], v[116:117]
	v_pk_mul_f32 v[112:113], v[144:145], v[126:127] op_sel_hi:[0,1]
	s_lshl_b64 s[0:1], s[0:1], 11
	v_pk_fma_f32 v[104:105], v[104:105], v[114:115], v[112:113]
	s_add_u32 s0, s2, s0
	s_waitcnt lgkmcnt(0)
	s_addc_u32 s1, s3, s1
	ds_read_b128 v[112:115], v160 offset:41648
	ds_read_b128 v[116:119], v160 offset:41664
	ds_read_b128 v[120:123], v160 offset:41680
	ds_read_b128 v[124:127], v160 offset:41696
	v_pk_mul_f32 v[142:143], v[22:23], v[14:15] op_sel_hi:[0,1]
	v_exp_f32_e32 v142, v142
	v_exp_f32_e32 v143, v143
	v_mul_f32_e32 v144, v22, v23
	v_pk_mul_f32 v[92:93], v[144:145], v[92:93] op_sel_hi:[0,1]
	v_pk_mul_f32 v[94:95], v[144:145], v[94:95] op_sel_hi:[0,1]
	v_pk_fma_f32 v[128:129], v[128:129], v[142:143], v[92:93]
	v_pk_mul_f32 v[92:93], v[22:23], v[16:17] op_sel_hi:[0,1]
	v_exp_f32_e32 v92, v92
	v_exp_f32_e32 v93, v93
	v_pk_mul_f32 v[96:97], v[144:145], v[96:97] op_sel_hi:[0,1]
	v_pk_fma_f32 v[130:131], v[130:131], v[92:93], v[94:95]
	v_pk_mul_f32 v[92:93], v[22:23], v[10:11] op_sel_hi:[0,1]
	v_exp_f32_e32 v92, v92
	v_exp_f32_e32 v93, v93
	v_pk_mul_f32 v[94:95], v[22:23], v[12:13] op_sel_hi:[0,1]
	v_exp_f32_e32 v94, v94
	v_exp_f32_e32 v95, v95
	v_pk_fma_f32 v[132:133], v[132:133], v[92:93], v[96:97]
	v_pk_mul_f32 v[92:93], v[144:145], v[98:99] op_sel_hi:[0,1]
	v_pk_mul_f32 v[96:97], v[144:145], v[100:101] op_sel_hi:[0,1]
	v_pk_fma_f32 v[134:135], v[134:135], v[94:95], v[92:93]
	v_pk_mul_f32 v[92:93], v[22:23], v[6:7] op_sel_hi:[0,1]
	v_exp_f32_e32 v92, v92
	v_exp_f32_e32 v93, v93
	v_pk_mul_f32 v[94:95], v[22:23], v[8:9] op_sel_hi:[0,1]
	v_exp_f32_e32 v94, v94
	v_exp_f32_e32 v95, v95
	v_pk_fma_f32 v[136:137], v[136:137], v[92:93], v[96:97]
	v_pk_mul_f32 v[92:93], v[144:145], v[102:103] op_sel_hi:[0,1]
	v_pk_mul_f32 v[96:97], v[144:145], v[108:109] op_sel_hi:[0,1]
	v_pk_fma_f32 v[138:139], v[138:139], v[94:95], v[92:93]
	v_pk_mul_f32 v[92:93], v[22:23], v[2:3] op_sel_hi:[0,1]
	v_exp_f32_e32 v92, v92
	v_exp_f32_e32 v93, v93
	v_pk_mul_f32 v[94:95], v[22:23], v[4:5] op_sel_hi:[0,1]
	v_exp_f32_e32 v94, v94
	v_exp_f32_e32 v95, v95
	v_pk_fma_f32 v[140:141], v[140:141], v[92:93], v[96:97]
	v_pk_mul_f32 v[92:93], v[144:145], v[110:111] op_sel_hi:[0,1]
	v_pk_fma_f32 v[104:105], v[104:105], v[94:95], v[92:93]
	s_nop 0
	s_waitcnt lgkmcnt(0)
	s_nop 0
	ds_read_b128 v[92:95], v160 offset:41856
	ds_read_b128 v[96:99], v160 offset:41872
	ds_read_b128 v[100:103], v160 offset:41888
	ds_read_b128 v[108:111], v160 offset:41904
	v_pk_mul_f32 v[142:143], v[24:25], v[14:15] op_sel_hi:[0,1]
	v_exp_f32_e32 v142, v142
	v_exp_f32_e32 v143, v143
	v_mul_f32_e32 v90, v24, v90
	v_pk_mul_f32 v[112:113], v[90:91], v[112:113] op_sel_hi:[0,1]
	v_pk_mul_f32 v[114:115], v[90:91], v[114:115] op_sel_hi:[0,1]
	v_pk_fma_f32 v[128:129], v[128:129], v[142:143], v[112:113]
	v_pk_mul_f32 v[112:113], v[24:25], v[16:17] op_sel_hi:[0,1]
	v_exp_f32_e32 v112, v112
	v_exp_f32_e32 v113, v113
	v_pk_mul_f32 v[116:117], v[90:91], v[116:117] op_sel_hi:[0,1]
	v_pk_fma_f32 v[130:131], v[130:131], v[112:113], v[114:115]
	v_pk_mul_f32 v[112:113], v[24:25], v[10:11] op_sel_hi:[0,1]
	v_exp_f32_e32 v112, v112
	v_exp_f32_e32 v113, v113
	v_pk_mul_f32 v[114:115], v[24:25], v[12:13] op_sel_hi:[0,1]
	v_exp_f32_e32 v114, v114
	v_exp_f32_e32 v115, v115
	v_pk_fma_f32 v[132:133], v[132:133], v[112:113], v[116:117]
	v_pk_mul_f32 v[112:113], v[90:91], v[118:119] op_sel_hi:[0,1]
	v_pk_mul_f32 v[116:117], v[90:91], v[120:121] op_sel_hi:[0,1]
	v_pk_fma_f32 v[134:135], v[134:135], v[114:115], v[112:113]
	v_pk_mul_f32 v[112:113], v[24:25], v[6:7] op_sel_hi:[0,1]
	v_exp_f32_e32 v112, v112
	v_exp_f32_e32 v113, v113
	v_pk_mul_f32 v[114:115], v[24:25], v[8:9] op_sel_hi:[0,1]
	v_exp_f32_e32 v114, v114
	v_exp_f32_e32 v115, v115
	v_pk_fma_f32 v[136:137], v[136:137], v[112:113], v[116:117]
	v_pk_mul_f32 v[112:113], v[90:91], v[122:123] op_sel_hi:[0,1]
	v_pk_mul_f32 v[116:117], v[90:91], v[124:125] op_sel_hi:[0,1]
	v_pk_fma_f32 v[138:139], v[138:139], v[114:115], v[112:113]
	v_pk_mul_f32 v[112:113], v[24:25], v[2:3] op_sel_hi:[0,1]
	v_pk_mul_f32 v[114:115], v[24:25], v[4:5] op_sel_hi:[0,1]
	v_exp_f32_e32 v112, v112
	v_exp_f32_e32 v113, v113
	v_exp_f32_e32 v114, v114
	v_exp_f32_e32 v115, v115
	v_pk_mul_f32 v[90:91], v[90:91], v[126:127] op_sel_hi:[0,1]
	v_pk_fma_f32 v[140:141], v[140:141], v[112:113], v[116:117]
	v_pk_fma_f32 v[90:91], v[104:105], v[114:115], v[90:91]
	s_nop 0
	s_waitcnt lgkmcnt(0)
	s_nop 0
	ds_read_b128 v[112:115], v160 offset:42064
	ds_read_b128 v[116:119], v160 offset:42080
	ds_read_b128 v[120:123], v160 offset:42096
	ds_read_b128 v[124:127], v160 offset:42112
	v_pk_mul_f32 v[104:105], v[26:27], v[14:15] op_sel_hi:[0,1]
	v_exp_f32_e32 v104, v104
	v_exp_f32_e32 v105, v105
	v_mul_f32_e32 v142, v26, v89
	v_pk_mul_f32 v[92:93], v[142:143], v[92:93] op_sel_hi:[0,1]
	v_pk_mul_f32 v[94:95], v[142:143], v[94:95] op_sel_hi:[0,1]
	v_pk_fma_f32 v[128:129], v[128:129], v[104:105], v[92:93]
	v_pk_mul_f32 v[92:93], v[26:27], v[16:17] op_sel_hi:[0,1]
	v_exp_f32_e32 v92, v92
	v_exp_f32_e32 v93, v93
	v_pk_mul_f32 v[96:97], v[142:143], v[96:97] op_sel_hi:[0,1]
	v_pk_fma_f32 v[130:131], v[130:131], v[92:93], v[94:95]
	v_pk_mul_f32 v[92:93], v[26:27], v[10:11] op_sel_hi:[0,1]
	v_exp_f32_e32 v92, v92
	v_exp_f32_e32 v93, v93
	v_pk_mul_f32 v[94:95], v[26:27], v[12:13] op_sel_hi:[0,1]
	v_exp_f32_e32 v94, v94
	v_exp_f32_e32 v95, v95
	v_pk_fma_f32 v[132:133], v[132:133], v[92:93], v[96:97]
	v_pk_mul_f32 v[92:93], v[142:143], v[98:99] op_sel_hi:[0,1]
	v_pk_mul_f32 v[96:97], v[142:143], v[100:101] op_sel_hi:[0,1]
	v_pk_fma_f32 v[134:135], v[134:135], v[94:95], v[92:93]
	v_pk_mul_f32 v[92:93], v[26:27], v[6:7] op_sel_hi:[0,1]
	v_exp_f32_e32 v92, v92
	v_exp_f32_e32 v93, v93
	v_pk_mul_f32 v[94:95], v[26:27], v[8:9] op_sel_hi:[0,1]
	v_exp_f32_e32 v94, v94
	v_exp_f32_e32 v95, v95
	v_pk_fma_f32 v[136:137], v[136:137], v[92:93], v[96:97]
	v_pk_mul_f32 v[92:93], v[142:143], v[102:103] op_sel_hi:[0,1]
	v_pk_mul_f32 v[96:97], v[142:143], v[108:109] op_sel_hi:[0,1]
	v_pk_fma_f32 v[138:139], v[138:139], v[94:95], v[92:93]
	v_pk_mul_f32 v[92:93], v[26:27], v[2:3] op_sel_hi:[0,1]
	v_exp_f32_e32 v92, v92
	v_exp_f32_e32 v93, v93
	v_pk_mul_f32 v[94:95], v[26:27], v[4:5] op_sel_hi:[0,1]
	v_exp_f32_e32 v94, v94
	v_exp_f32_e32 v95, v95
	v_pk_fma_f32 v[108:109], v[140:141], v[92:93], v[96:97]
	v_pk_mul_f32 v[92:93], v[142:143], v[110:111] op_sel_hi:[0,1]
	v_pk_fma_f32 v[110:111], v[90:91], v[94:95], v[92:93]
	s_nop 0
	s_waitcnt lgkmcnt(0)
	s_nop 0
	ds_read_b128 v[90:93], v160 offset:42272
	ds_read_b128 v[94:97], v160 offset:42288
	ds_read_b128 v[98:101], v160 offset:42304
	ds_read_b128 v[102:105], v160 offset:42320
	v_pk_mul_f32 v[140:141], v[28:29], v[14:15] op_sel_hi:[0,1]
	v_exp_f32_e32 v140, v140
	v_exp_f32_e32 v141, v141
	v_pk_mul_f32 v[142:143], v[28:29], v[16:17] op_sel_hi:[0,1]
	v_exp_f32_e32 v142, v142
	v_exp_f32_e32 v143, v143
	v_mul_f32_e32 v88, v28, v88
	v_pk_mul_f32 v[112:113], v[88:89], v[112:113] op_sel_hi:[0,1]
	v_pk_fma_f32 v[128:129], v[128:129], v[140:141], v[112:113]
	v_pk_mul_f32 v[112:113], v[88:89], v[114:115] op_sel_hi:[0,1]
	v_pk_fma_f32 v[130:131], v[130:131], v[142:143], v[112:113]
	v_pk_mul_f32 v[112:113], v[28:29], v[10:11] op_sel_hi:[0,1]
	v_exp_f32_e32 v112, v112
	v_exp_f32_e32 v113, v113
	v_pk_mul_f32 v[114:115], v[28:29], v[12:13] op_sel_hi:[0,1]
	v_exp_f32_e32 v114, v114
	v_exp_f32_e32 v115, v115
	v_pk_mul_f32 v[116:117], v[88:89], v[116:117] op_sel_hi:[0,1]
	v_pk_fma_f32 v[132:133], v[132:133], v[112:113], v[116:117]
	v_pk_mul_f32 v[112:113], v[88:89], v[118:119] op_sel_hi:[0,1]
	v_pk_fma_f32 v[134:135], v[134:135], v[114:115], v[112:113]
	v_pk_mul_f32 v[112:113], v[28:29], v[6:7] op_sel_hi:[0,1]
	v_exp_f32_e32 v112, v112
	v_exp_f32_e32 v113, v113
	v_pk_mul_f32 v[114:115], v[28:29], v[8:9] op_sel_hi:[0,1]
	v_exp_f32_e32 v114, v114
	v_exp_f32_e32 v115, v115
	v_pk_mul_f32 v[116:117], v[88:89], v[120:121] op_sel_hi:[0,1]
	v_pk_fma_f32 v[136:137], v[136:137], v[112:113], v[116:117]
	v_pk_mul_f32 v[112:113], v[88:89], v[122:123] op_sel_hi:[0,1]
	v_pk_fma_f32 v[138:139], v[138:139], v[114:115], v[112:113]
	v_pk_mul_f32 v[112:113], v[28:29], v[2:3] op_sel_hi:[0,1]
	v_pk_mul_f32 v[114:115], v[28:29], v[4:5] op_sel_hi:[0,1]
	v_exp_f32_e32 v112, v112
	v_exp_f32_e32 v113, v113
	v_exp_f32_e32 v114, v114
	v_exp_f32_e32 v115, v115
	v_pk_mul_f32 v[116:117], v[88:89], v[124:125] op_sel_hi:[0,1]
	v_pk_mul_f32 v[88:89], v[88:89], v[126:127] op_sel_hi:[0,1]
	v_pk_fma_f32 v[124:125], v[108:109], v[112:113], v[116:117]
	v_pk_fma_f32 v[88:89], v[110:111], v[114:115], v[88:89]
	s_nop 0
	s_waitcnt lgkmcnt(0)
	s_nop 0
	ds_read_b128 v[108:111], v160 offset:42480
	ds_read_b128 v[112:115], v160 offset:42496
	ds_read_b128 v[116:119], v160 offset:42512
	ds_read_b128 v[120:123], v160 offset:42528
	v_pk_mul_f32 v[140:141], v[30:31], v[14:15] op_sel_hi:[0,1]
	v_exp_f32_e32 v140, v140
	v_exp_f32_e32 v141, v141
	v_pk_mul_f32 v[142:143], v[30:31], v[16:17] op_sel_hi:[0,1]
	v_exp_f32_e32 v142, v142
	v_exp_f32_e32 v143, v143
	v_mul_f32_e32 v126, v30, v25
	v_pk_mul_f32 v[90:91], v[126:127], v[90:91] op_sel_hi:[0,1]
	v_pk_fma_f32 v[128:129], v[128:129], v[140:141], v[90:91]
	v_pk_mul_f32 v[90:91], v[126:127], v[92:93] op_sel_hi:[0,1]
	v_pk_fma_f32 v[130:131], v[130:131], v[142:143], v[90:91]
	v_pk_mul_f32 v[90:91], v[30:31], v[10:11] op_sel_hi:[0,1]
	v_exp_f32_e32 v90, v90
	v_exp_f32_e32 v91, v91
	v_pk_mul_f32 v[92:93], v[30:31], v[12:13] op_sel_hi:[0,1]
	v_exp_f32_e32 v92, v92
	v_exp_f32_e32 v93, v93
	v_pk_mul_f32 v[94:95], v[126:127], v[94:95] op_sel_hi:[0,1]
	v_pk_fma_f32 v[132:133], v[132:133], v[90:91], v[94:95]
	v_pk_mul_f32 v[90:91], v[126:127], v[96:97] op_sel_hi:[0,1]
	v_pk_fma_f32 v[134:135], v[134:135], v[92:93], v[90:91]
	v_pk_mul_f32 v[90:91], v[30:31], v[6:7] op_sel_hi:[0,1]
	v_exp_f32_e32 v90, v90
	v_exp_f32_e32 v91, v91
	v_pk_mul_f32 v[92:93], v[30:31], v[8:9] op_sel_hi:[0,1]
	v_exp_f32_e32 v92, v92
	v_exp_f32_e32 v93, v93
	v_pk_mul_f32 v[94:95], v[126:127], v[98:99] op_sel_hi:[0,1]
	v_pk_fma_f32 v[136:137], v[136:137], v[90:91], v[94:95]
	v_pk_mul_f32 v[90:91], v[126:127], v[100:101] op_sel_hi:[0,1]
	v_pk_fma_f32 v[138:139], v[138:139], v[92:93], v[90:91]
	v_pk_mul_f32 v[90:91], v[30:31], v[2:3] op_sel_hi:[0,1]
	v_exp_f32_e32 v90, v90
	v_exp_f32_e32 v91, v91
	v_pk_mul_f32 v[92:93], v[30:31], v[4:5] op_sel_hi:[0,1]
	v_exp_f32_e32 v92, v92
	v_exp_f32_e32 v93, v93
	v_pk_mul_f32 v[94:95], v[126:127], v[102:103] op_sel_hi:[0,1]
	v_pk_fma_f32 v[124:125], v[124:125], v[90:91], v[94:95]
	v_pk_mul_f32 v[90:91], v[126:127], v[104:105] op_sel_hi:[0,1]
	v_pk_fma_f32 v[104:105], v[88:89], v[92:93], v[90:91]
	s_nop 0
	s_waitcnt lgkmcnt(0)
	s_nop 0
	ds_read_b128 v[88:91], v160 offset:42688
	ds_read_b128 v[92:95], v160 offset:42704
	ds_read_b128 v[96:99], v160 offset:42720
	ds_read_b128 v[100:103], v160 offset:42736
	v_pk_mul_f32 v[140:141], v[32:33], v[14:15] op_sel_hi:[0,1]
	v_exp_f32_e32 v140, v140
	v_exp_f32_e32 v141, v141
	v_pk_mul_f32 v[142:143], v[32:33], v[16:17] op_sel_hi:[0,1]
	v_exp_f32_e32 v142, v142
	v_exp_f32_e32 v143, v143
	v_mul_f32_e32 v126, v32, v87
	v_pk_mul_f32 v[108:109], v[126:127], v[108:109] op_sel_hi:[0,1]
	v_pk_fma_f32 v[128:129], v[128:129], v[140:141], v[108:109]
	v_pk_mul_f32 v[108:109], v[126:127], v[110:111] op_sel_hi:[0,1]
	v_pk_fma_f32 v[130:131], v[130:131], v[142:143], v[108:109]
	v_pk_mul_f32 v[108:109], v[32:33], v[10:11] op_sel_hi:[0,1]
	v_exp_f32_e32 v108, v108
	v_exp_f32_e32 v109, v109
	v_pk_mul_f32 v[110:111], v[32:33], v[12:13] op_sel_hi:[0,1]
	v_exp_f32_e32 v110, v110
	v_exp_f32_e32 v111, v111
	v_pk_mul_f32 v[112:113], v[126:127], v[112:113] op_sel_hi:[0,1]
	v_pk_fma_f32 v[132:133], v[132:133], v[108:109], v[112:113]
	v_pk_mul_f32 v[108:109], v[126:127], v[114:115] op_sel_hi:[0,1]
	v_pk_fma_f32 v[134:135], v[134:135], v[110:111], v[108:109]
	v_pk_mul_f32 v[108:109], v[32:33], v[6:7] op_sel_hi:[0,1]
	v_exp_f32_e32 v108, v108
	v_exp_f32_e32 v109, v109
	v_pk_mul_f32 v[110:111], v[32:33], v[8:9] op_sel_hi:[0,1]
	v_exp_f32_e32 v110, v110
	v_exp_f32_e32 v111, v111
	v_pk_mul_f32 v[112:113], v[126:127], v[116:117] op_sel_hi:[0,1]
	v_pk_fma_f32 v[136:137], v[136:137], v[108:109], v[112:113]
	v_pk_mul_f32 v[108:109], v[126:127], v[118:119] op_sel_hi:[0,1]
	v_pk_fma_f32 v[138:139], v[138:139], v[110:111], v[108:109]
	v_pk_mul_f32 v[108:109], v[32:33], v[2:3] op_sel_hi:[0,1]
	v_exp_f32_e32 v108, v108
	v_exp_f32_e32 v109, v109
	v_pk_mul_f32 v[110:111], v[32:33], v[4:5] op_sel_hi:[0,1]
	v_exp_f32_e32 v110, v110
	v_exp_f32_e32 v111, v111
	v_pk_mul_f32 v[112:113], v[126:127], v[120:121] op_sel_hi:[0,1]
	v_pk_fma_f32 v[124:125], v[124:125], v[108:109], v[112:113]
	v_pk_mul_f32 v[108:109], v[126:127], v[122:123] op_sel_hi:[0,1]
	v_pk_fma_f32 v[104:105], v[104:105], v[110:111], v[108:109]
	s_nop 0
	s_waitcnt lgkmcnt(0)
	s_nop 0
	ds_read_b128 v[108:111], v160 offset:42896
	ds_read_b128 v[112:115], v160 offset:42912
	ds_read_b128 v[116:119], v160 offset:42928
	ds_read_b128 v[120:123], v160 offset:42944
	v_pk_mul_f32 v[126:127], v[34:35], v[14:15] op_sel_hi:[0,1]
	v_exp_f32_e32 v126, v126
	v_exp_f32_e32 v127, v127
	v_pk_mul_f32 v[140:141], v[34:35], v[16:17] op_sel_hi:[0,1]
	v_exp_f32_e32 v140, v140
	v_exp_f32_e32 v141, v141
	v_mul_f32_e32 v86, v34, v86
	v_pk_mul_f32 v[88:89], v[86:87], v[88:89] op_sel_hi:[0,1]
	v_pk_fma_f32 v[126:127], v[128:129], v[126:127], v[88:89]
	v_pk_mul_f32 v[88:89], v[86:87], v[90:91] op_sel_hi:[0,1]
	v_pk_fma_f32 v[128:129], v[130:131], v[140:141], v[88:89]
	v_pk_mul_f32 v[88:89], v[34:35], v[10:11] op_sel_hi:[0,1]
	v_exp_f32_e32 v88, v88
	v_exp_f32_e32 v89, v89
	v_pk_mul_f32 v[90:91], v[34:35], v[12:13] op_sel_hi:[0,1]
	v_exp_f32_e32 v90, v90
	v_exp_f32_e32 v91, v91
	v_pk_mul_f32 v[92:93], v[86:87], v[92:93] op_sel_hi:[0,1]
	v_pk_fma_f32 v[130:131], v[132:133], v[88:89], v[92:93]
	v_pk_mul_f32 v[88:89], v[86:87], v[94:95] op_sel_hi:[0,1]
	v_pk_fma_f32 v[132:133], v[134:135], v[90:91], v[88:89]
	v_pk_mul_f32 v[88:89], v[34:35], v[6:7] op_sel_hi:[0,1]
	v_exp_f32_e32 v88, v88
	v_exp_f32_e32 v89, v89
	v_pk_mul_f32 v[90:91], v[34:35], v[8:9] op_sel_hi:[0,1]
	v_exp_f32_e32 v90, v90
	v_exp_f32_e32 v91, v91
	v_pk_mul_f32 v[92:93], v[86:87], v[96:97] op_sel_hi:[0,1]
	v_pk_fma_f32 v[134:135], v[136:137], v[88:89], v[92:93]
	v_pk_mul_f32 v[88:89], v[86:87], v[98:99] op_sel_hi:[0,1]
	v_pk_fma_f32 v[136:137], v[138:139], v[90:91], v[88:89]
	v_pk_mul_f32 v[88:89], v[34:35], v[2:3] op_sel_hi:[0,1]
	v_pk_mul_f32 v[90:91], v[34:35], v[4:5] op_sel_hi:[0,1]
	v_exp_f32_e32 v88, v88
	v_exp_f32_e32 v89, v89
	v_exp_f32_e32 v90, v90
	v_exp_f32_e32 v91, v91
	v_pk_mul_f32 v[92:93], v[86:87], v[100:101] op_sel_hi:[0,1]
	v_pk_mul_f32 v[86:87], v[86:87], v[102:103] op_sel_hi:[0,1]
	v_pk_fma_f32 v[124:125], v[124:125], v[88:89], v[92:93]
	v_pk_fma_f32 v[102:103], v[104:105], v[90:91], v[86:87]
	s_nop 0
	s_waitcnt lgkmcnt(0)
	s_nop 0
	ds_read_b128 v[86:89], v160 offset:43104
	ds_read_b128 v[90:93], v160 offset:43120
	ds_read_b128 v[94:97], v160 offset:43136
	ds_read_b128 v[98:101], v160 offset:43152
	v_pk_mul_f32 v[138:139], v[36:37], v[14:15] op_sel_hi:[0,1]
	v_exp_f32_e32 v138, v138
	v_exp_f32_e32 v139, v139
	v_pk_mul_f32 v[140:141], v[36:37], v[16:17] op_sel_hi:[0,1]
	v_exp_f32_e32 v140, v140
	v_exp_f32_e32 v141, v141
	v_mul_f32_e32 v104, v36, v85
	v_pk_mul_f32 v[108:109], v[104:105], v[108:109] op_sel_hi:[0,1]
	v_pk_fma_f32 v[126:127], v[126:127], v[138:139], v[108:109]
	v_pk_mul_f32 v[108:109], v[104:105], v[110:111] op_sel_hi:[0,1]
	v_pk_fma_f32 v[128:129], v[128:129], v[140:141], v[108:109]
	v_pk_mul_f32 v[108:109], v[36:37], v[10:11] op_sel_hi:[0,1]
	v_exp_f32_e32 v108, v108
	v_exp_f32_e32 v109, v109
	v_pk_mul_f32 v[110:111], v[36:37], v[12:13] op_sel_hi:[0,1]
	v_exp_f32_e32 v110, v110
	v_exp_f32_e32 v111, v111
	v_pk_mul_f32 v[112:113], v[104:105], v[112:113] op_sel_hi:[0,1]
	v_pk_fma_f32 v[130:131], v[130:131], v[108:109], v[112:113]
	v_pk_mul_f32 v[108:109], v[104:105], v[114:115] op_sel_hi:[0,1]
	v_pk_fma_f32 v[132:133], v[132:133], v[110:111], v[108:109]
	v_pk_mul_f32 v[108:109], v[36:37], v[6:7] op_sel_hi:[0,1]
	v_exp_f32_e32 v108, v108
	v_exp_f32_e32 v109, v109
	v_pk_mul_f32 v[110:111], v[36:37], v[8:9] op_sel_hi:[0,1]
	v_exp_f32_e32 v110, v110
	v_exp_f32_e32 v111, v111
	v_pk_mul_f32 v[112:113], v[104:105], v[116:117] op_sel_hi:[0,1]
	v_pk_fma_f32 v[134:135], v[134:135], v[108:109], v[112:113]
	v_pk_mul_f32 v[108:109], v[104:105], v[118:119] op_sel_hi:[0,1]
	v_pk_fma_f32 v[136:137], v[136:137], v[110:111], v[108:109]
	v_pk_mul_f32 v[108:109], v[36:37], v[2:3] op_sel_hi:[0,1]
	v_pk_mul_f32 v[110:111], v[36:37], v[4:5] op_sel_hi:[0,1]
	v_exp_f32_e32 v108, v108
	v_exp_f32_e32 v109, v109
	v_exp_f32_e32 v110, v110
	v_exp_f32_e32 v111, v111
	v_pk_mul_f32 v[112:113], v[104:105], v[120:121] op_sel_hi:[0,1]
	v_pk_mul_f32 v[104:105], v[104:105], v[122:123] op_sel_hi:[0,1]
	v_pk_fma_f32 v[120:121], v[124:125], v[108:109], v[112:113]
	v_pk_fma_f32 v[122:123], v[102:103], v[110:111], v[104:105]
	s_nop 0
	s_waitcnt lgkmcnt(0)
	s_nop 0
	ds_read_b128 v[102:105], v160 offset:43312
	ds_read_b128 v[108:111], v160 offset:43328
	ds_read_b128 v[112:115], v160 offset:43344
	ds_read_b128 v[116:119], v160 offset:43360
	v_pk_mul_f32 v[124:125], v[38:39], v[14:15] op_sel_hi:[0,1]
	v_exp_f32_e32 v124, v124
	v_exp_f32_e32 v125, v125
	v_pk_mul_f32 v[138:139], v[38:39], v[16:17] op_sel_hi:[0,1]
	v_exp_f32_e32 v138, v138
	v_exp_f32_e32 v139, v139
	v_mul_f32_e32 v84, v38, v84
	v_pk_mul_f32 v[86:87], v[84:85], v[86:87] op_sel_hi:[0,1]
	v_pk_fma_f32 v[124:125], v[126:127], v[124:125], v[86:87]
	v_pk_mul_f32 v[86:87], v[84:85], v[88:89] op_sel_hi:[0,1]
	v_pk_fma_f32 v[126:127], v[128:129], v[138:139], v[86:87]
	v_pk_mul_f32 v[86:87], v[38:39], v[10:11] op_sel_hi:[0,1]
	v_exp_f32_e32 v86, v86
	v_exp_f32_e32 v87, v87
	v_pk_mul_f32 v[88:89], v[38:39], v[12:13] op_sel_hi:[0,1]
	v_exp_f32_e32 v88, v88
	v_exp_f32_e32 v89, v89
	v_pk_mul_f32 v[90:91], v[84:85], v[90:91] op_sel_hi:[0,1]
	v_pk_fma_f32 v[128:129], v[130:131], v[86:87], v[90:91]
	v_pk_mul_f32 v[86:87], v[84:85], v[92:93] op_sel_hi:[0,1]
	v_pk_fma_f32 v[130:131], v[132:133], v[88:89], v[86:87]
	v_pk_mul_f32 v[86:87], v[38:39], v[6:7] op_sel_hi:[0,1]
	v_exp_f32_e32 v86, v86
	v_exp_f32_e32 v87, v87
	v_pk_mul_f32 v[88:89], v[38:39], v[8:9] op_sel_hi:[0,1]
	v_exp_f32_e32 v88, v88
	v_exp_f32_e32 v89, v89
	v_pk_mul_f32 v[90:91], v[84:85], v[94:95] op_sel_hi:[0,1]
	v_pk_fma_f32 v[132:133], v[134:135], v[86:87], v[90:91]
	v_pk_mul_f32 v[86:87], v[84:85], v[96:97] op_sel_hi:[0,1]
	v_pk_fma_f32 v[134:135], v[136:137], v[88:89], v[86:87]
	v_pk_mul_f32 v[86:87], v[38:39], v[2:3] op_sel_hi:[0,1]
	v_pk_mul_f32 v[88:89], v[38:39], v[4:5] op_sel_hi:[0,1]
	v_exp_f32_e32 v86, v86
	v_exp_f32_e32 v87, v87
	v_exp_f32_e32 v88, v88
	v_exp_f32_e32 v89, v89
	v_pk_mul_f32 v[90:91], v[84:85], v[98:99] op_sel_hi:[0,1]
	v_pk_mul_f32 v[84:85], v[84:85], v[100:101] op_sel_hi:[0,1]
	v_pk_fma_f32 v[120:121], v[120:121], v[86:87], v[90:91]
	v_pk_fma_f32 v[100:101], v[122:123], v[88:89], v[84:85]
	s_nop 0
	s_waitcnt lgkmcnt(0)
	s_nop 0
	ds_read_b128 v[84:87], v160 offset:43520
	ds_read_b128 v[88:91], v160 offset:43536
	ds_read_b128 v[92:95], v160 offset:43552
	ds_read_b128 v[96:99], v160 offset:43568
	v_pk_mul_f32 v[136:137], v[40:41], v[14:15] op_sel_hi:[0,1]
	v_exp_f32_e32 v136, v136
	v_exp_f32_e32 v137, v137
	v_pk_mul_f32 v[138:139], v[40:41], v[16:17] op_sel_hi:[0,1]
	v_exp_f32_e32 v138, v138
	v_exp_f32_e32 v139, v139
	v_mul_f32_e32 v122, v40, v83
	v_pk_mul_f32 v[102:103], v[122:123], v[102:103] op_sel_hi:[0,1]
	v_pk_fma_f32 v[124:125], v[124:125], v[136:137], v[102:103]
	v_pk_mul_f32 v[102:103], v[122:123], v[104:105] op_sel_hi:[0,1]
	v_pk_fma_f32 v[104:105], v[126:127], v[138:139], v[102:103]
	v_pk_mul_f32 v[102:103], v[40:41], v[10:11] op_sel_hi:[0,1]
	v_exp_f32_e32 v102, v102
	v_exp_f32_e32 v103, v103
	v_pk_mul_f32 v[126:127], v[40:41], v[12:13] op_sel_hi:[0,1]
	v_exp_f32_e32 v126, v126
	v_exp_f32_e32 v127, v127
	v_pk_mul_f32 v[108:109], v[122:123], v[108:109] op_sel_hi:[0,1]
	v_pk_fma_f32 v[128:129], v[128:129], v[102:103], v[108:109]
	v_pk_mul_f32 v[102:103], v[122:123], v[110:111] op_sel_hi:[0,1]
	v_pk_fma_f32 v[126:127], v[130:131], v[126:127], v[102:103]
	v_pk_mul_f32 v[102:103], v[40:41], v[6:7] op_sel_hi:[0,1]
	v_exp_f32_e32 v102, v102
	v_exp_f32_e32 v103, v103
	v_pk_mul_f32 v[108:109], v[40:41], v[8:9] op_sel_hi:[0,1]
	v_exp_f32_e32 v108, v108
	v_exp_f32_e32 v109, v109
	v_pk_mul_f32 v[110:111], v[122:123], v[112:113] op_sel_hi:[0,1]
	v_pk_fma_f32 v[130:131], v[132:133], v[102:103], v[110:111]
	v_pk_mul_f32 v[102:103], v[122:123], v[114:115] op_sel_hi:[0,1]
	v_pk_fma_f32 v[132:133], v[134:135], v[108:109], v[102:103]
	v_pk_mul_f32 v[102:103], v[40:41], v[2:3] op_sel_hi:[0,1]
	v_exp_f32_e32 v102, v102
	v_exp_f32_e32 v103, v103
	v_pk_mul_f32 v[108:109], v[40:41], v[4:5] op_sel_hi:[0,1]
	v_exp_f32_e32 v108, v108
	v_exp_f32_e32 v109, v109
	v_pk_mul_f32 v[110:111], v[122:123], v[116:117] op_sel_hi:[0,1]
	v_pk_fma_f32 v[120:121], v[120:121], v[102:103], v[110:111]
	v_pk_mul_f32 v[102:103], v[122:123], v[118:119] op_sel_hi:[0,1]
	v_pk_fma_f32 v[122:123], v[100:101], v[108:109], v[102:103]
	s_nop 0
	s_waitcnt lgkmcnt(0)
	s_nop 0
	ds_read_b128 v[100:103], v160 offset:43728
	ds_read_b128 v[108:111], v160 offset:43744
	ds_read_b128 v[112:115], v160 offset:43760
	ds_read_b128 v[116:119], v160 offset:43776
	v_pk_mul_f32 v[134:135], v[42:43], v[14:15] op_sel_hi:[0,1]
	v_exp_f32_e32 v134, v134
	v_exp_f32_e32 v135, v135
	v_pk_mul_f32 v[136:137], v[42:43], v[16:17] op_sel_hi:[0,1]
	v_exp_f32_e32 v136, v136
	v_exp_f32_e32 v137, v137
	v_mul_f32_e32 v82, v42, v82
	v_pk_mul_f32 v[84:85], v[82:83], v[84:85] op_sel_hi:[0,1]
	v_pk_fma_f32 v[124:125], v[124:125], v[134:135], v[84:85]
	v_pk_mul_f32 v[84:85], v[82:83], v[86:87] op_sel_hi:[0,1]
	v_pk_fma_f32 v[104:105], v[104:105], v[136:137], v[84:85]
	v_pk_mul_f32 v[84:85], v[42:43], v[10:11] op_sel_hi:[0,1]
	v_exp_f32_e32 v84, v84
	v_exp_f32_e32 v85, v85
	v_pk_mul_f32 v[86:87], v[42:43], v[12:13] op_sel_hi:[0,1]
	v_exp_f32_e32 v86, v86
	v_exp_f32_e32 v87, v87
	v_pk_mul_f32 v[88:89], v[82:83], v[88:89] op_sel_hi:[0,1]
	v_pk_fma_f32 v[128:129], v[128:129], v[84:85], v[88:89]
	v_pk_mul_f32 v[84:85], v[82:83], v[90:91] op_sel_hi:[0,1]
	v_pk_fma_f32 v[126:127], v[126:127], v[86:87], v[84:85]
	v_pk_mul_f32 v[84:85], v[42:43], v[6:7] op_sel_hi:[0,1]
	v_exp_f32_e32 v84, v84
	v_exp_f32_e32 v85, v85
	v_pk_mul_f32 v[86:87], v[42:43], v[8:9] op_sel_hi:[0,1]
	v_exp_f32_e32 v86, v86
	v_exp_f32_e32 v87, v87
	v_pk_mul_f32 v[88:89], v[82:83], v[92:93] op_sel_hi:[0,1]
	v_pk_fma_f32 v[130:131], v[130:131], v[84:85], v[88:89]
	v_pk_mul_f32 v[84:85], v[82:83], v[94:95] op_sel_hi:[0,1]
	v_pk_fma_f32 v[132:133], v[132:133], v[86:87], v[84:85]
	v_pk_mul_f32 v[84:85], v[42:43], v[2:3] op_sel_hi:[0,1]
	v_pk_mul_f32 v[86:87], v[42:43], v[4:5] op_sel_hi:[0,1]
	v_exp_f32_e32 v84, v84
	v_exp_f32_e32 v85, v85
	v_exp_f32_e32 v86, v86
	v_exp_f32_e32 v87, v87
	v_pk_mul_f32 v[88:89], v[82:83], v[96:97] op_sel_hi:[0,1]
	v_pk_mul_f32 v[82:83], v[82:83], v[98:99] op_sel_hi:[0,1]
	v_pk_fma_f32 v[120:121], v[120:121], v[84:85], v[88:89]
	v_pk_fma_f32 v[98:99], v[122:123], v[86:87], v[82:83]
	s_nop 0
	s_waitcnt lgkmcnt(0)
	s_nop 0
	ds_read_b128 v[82:85], v160 offset:43936
	ds_read_b128 v[86:89], v160 offset:43952
	ds_read_b128 v[90:93], v160 offset:43968
	ds_read_b128 v[94:97], v160 offset:43984
	v_pk_mul_f32 v[134:135], v[44:45], v[14:15] op_sel_hi:[0,1]
	v_exp_f32_e32 v134, v134
	v_exp_f32_e32 v135, v135
	v_pk_mul_f32 v[136:137], v[44:45], v[16:17] op_sel_hi:[0,1]
	v_exp_f32_e32 v136, v136
	v_exp_f32_e32 v137, v137
	v_mul_f32_e32 v122, v44, v81
	v_pk_mul_f32 v[100:101], v[122:123], v[100:101] op_sel_hi:[0,1]
	v_pk_fma_f32 v[124:125], v[124:125], v[134:135], v[100:101]
	v_pk_mul_f32 v[100:101], v[122:123], v[102:103] op_sel_hi:[0,1]
	v_pk_fma_f32 v[134:135], v[104:105], v[136:137], v[100:101]
	v_pk_mul_f32 v[100:101], v[44:45], v[10:11] op_sel_hi:[0,1]
	v_exp_f32_e32 v100, v100
	v_exp_f32_e32 v101, v101
	v_pk_mul_f32 v[102:103], v[44:45], v[12:13] op_sel_hi:[0,1]
	v_exp_f32_e32 v102, v102
	v_exp_f32_e32 v103, v103
	v_pk_mul_f32 v[104:105], v[122:123], v[108:109] op_sel_hi:[0,1]
	v_pk_fma_f32 v[128:129], v[128:129], v[100:101], v[104:105]
	v_pk_mul_f32 v[100:101], v[122:123], v[110:111] op_sel_hi:[0,1]
	v_pk_fma_f32 v[126:127], v[126:127], v[102:103], v[100:101]
	v_pk_mul_f32 v[100:101], v[44:45], v[6:7] op_sel_hi:[0,1]
	v_exp_f32_e32 v100, v100
	v_exp_f32_e32 v101, v101
	v_pk_mul_f32 v[102:103], v[44:45], v[8:9] op_sel_hi:[0,1]
	v_exp_f32_e32 v102, v102
	v_exp_f32_e32 v103, v103
	v_pk_mul_f32 v[104:105], v[122:123], v[112:113] op_sel_hi:[0,1]
	v_pk_fma_f32 v[130:131], v[130:131], v[100:101], v[104:105]
	v_pk_mul_f32 v[100:101], v[122:123], v[114:115] op_sel_hi:[0,1]
	v_pk_fma_f32 v[132:133], v[132:133], v[102:103], v[100:101]
	v_pk_mul_f32 v[100:101], v[44:45], v[2:3] op_sel_hi:[0,1]
	v_exp_f32_e32 v100, v100
	v_exp_f32_e32 v101, v101
	v_pk_mul_f32 v[102:103], v[44:45], v[4:5] op_sel_hi:[0,1]
	v_exp_f32_e32 v102, v102
	v_exp_f32_e32 v103, v103
	v_pk_mul_f32 v[104:105], v[122:123], v[116:117] op_sel_hi:[0,1]
	v_pk_fma_f32 v[116:117], v[120:121], v[100:101], v[104:105]
	v_pk_mul_f32 v[100:101], v[122:123], v[118:119] op_sel_hi:[0,1]
	v_pk_fma_f32 v[118:119], v[98:99], v[102:103], v[100:101]
	s_nop 0
	s_waitcnt lgkmcnt(0)
	s_nop 0
	ds_read_b128 v[98:101], v160 offset:44144
	ds_read_b128 v[102:105], v160 offset:44160
	ds_read_b128 v[108:111], v160 offset:44176
	ds_read_b128 v[112:115], v160 offset:44192
	v_pk_mul_f32 v[122:123], v[46:47], v[14:15] op_sel_hi:[0,1]
	v_exp_f32_e32 v122, v122
	v_exp_f32_e32 v123, v123
	v_pk_mul_f32 v[136:137], v[46:47], v[16:17] op_sel_hi:[0,1]
	v_exp_f32_e32 v136, v136
	v_exp_f32_e32 v137, v137
	v_mul_f32_e32 v120, v46, v79
	v_pk_mul_f32 v[82:83], v[120:121], v[82:83] op_sel_hi:[0,1]
	v_pk_fma_f32 v[122:123], v[124:125], v[122:123], v[82:83]
	v_pk_mul_f32 v[82:83], v[120:121], v[84:85] op_sel_hi:[0,1]
	v_pk_fma_f32 v[124:125], v[134:135], v[136:137], v[82:83]
	v_pk_mul_f32 v[82:83], v[46:47], v[10:11] op_sel_hi:[0,1]
	v_exp_f32_e32 v82, v82
	v_exp_f32_e32 v83, v83
	v_pk_mul_f32 v[84:85], v[46:47], v[12:13] op_sel_hi:[0,1]
	v_exp_f32_e32 v84, v84
	v_exp_f32_e32 v85, v85
	v_pk_mul_f32 v[86:87], v[120:121], v[86:87] op_sel_hi:[0,1]
	v_pk_fma_f32 v[128:129], v[128:129], v[82:83], v[86:87]
	v_pk_mul_f32 v[82:83], v[120:121], v[88:89] op_sel_hi:[0,1]
	v_pk_fma_f32 v[126:127], v[126:127], v[84:85], v[82:83]
	v_pk_mul_f32 v[82:83], v[46:47], v[6:7] op_sel_hi:[0,1]
	v_exp_f32_e32 v82, v82
	v_exp_f32_e32 v83, v83
	v_pk_mul_f32 v[84:85], v[46:47], v[8:9] op_sel_hi:[0,1]
	v_exp_f32_e32 v84, v84
	v_exp_f32_e32 v85, v85
	v_pk_mul_f32 v[86:87], v[120:121], v[90:91] op_sel_hi:[0,1]
	v_pk_fma_f32 v[130:131], v[130:131], v[82:83], v[86:87]
	v_pk_mul_f32 v[82:83], v[120:121], v[92:93] op_sel_hi:[0,1]
	v_pk_fma_f32 v[132:133], v[132:133], v[84:85], v[82:83]
	v_pk_mul_f32 v[82:83], v[46:47], v[2:3] op_sel_hi:[0,1]
	v_exp_f32_e32 v82, v82
	v_exp_f32_e32 v83, v83
	v_pk_mul_f32 v[84:85], v[46:47], v[4:5] op_sel_hi:[0,1]
	v_exp_f32_e32 v84, v84
	v_exp_f32_e32 v85, v85
	v_pk_mul_f32 v[86:87], v[120:121], v[94:95] op_sel_hi:[0,1]
	v_pk_fma_f32 v[116:117], v[116:117], v[82:83], v[86:87]
	v_pk_mul_f32 v[82:83], v[120:121], v[96:97] op_sel_hi:[0,1]
	v_pk_fma_f32 v[118:119], v[118:119], v[84:85], v[82:83]
	s_nop 0
	s_waitcnt lgkmcnt(0)
	s_nop 0
	ds_read_b128 v[82:85], v160 offset:44352
	ds_read_b128 v[86:89], v160 offset:44368
	ds_read_b128 v[90:93], v160 offset:44384
	ds_read_b128 v[94:97], v160 offset:44400
	v_pk_mul_f32 v[134:135], v[48:49], v[14:15] op_sel_hi:[0,1]
	v_exp_f32_e32 v134, v134
	v_exp_f32_e32 v135, v135
	v_pk_mul_f32 v[136:137], v[48:49], v[16:17] op_sel_hi:[0,1]
	v_exp_f32_e32 v136, v136
	v_exp_f32_e32 v137, v137
	v_mul_f32_e32 v120, v48, v77
	v_pk_mul_f32 v[98:99], v[120:121], v[98:99] op_sel_hi:[0,1]
	v_pk_fma_f32 v[122:123], v[122:123], v[134:135], v[98:99]
	v_pk_mul_f32 v[98:99], v[120:121], v[100:101] op_sel_hi:[0,1]
	v_pk_fma_f32 v[124:125], v[124:125], v[136:137], v[98:99]
	v_pk_mul_f32 v[98:99], v[48:49], v[10:11] op_sel_hi:[0,1]
	v_exp_f32_e32 v98, v98
	v_exp_f32_e32 v99, v99
	v_pk_mul_f32 v[100:101], v[48:49], v[12:13] op_sel_hi:[0,1]
	v_exp_f32_e32 v100, v100
	v_exp_f32_e32 v101, v101
	v_pk_mul_f32 v[102:103], v[120:121], v[102:103] op_sel_hi:[0,1]
	v_pk_fma_f32 v[128:129], v[128:129], v[98:99], v[102:103]
	v_pk_mul_f32 v[98:99], v[120:121], v[104:105] op_sel_hi:[0,1]
	v_pk_fma_f32 v[126:127], v[126:127], v[100:101], v[98:99]
	v_pk_mul_f32 v[98:99], v[48:49], v[6:7] op_sel_hi:[0,1]
	v_exp_f32_e32 v98, v98
	v_exp_f32_e32 v99, v99
	v_pk_mul_f32 v[100:101], v[48:49], v[8:9] op_sel_hi:[0,1]
	v_exp_f32_e32 v100, v100
	v_exp_f32_e32 v101, v101
	v_pk_mul_f32 v[102:103], v[120:121], v[108:109] op_sel_hi:[0,1]
	v_pk_fma_f32 v[130:131], v[130:131], v[98:99], v[102:103]
	v_pk_mul_f32 v[98:99], v[120:121], v[110:111] op_sel_hi:[0,1]
	v_pk_fma_f32 v[132:133], v[132:133], v[100:101], v[98:99]
	v_pk_mul_f32 v[98:99], v[48:49], v[2:3] op_sel_hi:[0,1]
	v_exp_f32_e32 v98, v98
	v_exp_f32_e32 v99, v99
	v_pk_mul_f32 v[100:101], v[48:49], v[4:5] op_sel_hi:[0,1]
	v_exp_f32_e32 v100, v100
	v_exp_f32_e32 v101, v101
	v_pk_mul_f32 v[102:103], v[120:121], v[112:113] op_sel_hi:[0,1]
	v_pk_fma_f32 v[116:117], v[116:117], v[98:99], v[102:103]
	v_pk_mul_f32 v[98:99], v[120:121], v[114:115] op_sel_hi:[0,1]
	v_pk_fma_f32 v[118:119], v[118:119], v[100:101], v[98:99]
	s_nop 0
	s_waitcnt lgkmcnt(0)
	s_nop 0
	ds_read_b128 v[98:101], v160 offset:44560
	ds_read_b128 v[102:105], v160 offset:44576
	ds_read_b128 v[108:111], v160 offset:44592
	ds_read_b128 v[112:115], v160 offset:44608
	v_pk_mul_f32 v[134:135], v[50:51], v[14:15] op_sel_hi:[0,1]
	v_exp_f32_e32 v134, v134
	v_exp_f32_e32 v135, v135
	v_pk_mul_f32 v[136:137], v[50:51], v[16:17] op_sel_hi:[0,1]
	v_exp_f32_e32 v136, v136
	v_exp_f32_e32 v137, v137
	v_mul_f32_e32 v120, v50, v75
	v_pk_mul_f32 v[82:83], v[120:121], v[82:83] op_sel_hi:[0,1]
	v_pk_fma_f32 v[122:123], v[122:123], v[134:135], v[82:83]
	v_pk_mul_f32 v[82:83], v[120:121], v[84:85] op_sel_hi:[0,1]
	v_pk_fma_f32 v[124:125], v[124:125], v[136:137], v[82:83]
	v_pk_mul_f32 v[82:83], v[50:51], v[10:11] op_sel_hi:[0,1]
	v_exp_f32_e32 v82, v82
	v_exp_f32_e32 v83, v83
	v_pk_mul_f32 v[84:85], v[50:51], v[12:13] op_sel_hi:[0,1]
	v_exp_f32_e32 v84, v84
	v_exp_f32_e32 v85, v85
	v_pk_mul_f32 v[86:87], v[120:121], v[86:87] op_sel_hi:[0,1]
	v_pk_fma_f32 v[128:129], v[128:129], v[82:83], v[86:87]
	v_pk_mul_f32 v[82:83], v[120:121], v[88:89] op_sel_hi:[0,1]
	v_pk_fma_f32 v[126:127], v[126:127], v[84:85], v[82:83]
	v_pk_mul_f32 v[82:83], v[50:51], v[6:7] op_sel_hi:[0,1]
	v_exp_f32_e32 v82, v82
	v_exp_f32_e32 v83, v83
	v_pk_mul_f32 v[84:85], v[50:51], v[8:9] op_sel_hi:[0,1]
	v_exp_f32_e32 v84, v84
	v_exp_f32_e32 v85, v85
	v_pk_mul_f32 v[86:87], v[120:121], v[90:91] op_sel_hi:[0,1]
	v_pk_fma_f32 v[130:131], v[130:131], v[82:83], v[86:87]
	v_pk_mul_f32 v[82:83], v[120:121], v[92:93] op_sel_hi:[0,1]
	v_pk_fma_f32 v[132:133], v[132:133], v[84:85], v[82:83]
	v_pk_mul_f32 v[82:83], v[50:51], v[2:3] op_sel_hi:[0,1]
	v_exp_f32_e32 v82, v82
	v_exp_f32_e32 v83, v83
	v_pk_mul_f32 v[84:85], v[50:51], v[4:5] op_sel_hi:[0,1]
	v_exp_f32_e32 v84, v84
	v_exp_f32_e32 v85, v85
	v_pk_mul_f32 v[86:87], v[120:121], v[94:95] op_sel_hi:[0,1]
	v_pk_fma_f32 v[116:117], v[116:117], v[82:83], v[86:87]
	v_pk_mul_f32 v[82:83], v[120:121], v[96:97] op_sel_hi:[0,1]
	v_pk_fma_f32 v[118:119], v[118:119], v[84:85], v[82:83]
	s_nop 0
	s_waitcnt lgkmcnt(0)
	s_nop 0
	ds_read_b128 v[82:85], v160 offset:44768
	ds_read_b128 v[86:89], v160 offset:44784
	ds_read_b128 v[90:93], v160 offset:44800
	ds_read_b128 v[94:97], v160 offset:44816
	v_pk_mul_f32 v[134:135], v[52:53], v[14:15] op_sel_hi:[0,1]
	v_exp_f32_e32 v134, v134
	v_exp_f32_e32 v135, v135
	v_pk_mul_f32 v[136:137], v[52:53], v[16:17] op_sel_hi:[0,1]
	v_exp_f32_e32 v136, v136
	v_exp_f32_e32 v137, v137
	v_mul_f32_e32 v120, v52, v73
	v_pk_mul_f32 v[98:99], v[120:121], v[98:99] op_sel_hi:[0,1]
	v_pk_fma_f32 v[122:123], v[122:123], v[134:135], v[98:99]
	v_pk_mul_f32 v[98:99], v[120:121], v[100:101] op_sel_hi:[0,1]
	v_pk_fma_f32 v[124:125], v[124:125], v[136:137], v[98:99]
	v_pk_mul_f32 v[98:99], v[52:53], v[10:11] op_sel_hi:[0,1]
	v_exp_f32_e32 v98, v98
	v_exp_f32_e32 v99, v99
	v_pk_mul_f32 v[100:101], v[52:53], v[12:13] op_sel_hi:[0,1]
	v_exp_f32_e32 v100, v100
	v_exp_f32_e32 v101, v101
	v_pk_mul_f32 v[102:103], v[120:121], v[102:103] op_sel_hi:[0,1]
	v_pk_fma_f32 v[128:129], v[128:129], v[98:99], v[102:103]
	v_pk_mul_f32 v[98:99], v[120:121], v[104:105] op_sel_hi:[0,1]
	v_pk_fma_f32 v[126:127], v[126:127], v[100:101], v[98:99]
	v_pk_mul_f32 v[98:99], v[52:53], v[6:7] op_sel_hi:[0,1]
	v_exp_f32_e32 v98, v98
	v_exp_f32_e32 v99, v99
	v_pk_mul_f32 v[100:101], v[52:53], v[8:9] op_sel_hi:[0,1]
	v_exp_f32_e32 v100, v100
	v_exp_f32_e32 v101, v101
	v_pk_mul_f32 v[102:103], v[120:121], v[108:109] op_sel_hi:[0,1]
	v_pk_fma_f32 v[130:131], v[130:131], v[98:99], v[102:103]
	v_pk_mul_f32 v[98:99], v[120:121], v[110:111] op_sel_hi:[0,1]
	v_pk_fma_f32 v[132:133], v[132:133], v[100:101], v[98:99]
	v_pk_mul_f32 v[98:99], v[52:53], v[2:3] op_sel_hi:[0,1]
	v_exp_f32_e32 v98, v98
	v_exp_f32_e32 v99, v99
	v_pk_mul_f32 v[100:101], v[52:53], v[4:5] op_sel_hi:[0,1]
	v_exp_f32_e32 v100, v100
	v_exp_f32_e32 v101, v101
	v_pk_mul_f32 v[102:103], v[120:121], v[112:113] op_sel_hi:[0,1]
	v_pk_fma_f32 v[116:117], v[116:117], v[98:99], v[102:103]
	v_pk_mul_f32 v[98:99], v[120:121], v[114:115] op_sel_hi:[0,1]
	v_pk_fma_f32 v[118:119], v[118:119], v[100:101], v[98:99]
	s_nop 0
	s_waitcnt lgkmcnt(0)
	s_nop 0
	ds_read_b128 v[98:101], v160 offset:44976
	ds_read_b128 v[102:105], v160 offset:44992
	ds_read_b128 v[108:111], v160 offset:45008
	ds_read_b128 v[112:115], v160 offset:45024
	v_pk_mul_f32 v[134:135], v[54:55], v[14:15] op_sel_hi:[0,1]
	v_exp_f32_e32 v134, v134
	v_exp_f32_e32 v135, v135
	v_pk_mul_f32 v[136:137], v[54:55], v[16:17] op_sel_hi:[0,1]
	v_exp_f32_e32 v136, v136
	v_exp_f32_e32 v137, v137
	v_mul_f32_e32 v120, v54, v71
	v_pk_mul_f32 v[82:83], v[120:121], v[82:83] op_sel_hi:[0,1]
	v_pk_fma_f32 v[122:123], v[122:123], v[134:135], v[82:83]
	v_pk_mul_f32 v[82:83], v[120:121], v[84:85] op_sel_hi:[0,1]
	v_pk_fma_f32 v[124:125], v[124:125], v[136:137], v[82:83]
	v_pk_mul_f32 v[82:83], v[54:55], v[10:11] op_sel_hi:[0,1]
	v_exp_f32_e32 v82, v82
	v_exp_f32_e32 v83, v83
	v_pk_mul_f32 v[84:85], v[54:55], v[12:13] op_sel_hi:[0,1]
	v_exp_f32_e32 v84, v84
	v_exp_f32_e32 v85, v85
	v_pk_mul_f32 v[86:87], v[120:121], v[86:87] op_sel_hi:[0,1]
	v_pk_fma_f32 v[128:129], v[128:129], v[82:83], v[86:87]
	v_pk_mul_f32 v[82:83], v[120:121], v[88:89] op_sel_hi:[0,1]
	v_pk_fma_f32 v[126:127], v[126:127], v[84:85], v[82:83]
	v_pk_mul_f32 v[82:83], v[54:55], v[6:7] op_sel_hi:[0,1]
	v_exp_f32_e32 v82, v82
	v_exp_f32_e32 v83, v83
	v_pk_mul_f32 v[84:85], v[54:55], v[8:9] op_sel_hi:[0,1]
	v_exp_f32_e32 v84, v84
	v_exp_f32_e32 v85, v85
	v_pk_mul_f32 v[86:87], v[120:121], v[90:91] op_sel_hi:[0,1]
	v_pk_fma_f32 v[130:131], v[130:131], v[82:83], v[86:87]
	v_pk_mul_f32 v[82:83], v[120:121], v[92:93] op_sel_hi:[0,1]
	v_pk_fma_f32 v[132:133], v[132:133], v[84:85], v[82:83]
	v_pk_mul_f32 v[82:83], v[54:55], v[2:3] op_sel_hi:[0,1]
	v_exp_f32_e32 v82, v82
	v_exp_f32_e32 v83, v83
	v_pk_mul_f32 v[84:85], v[54:55], v[4:5] op_sel_hi:[0,1]
	v_exp_f32_e32 v84, v84
	v_exp_f32_e32 v85, v85
	v_pk_mul_f32 v[86:87], v[120:121], v[94:95] op_sel_hi:[0,1]
	v_pk_fma_f32 v[116:117], v[116:117], v[82:83], v[86:87]
	v_pk_mul_f32 v[82:83], v[120:121], v[96:97] op_sel_hi:[0,1]
	v_pk_fma_f32 v[118:119], v[118:119], v[84:85], v[82:83]
	s_nop 0
	s_waitcnt lgkmcnt(0)
	s_nop 0
	ds_read_b128 v[82:85], v160 offset:45184
	ds_read_b128 v[86:89], v160 offset:45200
	ds_read_b128 v[90:93], v160 offset:45216
	ds_read_b128 v[94:97], v160 offset:45232
	v_pk_mul_f32 v[134:135], v[56:57], v[14:15] op_sel_hi:[0,1]
	v_exp_f32_e32 v134, v134
	v_exp_f32_e32 v135, v135
	v_pk_mul_f32 v[136:137], v[56:57], v[16:17] op_sel_hi:[0,1]
	v_exp_f32_e32 v136, v136
	v_exp_f32_e32 v137, v137
	v_mul_f32_e32 v120, v56, v69
	v_pk_mul_f32 v[98:99], v[120:121], v[98:99] op_sel_hi:[0,1]
	v_pk_fma_f32 v[122:123], v[122:123], v[134:135], v[98:99]
	v_pk_mul_f32 v[98:99], v[120:121], v[100:101] op_sel_hi:[0,1]
	v_pk_fma_f32 v[124:125], v[124:125], v[136:137], v[98:99]
	v_pk_mul_f32 v[98:99], v[56:57], v[10:11] op_sel_hi:[0,1]
	v_exp_f32_e32 v98, v98
	v_exp_f32_e32 v99, v99
	v_pk_mul_f32 v[100:101], v[56:57], v[12:13] op_sel_hi:[0,1]
	v_exp_f32_e32 v100, v100
	v_exp_f32_e32 v101, v101
	v_pk_mul_f32 v[102:103], v[120:121], v[102:103] op_sel_hi:[0,1]
	v_pk_fma_f32 v[128:129], v[128:129], v[98:99], v[102:103]
	v_pk_mul_f32 v[98:99], v[120:121], v[104:105] op_sel_hi:[0,1]
	v_pk_fma_f32 v[126:127], v[126:127], v[100:101], v[98:99]
	v_pk_mul_f32 v[98:99], v[56:57], v[6:7] op_sel_hi:[0,1]
	v_exp_f32_e32 v98, v98
	v_exp_f32_e32 v99, v99
	v_pk_mul_f32 v[100:101], v[56:57], v[8:9] op_sel_hi:[0,1]
	v_exp_f32_e32 v100, v100
	v_exp_f32_e32 v101, v101
	v_pk_mul_f32 v[102:103], v[120:121], v[108:109] op_sel_hi:[0,1]
	v_pk_fma_f32 v[130:131], v[130:131], v[98:99], v[102:103]
	v_pk_mul_f32 v[98:99], v[120:121], v[110:111] op_sel_hi:[0,1]
	v_pk_fma_f32 v[132:133], v[132:133], v[100:101], v[98:99]
	v_pk_mul_f32 v[98:99], v[56:57], v[2:3] op_sel_hi:[0,1]
	v_exp_f32_e32 v98, v98
	v_exp_f32_e32 v99, v99
	v_pk_mul_f32 v[100:101], v[56:57], v[4:5] op_sel_hi:[0,1]
	v_exp_f32_e32 v100, v100
	v_exp_f32_e32 v101, v101
	v_pk_mul_f32 v[102:103], v[120:121], v[112:113] op_sel_hi:[0,1]
	v_pk_fma_f32 v[116:117], v[116:117], v[98:99], v[102:103]
	v_pk_mul_f32 v[98:99], v[120:121], v[114:115] op_sel_hi:[0,1]
	v_pk_fma_f32 v[118:119], v[118:119], v[100:101], v[98:99]
	s_nop 0
	s_waitcnt lgkmcnt(0)
	s_nop 0
	ds_read_b128 v[98:101], v160 offset:45392
	ds_read_b128 v[102:105], v160 offset:45408
	ds_read_b128 v[108:111], v160 offset:45424
	ds_read_b128 v[112:115], v160 offset:45440
	v_pk_mul_f32 v[134:135], v[58:59], v[14:15] op_sel_hi:[0,1]
	v_exp_f32_e32 v134, v134
	v_exp_f32_e32 v135, v135
	v_pk_mul_f32 v[136:137], v[58:59], v[16:17] op_sel_hi:[0,1]
	v_exp_f32_e32 v136, v136
	v_exp_f32_e32 v137, v137
	v_mul_f32_e32 v120, v58, v67
	v_pk_mul_f32 v[82:83], v[120:121], v[82:83] op_sel_hi:[0,1]
	v_pk_fma_f32 v[122:123], v[122:123], v[134:135], v[82:83]
	v_pk_mul_f32 v[82:83], v[120:121], v[84:85] op_sel_hi:[0,1]
	v_pk_fma_f32 v[124:125], v[124:125], v[136:137], v[82:83]
	v_pk_mul_f32 v[82:83], v[58:59], v[10:11] op_sel_hi:[0,1]
	v_exp_f32_e32 v82, v82
	v_exp_f32_e32 v83, v83
	v_pk_mul_f32 v[84:85], v[58:59], v[12:13] op_sel_hi:[0,1]
	v_exp_f32_e32 v84, v84
	v_exp_f32_e32 v85, v85
	v_pk_mul_f32 v[86:87], v[120:121], v[86:87] op_sel_hi:[0,1]
	v_pk_fma_f32 v[128:129], v[128:129], v[82:83], v[86:87]
	v_pk_mul_f32 v[82:83], v[120:121], v[88:89] op_sel_hi:[0,1]
	v_pk_fma_f32 v[126:127], v[126:127], v[84:85], v[82:83]
	v_pk_mul_f32 v[82:83], v[58:59], v[6:7] op_sel_hi:[0,1]
	v_exp_f32_e32 v82, v82
	v_exp_f32_e32 v83, v83
	v_pk_mul_f32 v[84:85], v[58:59], v[8:9] op_sel_hi:[0,1]
	v_exp_f32_e32 v84, v84
	v_exp_f32_e32 v85, v85
	v_pk_mul_f32 v[86:87], v[120:121], v[90:91] op_sel_hi:[0,1]
	v_pk_fma_f32 v[130:131], v[130:131], v[82:83], v[86:87]
	v_pk_mul_f32 v[82:83], v[120:121], v[92:93] op_sel_hi:[0,1]
	v_pk_fma_f32 v[132:133], v[132:133], v[84:85], v[82:83]
	v_pk_mul_f32 v[82:83], v[58:59], v[2:3] op_sel_hi:[0,1]
	v_exp_f32_e32 v82, v82
	v_exp_f32_e32 v83, v83
	v_pk_mul_f32 v[84:85], v[58:59], v[4:5] op_sel_hi:[0,1]
	v_exp_f32_e32 v84, v84
	v_exp_f32_e32 v85, v85
	v_pk_mul_f32 v[86:87], v[120:121], v[94:95] op_sel_hi:[0,1]
	v_pk_fma_f32 v[116:117], v[116:117], v[82:83], v[86:87]
	v_pk_mul_f32 v[82:83], v[120:121], v[96:97] op_sel_hi:[0,1]
	v_pk_fma_f32 v[118:119], v[118:119], v[84:85], v[82:83]
	s_nop 0
	s_waitcnt lgkmcnt(0)
	s_nop 0
	ds_read_b128 v[82:85], v160 offset:45600
	ds_read_b128 v[86:89], v160 offset:45616
	ds_read_b128 v[90:93], v160 offset:45632
	ds_read_b128 v[94:97], v160 offset:45648
	v_pk_mul_f32 v[134:135], v[60:61], v[14:15] op_sel_hi:[0,1]
	v_exp_f32_e32 v134, v134
	v_exp_f32_e32 v135, v135
	v_pk_mul_f32 v[136:137], v[60:61], v[16:17] op_sel_hi:[0,1]
	v_exp_f32_e32 v136, v136
	v_exp_f32_e32 v137, v137
	v_mul_f32_e32 v120, v60, v65
	v_pk_mul_f32 v[98:99], v[120:121], v[98:99] op_sel_hi:[0,1]
	v_pk_fma_f32 v[122:123], v[122:123], v[134:135], v[98:99]
	v_pk_mul_f32 v[98:99], v[120:121], v[100:101] op_sel_hi:[0,1]
	v_pk_fma_f32 v[124:125], v[124:125], v[136:137], v[98:99]
	v_pk_mul_f32 v[98:99], v[60:61], v[10:11] op_sel_hi:[0,1]
	v_exp_f32_e32 v98, v98
	v_exp_f32_e32 v99, v99
	v_pk_mul_f32 v[100:101], v[60:61], v[12:13] op_sel_hi:[0,1]
	v_exp_f32_e32 v100, v100
	v_exp_f32_e32 v101, v101
	v_pk_mul_f32 v[102:103], v[120:121], v[102:103] op_sel_hi:[0,1]
	v_pk_fma_f32 v[128:129], v[128:129], v[98:99], v[102:103]
	v_pk_mul_f32 v[98:99], v[120:121], v[104:105] op_sel_hi:[0,1]
	v_pk_fma_f32 v[126:127], v[126:127], v[100:101], v[98:99]
	v_pk_mul_f32 v[98:99], v[60:61], v[6:7] op_sel_hi:[0,1]
	v_exp_f32_e32 v98, v98
	v_exp_f32_e32 v99, v99
	v_pk_mul_f32 v[100:101], v[60:61], v[8:9] op_sel_hi:[0,1]
	v_exp_f32_e32 v100, v100
	v_exp_f32_e32 v101, v101
	v_pk_mul_f32 v[102:103], v[120:121], v[108:109] op_sel_hi:[0,1]
	v_pk_fma_f32 v[130:131], v[130:131], v[98:99], v[102:103]
	v_pk_mul_f32 v[98:99], v[120:121], v[110:111] op_sel_hi:[0,1]
	v_pk_fma_f32 v[132:133], v[132:133], v[100:101], v[98:99]
	v_pk_mul_f32 v[98:99], v[60:61], v[2:3] op_sel_hi:[0,1]
	v_exp_f32_e32 v98, v98
	v_exp_f32_e32 v99, v99
	v_pk_mul_f32 v[100:101], v[60:61], v[4:5] op_sel_hi:[0,1]
	v_exp_f32_e32 v100, v100
	v_exp_f32_e32 v101, v101
	v_pk_mul_f32 v[102:103], v[120:121], v[112:113] op_sel_hi:[0,1]
	v_pk_fma_f32 v[116:117], v[116:117], v[98:99], v[102:103]
	v_pk_mul_f32 v[98:99], v[120:121], v[114:115] op_sel_hi:[0,1]
	v_pk_fma_f32 v[118:119], v[118:119], v[100:101], v[98:99]
	s_nop 0
	s_waitcnt lgkmcnt(0)
	s_nop 0
	ds_read_b128 v[98:101], v160 offset:45808
	ds_read_b128 v[102:105], v160 offset:45824
	ds_read_b128 v[108:111], v160 offset:45840
	ds_read_b128 v[112:115], v160 offset:45856
	v_pk_mul_f32 v[134:135], v[62:63], v[14:15] op_sel_hi:[0,1]
	v_exp_f32_e32 v134, v134
	v_exp_f32_e32 v135, v135
	v_pk_mul_f32 v[136:137], v[62:63], v[16:17] op_sel_hi:[0,1]
	v_exp_f32_e32 v136, v136
	v_exp_f32_e32 v137, v137
	v_mul_f32_e32 v120, v62, v63
	v_pk_mul_f32 v[82:83], v[120:121], v[82:83] op_sel_hi:[0,1]
	v_pk_fma_f32 v[122:123], v[122:123], v[134:135], v[82:83]
	v_pk_mul_f32 v[82:83], v[120:121], v[84:85] op_sel_hi:[0,1]
	v_pk_fma_f32 v[124:125], v[124:125], v[136:137], v[82:83]
	v_pk_mul_f32 v[82:83], v[62:63], v[10:11] op_sel_hi:[0,1]
	v_exp_f32_e32 v82, v82
	v_exp_f32_e32 v83, v83
	v_pk_mul_f32 v[84:85], v[62:63], v[12:13] op_sel_hi:[0,1]
	v_exp_f32_e32 v84, v84
	v_exp_f32_e32 v85, v85
	v_pk_mul_f32 v[86:87], v[120:121], v[86:87] op_sel_hi:[0,1]
	v_pk_fma_f32 v[128:129], v[128:129], v[82:83], v[86:87]
	v_pk_mul_f32 v[82:83], v[120:121], v[88:89] op_sel_hi:[0,1]
	v_pk_fma_f32 v[126:127], v[126:127], v[84:85], v[82:83]
	v_pk_mul_f32 v[82:83], v[62:63], v[6:7] op_sel_hi:[0,1]
	v_exp_f32_e32 v82, v82
	v_exp_f32_e32 v83, v83
	v_pk_mul_f32 v[84:85], v[62:63], v[8:9] op_sel_hi:[0,1]
	v_exp_f32_e32 v84, v84
	v_exp_f32_e32 v85, v85
	v_pk_mul_f32 v[86:87], v[120:121], v[90:91] op_sel_hi:[0,1]
	v_pk_fma_f32 v[130:131], v[130:131], v[82:83], v[86:87]
	v_pk_mul_f32 v[82:83], v[120:121], v[92:93] op_sel_hi:[0,1]
	v_pk_fma_f32 v[132:133], v[132:133], v[84:85], v[82:83]
	v_pk_mul_f32 v[82:83], v[62:63], v[2:3] op_sel_hi:[0,1]
	v_exp_f32_e32 v82, v82
	v_exp_f32_e32 v83, v83
	v_pk_mul_f32 v[84:85], v[62:63], v[4:5] op_sel_hi:[0,1]
	v_exp_f32_e32 v84, v84
	v_exp_f32_e32 v85, v85
	v_pk_mul_f32 v[86:87], v[120:121], v[94:95] op_sel_hi:[0,1]
	v_pk_fma_f32 v[116:117], v[116:117], v[82:83], v[86:87]
	v_pk_mul_f32 v[82:83], v[120:121], v[96:97] op_sel_hi:[0,1]
	v_pk_fma_f32 v[118:119], v[118:119], v[84:85], v[82:83]
	s_nop 0
	s_waitcnt lgkmcnt(0)
	s_nop 0
	ds_read_b128 v[82:85], v160 offset:46016
	ds_read_b128 v[86:89], v160 offset:46032
	ds_read_b128 v[90:93], v160 offset:46048
	ds_read_b128 v[94:97], v160 offset:46064
	v_pk_mul_f32 v[134:135], v[64:65], v[14:15] op_sel_hi:[0,1]
	v_exp_f32_e32 v134, v134
	v_exp_f32_e32 v135, v135
	v_pk_mul_f32 v[136:137], v[64:65], v[16:17] op_sel_hi:[0,1]
	v_exp_f32_e32 v136, v136
	v_exp_f32_e32 v137, v137
	v_mul_f32_e32 v120, v64, v61
	v_pk_mul_f32 v[98:99], v[120:121], v[98:99] op_sel_hi:[0,1]
	v_pk_fma_f32 v[122:123], v[122:123], v[134:135], v[98:99]
	v_pk_mul_f32 v[98:99], v[120:121], v[100:101] op_sel_hi:[0,1]
	v_pk_fma_f32 v[124:125], v[124:125], v[136:137], v[98:99]
	v_pk_mul_f32 v[98:99], v[64:65], v[10:11] op_sel_hi:[0,1]
	v_exp_f32_e32 v98, v98
	v_exp_f32_e32 v99, v99
	v_pk_mul_f32 v[100:101], v[64:65], v[12:13] op_sel_hi:[0,1]
	v_exp_f32_e32 v100, v100
	v_exp_f32_e32 v101, v101
	v_pk_mul_f32 v[102:103], v[120:121], v[102:103] op_sel_hi:[0,1]
	v_pk_fma_f32 v[128:129], v[128:129], v[98:99], v[102:103]
	v_pk_mul_f32 v[98:99], v[120:121], v[104:105] op_sel_hi:[0,1]
	v_pk_fma_f32 v[126:127], v[126:127], v[100:101], v[98:99]
	v_pk_mul_f32 v[98:99], v[64:65], v[6:7] op_sel_hi:[0,1]
	v_exp_f32_e32 v98, v98
	v_exp_f32_e32 v99, v99
	v_pk_mul_f32 v[100:101], v[64:65], v[8:9] op_sel_hi:[0,1]
	v_exp_f32_e32 v100, v100
	v_exp_f32_e32 v101, v101
	v_pk_mul_f32 v[102:103], v[120:121], v[108:109] op_sel_hi:[0,1]
	v_pk_fma_f32 v[130:131], v[130:131], v[98:99], v[102:103]
	v_pk_mul_f32 v[98:99], v[120:121], v[110:111] op_sel_hi:[0,1]
	v_pk_fma_f32 v[132:133], v[132:133], v[100:101], v[98:99]
	v_pk_mul_f32 v[98:99], v[64:65], v[2:3] op_sel_hi:[0,1]
	v_exp_f32_e32 v98, v98
	v_exp_f32_e32 v99, v99
	v_pk_mul_f32 v[100:101], v[64:65], v[4:5] op_sel_hi:[0,1]
	v_exp_f32_e32 v100, v100
	v_exp_f32_e32 v101, v101
	v_pk_mul_f32 v[102:103], v[120:121], v[112:113] op_sel_hi:[0,1]
	v_pk_fma_f32 v[116:117], v[116:117], v[98:99], v[102:103]
	v_pk_mul_f32 v[98:99], v[120:121], v[114:115] op_sel_hi:[0,1]
	v_pk_fma_f32 v[118:119], v[118:119], v[100:101], v[98:99]
	s_nop 0
	s_waitcnt lgkmcnt(0)
	s_nop 0
	ds_read_b128 v[98:101], v160 offset:46224
	ds_read_b128 v[102:105], v160 offset:46240
	ds_read_b128 v[108:111], v160 offset:46256
	ds_read_b128 v[112:115], v160 offset:46272
	v_pk_mul_f32 v[134:135], v[66:67], v[14:15] op_sel_hi:[0,1]
	v_exp_f32_e32 v134, v134
	v_exp_f32_e32 v135, v135
	v_pk_mul_f32 v[136:137], v[66:67], v[16:17] op_sel_hi:[0,1]
	v_exp_f32_e32 v136, v136
	v_exp_f32_e32 v137, v137
	v_mul_f32_e32 v120, v66, v59
	v_pk_mul_f32 v[82:83], v[120:121], v[82:83] op_sel_hi:[0,1]
	v_pk_fma_f32 v[122:123], v[122:123], v[134:135], v[82:83]
	v_pk_mul_f32 v[82:83], v[120:121], v[84:85] op_sel_hi:[0,1]
	v_pk_fma_f32 v[124:125], v[124:125], v[136:137], v[82:83]
	v_pk_mul_f32 v[82:83], v[66:67], v[10:11] op_sel_hi:[0,1]
	v_exp_f32_e32 v82, v82
	v_exp_f32_e32 v83, v83
	v_pk_mul_f32 v[84:85], v[66:67], v[12:13] op_sel_hi:[0,1]
	v_exp_f32_e32 v84, v84
	v_exp_f32_e32 v85, v85
	v_pk_mul_f32 v[86:87], v[120:121], v[86:87] op_sel_hi:[0,1]
	v_pk_fma_f32 v[128:129], v[128:129], v[82:83], v[86:87]
	v_pk_mul_f32 v[82:83], v[120:121], v[88:89] op_sel_hi:[0,1]
	v_pk_fma_f32 v[126:127], v[126:127], v[84:85], v[82:83]
	v_pk_mul_f32 v[82:83], v[66:67], v[6:7] op_sel_hi:[0,1]
	v_exp_f32_e32 v82, v82
	v_exp_f32_e32 v83, v83
	v_pk_mul_f32 v[84:85], v[66:67], v[8:9] op_sel_hi:[0,1]
	v_exp_f32_e32 v84, v84
	v_exp_f32_e32 v85, v85
	v_pk_mul_f32 v[86:87], v[120:121], v[90:91] op_sel_hi:[0,1]
	v_pk_fma_f32 v[130:131], v[130:131], v[82:83], v[86:87]
	v_pk_mul_f32 v[82:83], v[120:121], v[92:93] op_sel_hi:[0,1]
	v_pk_fma_f32 v[132:133], v[132:133], v[84:85], v[82:83]
	v_pk_mul_f32 v[82:83], v[66:67], v[2:3] op_sel_hi:[0,1]
	v_exp_f32_e32 v82, v82
	v_exp_f32_e32 v83, v83
	v_pk_mul_f32 v[84:85], v[66:67], v[4:5] op_sel_hi:[0,1]
	v_exp_f32_e32 v84, v84
	v_exp_f32_e32 v85, v85
	v_pk_mul_f32 v[86:87], v[120:121], v[94:95] op_sel_hi:[0,1]
	v_pk_fma_f32 v[116:117], v[116:117], v[82:83], v[86:87]
	v_pk_mul_f32 v[82:83], v[120:121], v[96:97] op_sel_hi:[0,1]
	v_pk_fma_f32 v[118:119], v[118:119], v[84:85], v[82:83]
	s_nop 0
	s_waitcnt lgkmcnt(0)
	s_nop 0
	ds_read_b128 v[82:85], v160 offset:46432
	ds_read_b128 v[86:89], v160 offset:46448
	ds_read_b128 v[90:93], v160 offset:46464
	ds_read_b128 v[94:97], v160 offset:46480
	v_pk_mul_f32 v[134:135], v[68:69], v[14:15] op_sel_hi:[0,1]
	v_exp_f32_e32 v134, v134
	v_exp_f32_e32 v135, v135
	v_pk_mul_f32 v[136:137], v[68:69], v[16:17] op_sel_hi:[0,1]
	v_exp_f32_e32 v136, v136
	v_exp_f32_e32 v137, v137
	v_mul_f32_e32 v120, v68, v57
	v_pk_mul_f32 v[98:99], v[120:121], v[98:99] op_sel_hi:[0,1]
	v_pk_fma_f32 v[122:123], v[122:123], v[134:135], v[98:99]
	v_pk_mul_f32 v[98:99], v[120:121], v[100:101] op_sel_hi:[0,1]
	v_pk_fma_f32 v[124:125], v[124:125], v[136:137], v[98:99]
	v_pk_mul_f32 v[98:99], v[68:69], v[10:11] op_sel_hi:[0,1]
	v_exp_f32_e32 v98, v98
	v_exp_f32_e32 v99, v99
	v_pk_mul_f32 v[100:101], v[68:69], v[12:13] op_sel_hi:[0,1]
	v_exp_f32_e32 v100, v100
	v_exp_f32_e32 v101, v101
	v_pk_mul_f32 v[102:103], v[120:121], v[102:103] op_sel_hi:[0,1]
	v_pk_fma_f32 v[128:129], v[128:129], v[98:99], v[102:103]
	v_pk_mul_f32 v[98:99], v[120:121], v[104:105] op_sel_hi:[0,1]
	v_pk_fma_f32 v[126:127], v[126:127], v[100:101], v[98:99]
	v_pk_mul_f32 v[98:99], v[68:69], v[6:7] op_sel_hi:[0,1]
	v_exp_f32_e32 v98, v98
	v_exp_f32_e32 v99, v99
	v_pk_mul_f32 v[100:101], v[68:69], v[8:9] op_sel_hi:[0,1]
	v_exp_f32_e32 v100, v100
	v_exp_f32_e32 v101, v101
	v_pk_mul_f32 v[102:103], v[120:121], v[108:109] op_sel_hi:[0,1]
	v_pk_fma_f32 v[130:131], v[130:131], v[98:99], v[102:103]
	v_pk_mul_f32 v[98:99], v[120:121], v[110:111] op_sel_hi:[0,1]
	v_pk_fma_f32 v[132:133], v[132:133], v[100:101], v[98:99]
	v_pk_mul_f32 v[98:99], v[68:69], v[2:3] op_sel_hi:[0,1]
	v_exp_f32_e32 v98, v98
	v_exp_f32_e32 v99, v99
	v_pk_mul_f32 v[100:101], v[68:69], v[4:5] op_sel_hi:[0,1]
	v_exp_f32_e32 v100, v100
	v_exp_f32_e32 v101, v101
	v_pk_mul_f32 v[102:103], v[120:121], v[112:113] op_sel_hi:[0,1]
	v_pk_fma_f32 v[116:117], v[116:117], v[98:99], v[102:103]
	v_pk_mul_f32 v[98:99], v[120:121], v[114:115] op_sel_hi:[0,1]
	v_pk_fma_f32 v[118:119], v[118:119], v[100:101], v[98:99]
	s_nop 0
	s_waitcnt lgkmcnt(0)
	s_nop 0
	ds_read_b128 v[98:101], v160 offset:46640
	ds_read_b128 v[102:105], v160 offset:46656
	ds_read_b128 v[108:111], v160 offset:46672
	ds_read_b128 v[112:115], v160 offset:46688
	v_pk_mul_f32 v[134:135], v[70:71], v[14:15] op_sel_hi:[0,1]
	v_exp_f32_e32 v134, v134
	v_exp_f32_e32 v135, v135
	v_pk_mul_f32 v[136:137], v[70:71], v[16:17] op_sel_hi:[0,1]
	v_exp_f32_e32 v136, v136
	v_exp_f32_e32 v137, v137
	v_mul_f32_e32 v120, v70, v55
	v_pk_mul_f32 v[82:83], v[120:121], v[82:83] op_sel_hi:[0,1]
	v_pk_fma_f32 v[122:123], v[122:123], v[134:135], v[82:83]
	v_pk_mul_f32 v[82:83], v[120:121], v[84:85] op_sel_hi:[0,1]
	v_pk_fma_f32 v[124:125], v[124:125], v[136:137], v[82:83]
	v_pk_mul_f32 v[82:83], v[70:71], v[10:11] op_sel_hi:[0,1]
	v_exp_f32_e32 v82, v82
	v_exp_f32_e32 v83, v83
	v_pk_mul_f32 v[84:85], v[70:71], v[12:13] op_sel_hi:[0,1]
	v_exp_f32_e32 v84, v84
	v_exp_f32_e32 v85, v85
	v_pk_mul_f32 v[86:87], v[120:121], v[86:87] op_sel_hi:[0,1]
	v_pk_fma_f32 v[128:129], v[128:129], v[82:83], v[86:87]
	v_pk_mul_f32 v[82:83], v[120:121], v[88:89] op_sel_hi:[0,1]
	v_pk_fma_f32 v[126:127], v[126:127], v[84:85], v[82:83]
	v_pk_mul_f32 v[82:83], v[70:71], v[6:7] op_sel_hi:[0,1]
	v_exp_f32_e32 v82, v82
	v_exp_f32_e32 v83, v83
	v_pk_mul_f32 v[84:85], v[70:71], v[8:9] op_sel_hi:[0,1]
	v_exp_f32_e32 v84, v84
	v_exp_f32_e32 v85, v85
	v_pk_mul_f32 v[86:87], v[120:121], v[90:91] op_sel_hi:[0,1]
	v_pk_fma_f32 v[130:131], v[130:131], v[82:83], v[86:87]
	v_pk_mul_f32 v[82:83], v[120:121], v[92:93] op_sel_hi:[0,1]
	v_pk_fma_f32 v[132:133], v[132:133], v[84:85], v[82:83]
	v_pk_mul_f32 v[82:83], v[70:71], v[2:3] op_sel_hi:[0,1]
	v_exp_f32_e32 v82, v82
	v_exp_f32_e32 v83, v83
	v_pk_mul_f32 v[84:85], v[70:71], v[4:5] op_sel_hi:[0,1]
	v_exp_f32_e32 v84, v84
	v_exp_f32_e32 v85, v85
	v_pk_mul_f32 v[86:87], v[120:121], v[94:95] op_sel_hi:[0,1]
	v_pk_fma_f32 v[116:117], v[116:117], v[82:83], v[86:87]
	v_pk_mul_f32 v[82:83], v[120:121], v[96:97] op_sel_hi:[0,1]
	v_pk_fma_f32 v[118:119], v[118:119], v[84:85], v[82:83]
	s_nop 0
	s_waitcnt lgkmcnt(0)
	s_nop 0
	ds_read_b128 v[82:85], v160 offset:46848
	ds_read_b128 v[86:89], v160 offset:46864
	ds_read_b128 v[90:93], v160 offset:46880
	ds_read_b128 v[94:97], v160 offset:46896
	v_pk_mul_f32 v[134:135], v[72:73], v[14:15] op_sel_hi:[0,1]
	v_exp_f32_e32 v134, v134
	v_exp_f32_e32 v135, v135
	v_pk_mul_f32 v[136:137], v[72:73], v[16:17] op_sel_hi:[0,1]
	v_exp_f32_e32 v136, v136
	v_exp_f32_e32 v137, v137
	v_mul_f32_e32 v120, v72, v53
	v_pk_mul_f32 v[98:99], v[120:121], v[98:99] op_sel_hi:[0,1]
	v_pk_fma_f32 v[122:123], v[122:123], v[134:135], v[98:99]
	v_pk_mul_f32 v[98:99], v[120:121], v[100:101] op_sel_hi:[0,1]
	v_pk_fma_f32 v[124:125], v[124:125], v[136:137], v[98:99]
	v_pk_mul_f32 v[98:99], v[72:73], v[10:11] op_sel_hi:[0,1]
	v_exp_f32_e32 v98, v98
	v_exp_f32_e32 v99, v99
	v_pk_mul_f32 v[100:101], v[72:73], v[12:13] op_sel_hi:[0,1]
	v_exp_f32_e32 v100, v100
	v_exp_f32_e32 v101, v101
	v_pk_mul_f32 v[102:103], v[120:121], v[102:103] op_sel_hi:[0,1]
	v_pk_fma_f32 v[128:129], v[128:129], v[98:99], v[102:103]
	v_pk_mul_f32 v[98:99], v[120:121], v[104:105] op_sel_hi:[0,1]
	v_pk_fma_f32 v[126:127], v[126:127], v[100:101], v[98:99]
	v_pk_mul_f32 v[98:99], v[72:73], v[6:7] op_sel_hi:[0,1]
	v_exp_f32_e32 v98, v98
	v_exp_f32_e32 v99, v99
	v_pk_mul_f32 v[100:101], v[72:73], v[8:9] op_sel_hi:[0,1]
	v_exp_f32_e32 v100, v100
	v_exp_f32_e32 v101, v101
	v_pk_mul_f32 v[102:103], v[120:121], v[108:109] op_sel_hi:[0,1]
	v_pk_fma_f32 v[130:131], v[130:131], v[98:99], v[102:103]
	v_pk_mul_f32 v[98:99], v[120:121], v[110:111] op_sel_hi:[0,1]
	v_pk_fma_f32 v[132:133], v[132:133], v[100:101], v[98:99]
	v_pk_mul_f32 v[98:99], v[72:73], v[2:3] op_sel_hi:[0,1]
	v_exp_f32_e32 v98, v98
	v_exp_f32_e32 v99, v99
	v_pk_mul_f32 v[100:101], v[72:73], v[4:5] op_sel_hi:[0,1]
	v_exp_f32_e32 v100, v100
	v_exp_f32_e32 v101, v101
	v_pk_mul_f32 v[102:103], v[120:121], v[112:113] op_sel_hi:[0,1]
	v_pk_fma_f32 v[116:117], v[116:117], v[98:99], v[102:103]
	v_pk_mul_f32 v[98:99], v[120:121], v[114:115] op_sel_hi:[0,1]
	v_pk_fma_f32 v[118:119], v[118:119], v[100:101], v[98:99]
	s_nop 0
	s_waitcnt lgkmcnt(0)
	s_nop 0
	ds_read_b128 v[98:101], v160 offset:47056
	ds_read_b128 v[102:105], v160 offset:47072
	ds_read_b128 v[108:111], v160 offset:47088
	ds_read_b128 v[112:115], v160 offset:47104
	v_pk_mul_f32 v[134:135], v[74:75], v[14:15] op_sel_hi:[0,1]
	v_exp_f32_e32 v134, v134
	v_exp_f32_e32 v135, v135
	v_pk_mul_f32 v[136:137], v[74:75], v[16:17] op_sel_hi:[0,1]
	v_exp_f32_e32 v136, v136
	v_exp_f32_e32 v137, v137
	v_mul_f32_e32 v120, v74, v51
	v_pk_mul_f32 v[82:83], v[120:121], v[82:83] op_sel_hi:[0,1]
	v_pk_fma_f32 v[122:123], v[122:123], v[134:135], v[82:83]
	v_pk_mul_f32 v[82:83], v[120:121], v[84:85] op_sel_hi:[0,1]
	v_pk_fma_f32 v[124:125], v[124:125], v[136:137], v[82:83]
	v_pk_mul_f32 v[82:83], v[74:75], v[10:11] op_sel_hi:[0,1]
	v_exp_f32_e32 v82, v82
	v_exp_f32_e32 v83, v83
	v_pk_mul_f32 v[84:85], v[74:75], v[12:13] op_sel_hi:[0,1]
	v_exp_f32_e32 v84, v84
	v_exp_f32_e32 v85, v85
	v_pk_mul_f32 v[86:87], v[120:121], v[86:87] op_sel_hi:[0,1]
	v_pk_fma_f32 v[128:129], v[128:129], v[82:83], v[86:87]
	v_pk_mul_f32 v[82:83], v[120:121], v[88:89] op_sel_hi:[0,1]
	v_pk_fma_f32 v[126:127], v[126:127], v[84:85], v[82:83]
	v_pk_mul_f32 v[82:83], v[74:75], v[6:7] op_sel_hi:[0,1]
	v_exp_f32_e32 v82, v82
	v_exp_f32_e32 v83, v83
	v_pk_mul_f32 v[84:85], v[74:75], v[8:9] op_sel_hi:[0,1]
	v_exp_f32_e32 v84, v84
	v_exp_f32_e32 v85, v85
	v_pk_mul_f32 v[86:87], v[120:121], v[90:91] op_sel_hi:[0,1]
	v_pk_fma_f32 v[130:131], v[130:131], v[82:83], v[86:87]
	v_pk_mul_f32 v[82:83], v[120:121], v[92:93] op_sel_hi:[0,1]
	v_pk_fma_f32 v[132:133], v[132:133], v[84:85], v[82:83]
	v_pk_mul_f32 v[82:83], v[74:75], v[2:3] op_sel_hi:[0,1]
	v_exp_f32_e32 v82, v82
	v_exp_f32_e32 v83, v83
	v_pk_mul_f32 v[84:85], v[74:75], v[4:5] op_sel_hi:[0,1]
	v_exp_f32_e32 v84, v84
	v_exp_f32_e32 v85, v85
	v_pk_mul_f32 v[86:87], v[120:121], v[94:95] op_sel_hi:[0,1]
	v_pk_fma_f32 v[116:117], v[116:117], v[82:83], v[86:87]
	v_pk_mul_f32 v[82:83], v[120:121], v[96:97] op_sel_hi:[0,1]
	v_pk_fma_f32 v[118:119], v[118:119], v[84:85], v[82:83]
	s_nop 0
	s_waitcnt lgkmcnt(0)
	s_nop 0
	ds_read_b128 v[82:85], v160 offset:47264
	ds_read_b128 v[86:89], v160 offset:47280
	ds_read_b128 v[90:93], v160 offset:47296
	ds_read_b128 v[94:97], v160 offset:47312
	v_pk_mul_f32 v[134:135], v[76:77], v[14:15] op_sel_hi:[0,1]
	v_exp_f32_e32 v134, v134
	v_exp_f32_e32 v135, v135
	v_pk_mul_f32 v[136:137], v[76:77], v[16:17] op_sel_hi:[0,1]
	v_exp_f32_e32 v136, v136
	v_exp_f32_e32 v137, v137
	v_mul_f32_e32 v120, v76, v49
	v_pk_mul_f32 v[98:99], v[120:121], v[98:99] op_sel_hi:[0,1]
	v_pk_fma_f32 v[122:123], v[122:123], v[134:135], v[98:99]
	v_pk_mul_f32 v[98:99], v[120:121], v[100:101] op_sel_hi:[0,1]
	v_pk_fma_f32 v[124:125], v[124:125], v[136:137], v[98:99]
	v_pk_mul_f32 v[98:99], v[76:77], v[10:11] op_sel_hi:[0,1]
	v_exp_f32_e32 v98, v98
	v_exp_f32_e32 v99, v99
	v_pk_mul_f32 v[100:101], v[76:77], v[12:13] op_sel_hi:[0,1]
	v_exp_f32_e32 v100, v100
	v_exp_f32_e32 v101, v101
	v_pk_mul_f32 v[102:103], v[120:121], v[102:103] op_sel_hi:[0,1]
	v_pk_fma_f32 v[128:129], v[128:129], v[98:99], v[102:103]
	v_pk_mul_f32 v[98:99], v[120:121], v[104:105] op_sel_hi:[0,1]
	v_pk_fma_f32 v[126:127], v[126:127], v[100:101], v[98:99]
	v_pk_mul_f32 v[98:99], v[76:77], v[6:7] op_sel_hi:[0,1]
	v_exp_f32_e32 v98, v98
	v_exp_f32_e32 v99, v99
	v_pk_mul_f32 v[100:101], v[76:77], v[8:9] op_sel_hi:[0,1]
	v_exp_f32_e32 v100, v100
	v_exp_f32_e32 v101, v101
	v_pk_mul_f32 v[102:103], v[120:121], v[108:109] op_sel_hi:[0,1]
	v_pk_fma_f32 v[130:131], v[130:131], v[98:99], v[102:103]
	v_pk_mul_f32 v[98:99], v[120:121], v[110:111] op_sel_hi:[0,1]
	v_pk_fma_f32 v[132:133], v[132:133], v[100:101], v[98:99]
	v_pk_mul_f32 v[98:99], v[76:77], v[2:3] op_sel_hi:[0,1]
	v_exp_f32_e32 v98, v98
	v_exp_f32_e32 v99, v99
	v_pk_mul_f32 v[100:101], v[76:77], v[4:5] op_sel_hi:[0,1]
	v_exp_f32_e32 v100, v100
	v_exp_f32_e32 v101, v101
	v_pk_mul_f32 v[102:103], v[120:121], v[112:113] op_sel_hi:[0,1]
	v_pk_fma_f32 v[116:117], v[116:117], v[98:99], v[102:103]
	v_pk_mul_f32 v[98:99], v[120:121], v[114:115] op_sel_hi:[0,1]
	v_pk_fma_f32 v[118:119], v[118:119], v[100:101], v[98:99]
	s_nop 0
	s_waitcnt lgkmcnt(0)
	s_nop 0
	ds_read_b128 v[98:101], v160 offset:47472
	ds_read_b128 v[102:105], v160 offset:47488
	ds_read_b128 v[108:111], v160 offset:47504
	ds_read_b128 v[112:115], v160 offset:47520
	v_add_f32_e32 v19, 0, v80
	v_add_f32_e32 v19, v19, v20
	v_add_f32_e32 v19, v19, v22
	v_add_f32_e32 v19, v19, v24
	v_add_f32_e32 v19, v19, v26
	v_add_f32_e32 v19, v19, v28
	v_add_f32_e32 v19, v19, v30
	v_add_f32_e32 v19, v19, v32
	v_add_f32_e32 v19, v19, v34
	v_add_f32_e32 v19, v19, v36
	v_pk_mul_f32 v[134:135], v[78:79], v[14:15] op_sel_hi:[0,1]
	v_pk_mul_f32 v[136:137], v[78:79], v[16:17] op_sel_hi:[0,1]
	v_add_f32_e32 v19, v19, v38
	v_exp_f32_e32 v134, v134
	v_exp_f32_e32 v135, v135
	v_exp_f32_e32 v136, v136
	v_exp_f32_e32 v137, v137
	v_add_f32_e32 v19, v19, v40
	v_add_f32_e32 v19, v19, v42
	v_mul_f32_e32 v120, v78, v47
	v_add_f32_e32 v19, v19, v44
	v_pk_mul_f32 v[82:83], v[120:121], v[82:83] op_sel_hi:[0,1]
	v_pk_mul_f32 v[84:85], v[120:121], v[84:85] op_sel_hi:[0,1]
	v_add_f32_e32 v19, v19, v46
	v_pk_fma_f32 v[82:83], v[122:123], v[134:135], v[82:83]
	v_pk_fma_f32 v[84:85], v[124:125], v[136:137], v[84:85]
	v_pk_mul_f32 v[122:123], v[78:79], v[10:11] op_sel_hi:[0,1]
	v_pk_mul_f32 v[124:125], v[78:79], v[12:13] op_sel_hi:[0,1]
	v_add_f32_e32 v19, v19, v48
	v_exp_f32_e32 v122, v122
	v_exp_f32_e32 v123, v123
	v_exp_f32_e32 v124, v124
	v_exp_f32_e32 v125, v125
	v_add_f32_e32 v19, v19, v50
	v_add_f32_e32 v19, v19, v52
	v_add_f32_e32 v19, v19, v54
	v_pk_mul_f32 v[86:87], v[120:121], v[86:87] op_sel_hi:[0,1]
	v_pk_mul_f32 v[88:89], v[120:121], v[88:89] op_sel_hi:[0,1]
	v_add_f32_e32 v19, v19, v56
	v_pk_fma_f32 v[86:87], v[128:129], v[122:123], v[86:87]
	v_pk_fma_f32 v[88:89], v[126:127], v[124:125], v[88:89]
	v_pk_mul_f32 v[122:123], v[78:79], v[6:7] op_sel_hi:[0,1]
	v_pk_mul_f32 v[124:125], v[78:79], v[8:9] op_sel_hi:[0,1]
	v_add_f32_e32 v19, v19, v58
	v_exp_f32_e32 v122, v122
	v_exp_f32_e32 v123, v123
	v_exp_f32_e32 v124, v124
	v_exp_f32_e32 v125, v125
	v_add_f32_e32 v19, v19, v60
	v_add_f32_e32 v19, v19, v62
	v_add_f32_e32 v19, v19, v64
	v_pk_mul_f32 v[90:91], v[120:121], v[90:91] op_sel_hi:[0,1]
	v_pk_mul_f32 v[92:93], v[120:121], v[92:93] op_sel_hi:[0,1]
	v_add_f32_e32 v19, v19, v66
	v_pk_fma_f32 v[90:91], v[130:131], v[122:123], v[90:91]
	v_pk_fma_f32 v[92:93], v[132:133], v[124:125], v[92:93]
	v_pk_mul_f32 v[122:123], v[78:79], v[2:3] op_sel_hi:[0,1]
	v_pk_mul_f32 v[124:125], v[78:79], v[4:5] op_sel_hi:[0,1]
	v_add_f32_e32 v19, v19, v68
	v_exp_f32_e32 v122, v122
	v_exp_f32_e32 v123, v123
	v_exp_f32_e32 v124, v124
	v_exp_f32_e32 v125, v125
	v_add_f32_e32 v19, v19, v70
	v_add_f32_e32 v19, v19, v72
	v_add_f32_e32 v19, v19, v74
	v_pk_mul_f32 v[94:95], v[120:121], v[94:95] op_sel_hi:[0,1]
	v_pk_mul_f32 v[96:97], v[120:121], v[96:97] op_sel_hi:[0,1]
	v_add_f32_e32 v19, v19, v76
	v_pk_fma_f32 v[94:95], v[116:117], v[122:123], v[94:95]
	v_pk_fma_f32 v[96:97], v[118:119], v[124:125], v[96:97]
	v_add_f32_e32 v19, v19, v78
	s_waitcnt lgkmcnt(0)
	v_cvt_f32_f16_e32 v20, v106
	v_add_f32_e32 v19, v19, v18
	v_pk_mul_f32 v[4:5], v[18:19], v[4:5] op_sel_hi:[0,1]
	v_exp_f32_e32 v4, v4
	v_exp_f32_e32 v5, v5
	v_pk_mul_f32 v[14:15], v[18:19], v[14:15] op_sel_hi:[0,1]
	v_exp_f32_e32 v14, v14
	v_exp_f32_e32 v15, v15
	v_mul_f32_e32 v20, v18, v20
	v_pk_mul_f32 v[22:23], v[20:21], v[114:115] op_sel_hi:[0,1]
	v_pk_fma_f32 v[22:23], v[96:97], v[4:5], v[22:23]
	v_pk_mul_f32 v[4:5], v[20:21], v[98:99] op_sel_hi:[0,1]
	v_pk_fma_f32 v[14:15], v[82:83], v[14:15], v[4:5]
	v_pk_mul_f32 v[4:5], v[18:19], v[16:17] op_sel_hi:[0,1]
	v_exp_f32_e32 v4, v4
	v_exp_f32_e32 v5, v5
	v_pk_mul_f32 v[10:11], v[18:19], v[10:11] op_sel_hi:[0,1]
	v_exp_f32_e32 v10, v10
	v_exp_f32_e32 v11, v11
	v_pk_mul_f32 v[16:17], v[20:21], v[100:101] op_sel_hi:[0,1]
	v_pk_fma_f32 v[16:17], v[84:85], v[4:5], v[16:17]
	v_pk_mul_f32 v[4:5], v[20:21], v[102:103] op_sel_hi:[0,1]
	v_pk_fma_f32 v[10:11], v[86:87], v[10:11], v[4:5]
	v_pk_mul_f32 v[4:5], v[18:19], v[12:13] op_sel_hi:[0,1]
	v_exp_f32_e32 v4, v4
	v_exp_f32_e32 v5, v5
	v_pk_mul_f32 v[6:7], v[18:19], v[6:7] op_sel_hi:[0,1]
	v_exp_f32_e32 v6, v6
	v_exp_f32_e32 v7, v7
	v_pk_mul_f32 v[8:9], v[18:19], v[8:9] op_sel_hi:[0,1]
	v_exp_f32_e32 v8, v8
	v_exp_f32_e32 v9, v9
	v_pk_mul_f32 v[2:3], v[18:19], v[2:3] op_sel_hi:[0,1]
	v_pk_mul_f32 v[12:13], v[20:21], v[104:105] op_sel_hi:[0,1]
	v_exp_f32_e32 v2, v2
	v_exp_f32_e32 v3, v3
	v_pk_fma_f32 v[4:5], v[88:89], v[4:5], v[12:13]
	v_pk_mul_f32 v[12:13], v[20:21], v[108:109] op_sel_hi:[0,1]
	v_pk_fma_f32 v[6:7], v[90:91], v[6:7], v[12:13]
	v_pk_mul_f32 v[12:13], v[20:21], v[110:111] op_sel_hi:[0,1]
	v_pk_fma_f32 v[8:9], v[92:93], v[8:9], v[12:13]
	v_pk_mul_f32 v[12:13], v[20:21], v[112:113] op_sel_hi:[0,1]
	v_cvt_pk_f16_f32 v5, v4, v5
	v_cvt_pk_f16_f32 v4, v10, v11
	v_lshl_or_b32 v10, v0, 4, s6
	v_mov_b32_e32 v11, s7
	v_pk_fma_f32 v[12:13], v[94:95], v[2:3], v[12:13]
	v_cvt_pk_f16_f32 v3, v16, v17
	v_cvt_pk_f16_f32 v2, v14, v15
	v_lshl_add_u64 v[10:11], s[4:5], 0, v[10:11]
	s_movk_i32 s4, 0x2000
	global_store_dwordx4 v[10:11], v[2:5], off sc0 sc1
	global_store_dword v1, v19, s[0:1] sc0 sc1
	s_nop 0
	v_cvt_pk_f16_f32 v2, v6, v7
	v_add_co_u32_e32 v6, vcc, s4, v10
	v_cvt_pk_f16_f32 v5, v22, v23
	v_cvt_pk_f16_f32 v4, v12, v13
	v_cvt_pk_f16_f32 v3, v8, v9
	v_addc_co_u32_e32 v7, vcc, 0, v11, vcc
	global_store_dwordx4 v[6:7], v[2:5], off sc0 sc1
	s_endpgm

	.amdhsa_kernel _Z12k_conv_xprojPKDF16_PKfS2_S0_S0_S2_PDF16_S3_PfS2_S3_S4_
		.amdhsa_group_segment_fixed_size 47616
		.amdhsa_private_segment_fixed_size 0
		.amdhsa_kernarg_size 96
		.amdhsa_user_sgpr_count 2
		.amdhsa_user_sgpr_dispatch_ptr 0
		.amdhsa_user_sgpr_queue_ptr 0
		.amdhsa_user_sgpr_kernarg_segment_ptr 1
		.amdhsa_user_sgpr_dispatch_id 0
		.amdhsa_user_sgpr_kernarg_preload_length 0
		.amdhsa_user_sgpr_kernarg_preload_offset 0
		.amdhsa_user_sgpr_private_segment_size 0
		.amdhsa_uses_dynamic_stack 0
		.amdhsa_enable_private_segment 0
		.amdhsa_system_sgpr_workgroup_id_x 1
		.amdhsa_system_sgpr_workgroup_id_y 0
		.amdhsa_system_sgpr_workgroup_id_z 0
		.amdhsa_system_sgpr_workgroup_info 0
		.amdhsa_system_vgpr_workitem_id 0
		.amdhsa_next_free_vgpr 164
		.amdhsa_next_free_sgpr 91
		.amdhsa_accum_offset 164
		.amdhsa_reserve_vcc 1
		.amdhsa_float_round_mode_32 0
		.amdhsa_float_round_mode_16_64 0
		.amdhsa_float_denorm_mode_32 3
		.amdhsa_float_denorm_mode_16_64 3
		.amdhsa_dx10_clamp 1
		.amdhsa_ieee_mode 1
		.amdhsa_fp16_overflow 0
		.amdhsa_tg_split 0
		.amdhsa_exception_fp_ieee_invalid_op 0
		.amdhsa_exception_fp_denorm_src 0
		.amdhsa_exception_fp_ieee_div_zero 0
		.amdhsa_exception_fp_ieee_overflow 0
		.amdhsa_exception_fp_ieee_underflow 0
		.amdhsa_exception_fp_ieee_inexact 0
		.amdhsa_exception_int_div_zero 0
	.end_amdhsa_kernel

_Z4k_k2ILb0EEvPKDF16_S1_PKfS3_S3_S1_S1_PfS3_S3_S1_PDF16_PKiS4_S4_:
	s_load_dwordx2 s[24:25], s[0:1], 0x58
	s_load_dwordx8 s[4:11], s[0:1], 0x38
	s_load_dwordx4 s[20:23], s[0:1], 0x0
	s_load_dwordx8 s[12:19], s[0:1], 0x18
	s_load_dwordx2 s[54:55], s[0:1], 0x10
	s_lshl_b32 s3, s2, 5
	s_and_b32 s3, s3, 0xe0
	s_lshr_b32 s26, s2, 3
	s_or_b32 s3, s3, s26
	s_movk_i32 s26, 0x100
	s_lshl_b32 s28, s3, 5
	v_cmp_gt_u32_e32 vcc, s26, v0
	v_mov_b32_e32 v67, 0
	v_lshlrev_b32_e32 v66, 4, v0
	s_lshl_b32 s0, s3, 1
	s_and_b32 s26, s0, 0xffffffe
	s_mov_b32 s27, 0
	s_waitcnt lgkmcnt(0)
	v_lshl_add_u64 v[2:3], s[16:17], 0, v[66:67]
	s_lshl_b64 s[0:1], s[26:27], 13
	s_or_b32 s26, s26, 1
	v_lshl_add_u64 v[4:5], v[2:3], 0, s[0:1]
	s_lshl_b64 s[0:1], s[26:27], 13
	v_lshl_add_u64 v[2:3], v[2:3], 0, s[0:1]
	global_load_dwordx4 v[68:71], v[4:5], off
	global_load_dwordx4 v[72:75], v[2:3], off
	v_lshl_add_u64 v[2:3], s[12:13], 0, v[66:67]
	s_movk_i32 s29, 0x2000
	v_add_co_u32_e32 v4, vcc, s29, v2
	s_movk_i32 s52, 0x4000
	s_nop 0
	v_addc_co_u32_e32 v5, vcc, 0, v3, vcc
	v_add_co_u32_e32 v18, vcc, s52, v2
	s_movk_i32 s33, 0x6000
	s_nop 0
	v_addc_co_u32_e32 v19, vcc, 0, v3, vcc
	s_lshl_b32 s26, s3, 2
	global_load_dwordx4 v[14:17], v66, s[12:13]
	global_load_dwordx4 v[10:13], v[4:5], off
	global_load_dwordx4 v[6:9], v[18:19], off
	v_add_co_u32_e32 v18, vcc, s33, v2
	s_add_u32 s0, s24, 0x800000
	s_nop 0
	v_addc_co_u32_e32 v19, vcc, 0, v3, vcc
	s_addc_u32 s1, s25, 0
	s_lshl_b64 s[12:13], s[26:27], 13
	v_lshlrev_b32_e32 v20, 2, v0
	global_load_dwordx4 v[2:5], v[18:19], off
	global_load_dword v1, v20, s[14:15]
	v_or_b32_e32 v18, s12, v66
	v_mov_b32_e32 v19, s13
	s_or_b32 s12, s26, 1
	s_mov_b32 s13, s27
	s_lshl_b64 s[12:13], s[12:13], 13
	v_lshl_add_u64 v[76:77], s[22:23], 0, v[18:19]
	v_lshl_add_u64 v[78:79], s[20:21], 0, v[18:19]
	v_lshl_add_u64 v[80:81], s[0:1], 0, v[18:19]
	v_or_b32_e32 v18, s12, v66
	v_mov_b32_e32 v19, s13
	s_or_b32 s12, s26, 2
	s_mov_b32 s13, s27
	s_lshl_b64 s[12:13], s[12:13], 13
	s_or_b32 s26, s26, 3
	v_lshl_add_u64 v[82:83], s[22:23], 0, v[18:19]
	v_lshl_add_u64 v[84:85], s[20:21], 0, v[18:19]
	v_lshl_add_u64 v[86:87], s[0:1], 0, v[18:19]
	v_or_b32_e32 v18, s12, v66
	v_mov_b32_e32 v19, s13
	s_lshl_b64 s[12:13], s[26:27], 13
	v_lshl_add_u64 v[88:89], s[22:23], 0, v[18:19]
	v_lshl_add_u64 v[90:91], s[20:21], 0, v[18:19]
	v_lshl_add_u64 v[92:93], s[0:1], 0, v[18:19]
	v_or_b32_e32 v18, s12, v66
	v_mov_b32_e32 v19, s13
	v_lshl_add_u64 v[94:95], s[22:23], 0, v[18:19]
	v_lshl_add_u64 v[96:97], s[20:21], 0, v[18:19]
	v_lshl_add_u64 v[98:99], s[0:1], 0, v[18:19]
	global_load_dwordx4 v[62:65], v[76:77], off
	global_load_dwordx4 v[54:57], v[78:79], off
	global_load_dwordx4 v[58:61], v[80:81], off
	v_mov_b64_e32 v[212:213], v[82:83]
	v_mov_b64_e32 v[214:215], v[84:85]
	v_mov_b64_e32 v[216:217], v[86:87]
	v_mov_b64_e32 v[218:219], v[88:89]
	v_mov_b64_e32 v[220:221], v[90:91]
	v_mov_b64_e32 v[222:223], v[92:93]
	v_mov_b64_e32 v[224:225], v[94:95]
	v_mov_b64_e32 v[226:227], v[96:97]
	v_mov_b64_e32 v[228:229], v[98:99]
	s_lshl_b32 s30, s28, 7
	s_add_u32 s54, s54, s30
	s_addc_u32 s55, s55, 0
	s_load_dwordx16 s[36:51], s[54:55], 0x0
	s_load_dwordx16 s[72:87], s[54:55], 0x40
	s_load_dwordx16 s[56:71], s[54:55], 0x80
	s_load_dwordx8 s[88:95], s[54:55], 0xc0
	s_load_dwordx4 s[96:99], s[54:55], 0xe0
	s_load_dwordx4 s[20:23], s[54:55], 0xf0
	v_lshrrev_b32_e32 v196, 6, v0
	s_nop 1
	v_readfirstlane_b32 s16, v196
	s_nop 3
	s_lshl_b32 s16, s16, 9
	s_add_u32 s16, s54, s16
	s_addc_u32 s17, s55, 0
	s_load_dword s30, s[16:17], 0x0
	s_load_dword s30, s[16:17], 0x40
	s_load_dword s30, s[16:17], 0x80
	s_load_dword s30, s[16:17], 0xc0
	s_load_dword s30, s[16:17], 0x100
	s_load_dword s30, s[16:17], 0x140
	s_load_dword s30, s[16:17], 0x180
	s_load_dword s30, s[16:17], 0x1c0
	s_waitcnt vmcnt(9)
	v_cvt_f32_f16_e32 v134, v68
	v_cvt_f32_f16_sdwa v135, v68 dst_sel:DWORD dst_unused:UNUSED_PAD src0_sel:WORD_1
	v_cvt_f32_f16_e32 v136, v69
	v_cvt_f32_f16_sdwa v137, v69 dst_sel:DWORD dst_unused:UNUSED_PAD src0_sel:WORD_1
	v_cvt_f32_f16_e32 v138, v70
	v_cvt_f32_f16_sdwa v139, v70 dst_sel:DWORD dst_unused:UNUSED_PAD src0_sel:WORD_1
	v_cvt_f32_f16_e32 v140, v71
	v_cvt_f32_f16_sdwa v141, v71 dst_sel:DWORD dst_unused:UNUSED_PAD src0_sel:WORD_1
	s_waitcnt vmcnt(8)
	v_cvt_f32_f16_e32 v142, v72
	v_cvt_f32_f16_sdwa v143, v72 dst_sel:DWORD dst_unused:UNUSED_PAD src0_sel:WORD_1
	v_cvt_f32_f16_e32 v144, v73
	v_cvt_f32_f16_sdwa v145, v73 dst_sel:DWORD dst_unused:UNUSED_PAD src0_sel:WORD_1
	v_cvt_f32_f16_e32 v146, v74
	v_cvt_f32_f16_sdwa v147, v74 dst_sel:DWORD dst_unused:UNUSED_PAD src0_sel:WORD_1
	v_cvt_f32_f16_e32 v148, v75
	v_cvt_f32_f16_sdwa v149, v75 dst_sel:DWORD dst_unused:UNUSED_PAD src0_sel:WORD_1
	s_waitcnt lgkmcnt(0)
	v_lshlrev_b32_e32 v68, 1, v0
	s_waitcnt vmcnt(2)
	v_cvt_f32_f16_e32 v150, v62
	s_waitcnt vmcnt(1)
	v_pk_mul_f32 v[154:155], v[150:151], v[14:15] op_sel_hi:[0,1]
	v_exp_f32_e32 v154, v154
	v_exp_f32_e32 v155, v155
	v_pk_mul_f32 v[156:157], v[150:151], v[16:17] op_sel_hi:[0,1]
	v_exp_f32_e32 v156, v156
	v_exp_f32_e32 v157, v157
	v_fma_mix_f32 v152, v150, v54, 0 op_sel_hi:[0,1,0]
	v_pk_mul_f32 v[134:135], v[154:155], v[134:135]
	v_pk_fma_f32 v[134:135], v[152:153], s[36:37], v[134:135] op_sel_hi:[0, 1, 1]
	v_pk_fma_f32 v[70:71], s[72:73], v[134:135], 0 op_sel_hi:[1, 1, 0]
	v_pk_mul_f32 v[86:87], v[156:157], v[136:137]
	s_nop 0
	v_pk_fma_f32 v[136:137], v[152:153], s[38:39], v[86:87] op_sel_hi:[0, 1, 1]
	v_pk_mul_f32 v[72:73], v[150:151], v[10:11] op_sel_hi:[0,1]
	v_exp_f32_e32 v72, v72
	v_exp_f32_e32 v73, v73
	v_pk_mul_f32 v[86:87], v[150:151], v[12:13] op_sel_hi:[0,1]
	v_exp_f32_e32 v86, v86
	v_exp_f32_e32 v87, v87
	v_pk_mul_f32 v[72:73], v[72:73], v[138:139]
	v_pk_fma_f32 v[70:71], s[74:75], v[136:137], v[70:71]
	v_pk_fma_f32 v[138:139], v[152:153], s[40:41], v[72:73] op_sel_hi:[0, 1, 1]
	v_pk_mul_f32 v[72:73], v[86:87], v[140:141]
	v_pk_mul_f32 v[74:75], v[150:151], v[8:9] op_sel_hi:[0,1]
	v_pk_fma_f32 v[140:141], v[152:153], s[42:43], v[72:73] op_sel_hi:[0, 1, 1]
	v_pk_mul_f32 v[72:73], v[150:151], v[6:7] op_sel_hi:[0,1]
	v_exp_f32_e32 v72, v72
	v_exp_f32_e32 v73, v73
	v_exp_f32_e32 v74, v74
	v_exp_f32_e32 v75, v75
	v_pk_fma_f32 v[70:71], s[76:77], v[138:139], v[70:71]
	v_pk_mul_f32 v[72:73], v[72:73], v[142:143]
	v_pk_fma_f32 v[70:71], s[78:79], v[140:141], v[70:71]
	v_pk_fma_f32 v[142:143], v[152:153], s[44:45], v[72:73] op_sel_hi:[0, 1, 1]
	v_pk_mul_f32 v[72:73], v[74:75], v[144:145]
	v_pk_mul_f32 v[74:75], v[150:151], v[4:5] op_sel_hi:[0,1]
	v_pk_fma_f32 v[144:145], v[152:153], s[46:47], v[72:73] op_sel_hi:[0, 1, 1]
	v_pk_mul_f32 v[72:73], v[150:151], v[2:3] op_sel_hi:[0,1]
	v_exp_f32_e32 v72, v72
	v_exp_f32_e32 v73, v73
	v_exp_f32_e32 v74, v74
	v_exp_f32_e32 v75, v75
	v_pk_fma_f32 v[70:71], s[80:81], v[142:143], v[70:71]
	v_pk_mul_f32 v[72:73], v[72:73], v[146:147]
	v_pk_fma_f32 v[70:71], s[82:83], v[144:145], v[70:71]
	v_pk_fma_f32 v[146:147], v[152:153], s[48:49], v[72:73] op_sel_hi:[0, 1, 1]
	v_pk_mul_f32 v[72:73], v[74:75], v[148:149]
	v_pk_fma_f32 v[70:71], s[84:85], v[146:147], v[70:71]
	v_pk_fma_f32 v[148:149], v[152:153], s[50:51], v[72:73] op_sel_hi:[0, 1, 1]
	v_pk_fma_f32 v[70:71], s[86:87], v[148:149], v[70:71]
	s_nop 0
	v_add_f32_e32 v69, v70, v71
	v_fma_mix_f32 v69, v1, v54, v69 op_sel_hi:[0,1,0]
	s_waitcnt vmcnt(0)
	v_fma_mixlo_f16 v69, v69, v58, 0 op_sel_hi:[0,1,0]
	ds_write_b16 v68, v69 offset:4096
	global_load_dwordx4 v[50:53], v[212:213], off
	global_load_dwordx4 v[42:45], v[214:215], off
	global_load_dwordx4 v[46:49], v[216:217], off
	global_load_dwordx4 v[38:41], v[218:219], off
	global_load_dwordx4 v[30:33], v[220:221], off
	global_load_dwordx4 v[34:37], v[222:223], off
	global_load_dwordx4 v[26:29], v[224:225], off
	global_load_dwordx4 v[18:21], v[226:227], off
	global_load_dwordx4 v[22:25], v[228:229], off
	s_waitcnt lgkmcnt(0)
	s_load_dwordx16 s[36:51], s[54:55], 0x100
	s_load_dwordx16 s[72:87], s[54:55], 0x140
	v_cvt_f32_f16_sdwa v62, v62 dst_sel:DWORD dst_unused:UNUSED_PAD src0_sel:WORD_1
	v_pk_mul_f32 v[152:153], v[62:63], v[14:15] op_sel_hi:[0,1]
	v_exp_f32_e32 v152, v152
	v_exp_f32_e32 v153, v153
	v_pk_mul_f32 v[154:155], v[62:63], v[16:17] op_sel_hi:[0,1]
	v_exp_f32_e32 v154, v154
	v_exp_f32_e32 v155, v155
	v_fma_mix_f32 v150, v62, v54, 0 op_sel:[0,1,0] op_sel_hi:[0,1,0]
	v_pk_mul_f32 v[134:135], v[152:153], v[134:135]
	v_pk_fma_f32 v[134:135], v[150:151], s[56:57], v[134:135] op_sel_hi:[0, 1, 1]
	v_pk_fma_f32 v[102:103], s[88:89], v[134:135], 0 op_sel_hi:[1, 1, 0]
	v_pk_mul_f32 v[118:119], v[154:155], v[136:137]
	s_nop 0
	v_pk_fma_f32 v[136:137], v[150:151], s[58:59], v[118:119] op_sel_hi:[0, 1, 1]
	v_pk_mul_f32 v[104:105], v[62:63], v[10:11] op_sel_hi:[0,1]
	v_exp_f32_e32 v104, v104
	v_exp_f32_e32 v105, v105
	v_pk_mul_f32 v[118:119], v[62:63], v[12:13] op_sel_hi:[0,1]
	v_exp_f32_e32 v118, v118
	v_exp_f32_e32 v119, v119
	v_pk_mul_f32 v[104:105], v[104:105], v[138:139]
	v_pk_fma_f32 v[102:103], s[90:91], v[136:137], v[102:103]
	v_pk_fma_f32 v[138:139], v[150:151], s[60:61], v[104:105] op_sel_hi:[0, 1, 1]
	v_pk_mul_f32 v[104:105], v[118:119], v[140:141]
	v_pk_mul_f32 v[106:107], v[62:63], v[8:9] op_sel_hi:[0,1]
	v_pk_fma_f32 v[140:141], v[150:151], s[62:63], v[104:105] op_sel_hi:[0, 1, 1]
	v_pk_mul_f32 v[104:105], v[62:63], v[6:7] op_sel_hi:[0,1]
	v_exp_f32_e32 v104, v104
	v_exp_f32_e32 v105, v105
	v_exp_f32_e32 v106, v106
	v_exp_f32_e32 v107, v107
	v_pk_fma_f32 v[102:103], s[92:93], v[138:139], v[102:103]
	v_pk_mul_f32 v[104:105], v[104:105], v[142:143]
	v_pk_fma_f32 v[102:103], s[94:95], v[140:141], v[102:103]
	v_pk_fma_f32 v[142:143], v[150:151], s[64:65], v[104:105] op_sel_hi:[0, 1, 1]
	v_pk_mul_f32 v[104:105], v[106:107], v[144:145]
	v_pk_mul_f32 v[106:107], v[62:63], v[4:5] op_sel_hi:[0,1]
	v_pk_fma_f32 v[144:145], v[150:151], s[66:67], v[104:105] op_sel_hi:[0, 1, 1]
	v_pk_mul_f32 v[104:105], v[62:63], v[2:3] op_sel_hi:[0,1]
	v_exp_f32_e32 v104, v104
	v_exp_f32_e32 v105, v105
	v_exp_f32_e32 v106, v106
	v_exp_f32_e32 v107, v107
	v_pk_fma_f32 v[102:103], s[96:97], v[142:143], v[102:103]
	v_pk_mul_f32 v[104:105], v[104:105], v[146:147]
	v_pk_fma_f32 v[102:103], s[98:99], v[144:145], v[102:103]
	v_pk_fma_f32 v[146:147], v[150:151], s[68:69], v[104:105] op_sel_hi:[0, 1, 1]
	v_pk_mul_f32 v[104:105], v[106:107], v[148:149]
	v_pk_fma_f32 v[102:103], s[20:21], v[146:147], v[102:103]
	v_pk_fma_f32 v[148:149], v[150:151], s[70:71], v[104:105] op_sel_hi:[0, 1, 1]
	v_pk_fma_f32 v[102:103], s[22:23], v[148:149], v[102:103]
	s_nop 0
	v_add_f32_e32 v62, v102, v103
	v_fma_mix_f32 v54, v1, v54, v62 op_sel:[0,1,0] op_sel_hi:[0,1,0]
	v_fma_mixlo_f16 v54, v54, v58, 0 op_sel:[0,1,0] op_sel_hi:[0,1,0]
	ds_write_b16 v68, v54 offset:5136
	s_waitcnt lgkmcnt(0)
	s_load_dwordx16 s[56:71], s[54:55], 0x180
	s_load_dwordx8 s[88:95], s[54:55], 0x1c0
	s_load_dwordx4 s[96:99], s[54:55], 0x1e0
	s_load_dwordx4 s[20:23], s[54:55], 0x1f0
	v_cvt_f32_f16_e32 v54, v63
	v_pk_mul_f32 v[150:151], v[54:55], v[14:15] op_sel_hi:[0,1]
	v_exp_f32_e32 v150, v150
	v_exp_f32_e32 v151, v151
	v_pk_mul_f32 v[152:153], v[54:55], v[16:17] op_sel_hi:[0,1]
	v_exp_f32_e32 v152, v152
	v_exp_f32_e32 v153, v153
	v_fma_mix_f32 v58, v54, v55, 0 op_sel_hi:[0,1,0]
	v_pk_mul_f32 v[134:135], v[150:151], v[134:135]
	v_pk_fma_f32 v[134:135], v[58:59], s[36:37], v[134:135] op_sel_hi:[0, 1, 1]
	v_pk_fma_f32 v[70:71], s[72:73], v[134:135], 0 op_sel_hi:[1, 1, 0]
	v_pk_mul_f32 v[86:87], v[152:153], v[136:137]
	s_nop 0
	v_pk_fma_f32 v[136:137], v[58:59], s[38:39], v[86:87] op_sel_hi:[0, 1, 1]
	v_pk_mul_f32 v[72:73], v[54:55], v[10:11] op_sel_hi:[0,1]
	v_exp_f32_e32 v72, v72
	v_exp_f32_e32 v73, v73
	v_pk_mul_f32 v[86:87], v[54:55], v[12:13] op_sel_hi:[0,1]
	v_exp_f32_e32 v86, v86
	v_exp_f32_e32 v87, v87
	v_pk_mul_f32 v[72:73], v[72:73], v[138:139]
	v_pk_fma_f32 v[70:71], s[74:75], v[136:137], v[70:71]
	v_pk_fma_f32 v[138:139], v[58:59], s[40:41], v[72:73] op_sel_hi:[0, 1, 1]
	v_pk_mul_f32 v[72:73], v[86:87], v[140:141]
	v_pk_mul_f32 v[74:75], v[54:55], v[8:9] op_sel_hi:[0,1]
	v_pk_fma_f32 v[140:141], v[58:59], s[42:43], v[72:73] op_sel_hi:[0, 1, 1]
	v_pk_mul_f32 v[72:73], v[54:55], v[6:7] op_sel_hi:[0,1]
	v_exp_f32_e32 v72, v72
	v_exp_f32_e32 v73, v73
	v_exp_f32_e32 v74, v74
	v_exp_f32_e32 v75, v75
	v_pk_fma_f32 v[70:71], s[76:77], v[138:139], v[70:71]
	v_pk_mul_f32 v[72:73], v[72:73], v[142:143]
	v_pk_fma_f32 v[70:71], s[78:79], v[140:141], v[70:71]
	v_pk_fma_f32 v[142:143], v[58:59], s[44:45], v[72:73] op_sel_hi:[0, 1, 1]
	v_pk_mul_f32 v[72:73], v[74:75], v[144:145]
	v_pk_mul_f32 v[74:75], v[54:55], v[4:5] op_sel_hi:[0,1]
	v_pk_fma_f32 v[144:145], v[58:59], s[46:47], v[72:73] op_sel_hi:[0, 1, 1]
	v_pk_mul_f32 v[72:73], v[54:55], v[2:3] op_sel_hi:[0,1]
	v_exp_f32_e32 v72, v72
	v_exp_f32_e32 v73, v73
	v_exp_f32_e32 v74, v74
	v_exp_f32_e32 v75, v75
	v_pk_fma_f32 v[70:71], s[80:81], v[142:143], v[70:71]
	v_pk_mul_f32 v[72:73], v[72:73], v[146:147]
	v_pk_fma_f32 v[70:71], s[82:83], v[144:145], v[70:71]
	v_pk_fma_f32 v[146:147], v[58:59], s[48:49], v[72:73] op_sel_hi:[0, 1, 1]
	v_pk_mul_f32 v[72:73], v[74:75], v[148:149]
	v_pk_fma_f32 v[70:71], s[84:85], v[146:147], v[70:71]
	v_pk_fma_f32 v[148:149], v[58:59], s[50:51], v[72:73] op_sel_hi:[0, 1, 1]
	v_pk_fma_f32 v[70:71], s[86:87], v[148:149], v[70:71]
	s_nop 0
	v_add_f32_e32 v54, v70, v71
	v_fma_mix_f32 v54, v1, v55, v54 op_sel_hi:[0,1,0]
	v_fma_mixlo_f16 v54, v54, v59, 0 op_sel_hi:[0,1,0]
	ds_write_b16 v68, v54 offset:6176
	s_waitcnt lgkmcnt(0)
	s_load_dwordx16 s[36:51], s[54:55], 0x200
	s_load_dwordx16 s[72:87], s[54:55], 0x240
	v_cvt_f32_f16_sdwa v54, v63 dst_sel:DWORD dst_unused:UNUSED_PAD src0_sel:WORD_1
	v_pk_mul_f32 v[62:63], v[54:55], v[14:15] op_sel_hi:[0,1]
	v_exp_f32_e32 v62, v62
	v_exp_f32_e32 v63, v63
	v_pk_mul_f32 v[150:151], v[54:55], v[16:17] op_sel_hi:[0,1]
	v_exp_f32_e32 v150, v150
	v_exp_f32_e32 v151, v151
	v_fma_mix_f32 v58, v54, v55, 0 op_sel:[0,1,0] op_sel_hi:[0,1,0]
	v_pk_mul_f32 v[62:63], v[62:63], v[134:135]
	v_pk_fma_f32 v[62:63], v[58:59], s[56:57], v[62:63] op_sel_hi:[0, 1, 1]
	v_pk_fma_f32 v[102:103], s[88:89], v[62:63], 0 op_sel_hi:[1, 1, 0]
	v_pk_mul_f32 v[118:119], v[150:151], v[136:137]
	s_nop 0
	v_pk_fma_f32 v[134:135], v[58:59], s[58:59], v[118:119] op_sel_hi:[0, 1, 1]
	v_pk_mul_f32 v[104:105], v[54:55], v[10:11] op_sel_hi:[0,1]
	v_exp_f32_e32 v104, v104
	v_exp_f32_e32 v105, v105
	v_pk_mul_f32 v[118:119], v[54:55], v[12:13] op_sel_hi:[0,1]
	v_exp_f32_e32 v118, v118
	v_exp_f32_e32 v119, v119
	v_pk_mul_f32 v[104:105], v[104:105], v[138:139]
	v_pk_fma_f32 v[102:103], s[90:91], v[134:135], v[102:103]
	v_pk_fma_f32 v[136:137], v[58:59], s[60:61], v[104:105] op_sel_hi:[0, 1, 1]
	v_pk_mul_f32 v[104:105], v[118:119], v[140:141]
	v_pk_mul_f32 v[106:107], v[54:55], v[8:9] op_sel_hi:[0,1]
	v_pk_fma_f32 v[138:139], v[58:59], s[62:63], v[104:105] op_sel_hi:[0, 1, 1]
	v_pk_mul_f32 v[104:105], v[54:55], v[6:7] op_sel_hi:[0,1]
	v_exp_f32_e32 v104, v104
	v_exp_f32_e32 v105, v105
	v_exp_f32_e32 v106, v106
	v_exp_f32_e32 v107, v107
	v_pk_fma_f32 v[102:103], s[92:93], v[136:137], v[102:103]
	v_pk_mul_f32 v[104:105], v[104:105], v[142:143]
	v_pk_fma_f32 v[102:103], s[94:95], v[138:139], v[102:103]
	v_pk_fma_f32 v[140:141], v[58:59], s[64:65], v[104:105] op_sel_hi:[0, 1, 1]
	v_pk_mul_f32 v[104:105], v[106:107], v[144:145]
	v_pk_mul_f32 v[106:107], v[54:55], v[4:5] op_sel_hi:[0,1]
	v_pk_fma_f32 v[142:143], v[58:59], s[66:67], v[104:105] op_sel_hi:[0, 1, 1]
	v_pk_mul_f32 v[104:105], v[54:55], v[2:3] op_sel_hi:[0,1]
	v_exp_f32_e32 v104, v104
	v_exp_f32_e32 v105, v105
	v_exp_f32_e32 v106, v106
	v_exp_f32_e32 v107, v107
	v_pk_fma_f32 v[102:103], s[96:97], v[140:141], v[102:103]
	v_pk_mul_f32 v[104:105], v[104:105], v[146:147]
	v_pk_fma_f32 v[102:103], s[98:99], v[142:143], v[102:103]
	v_pk_fma_f32 v[144:145], v[58:59], s[68:69], v[104:105] op_sel_hi:[0, 1, 1]
	v_pk_mul_f32 v[104:105], v[106:107], v[148:149]
	v_pk_fma_f32 v[102:103], s[20:21], v[144:145], v[102:103]
	v_pk_fma_f32 v[146:147], v[58:59], s[70:71], v[104:105] op_sel_hi:[0, 1, 1]
	v_pk_fma_f32 v[102:103], s[22:23], v[146:147], v[102:103]
	s_nop 0
	v_add_f32_e32 v54, v102, v103
	v_fma_mix_f32 v54, v1, v55, v54 op_sel:[0,1,0] op_sel_hi:[0,1,0]
	v_fma_mixlo_f16 v54, v54, v59, 0 op_sel:[0,1,0] op_sel_hi:[0,1,0]
	ds_write_b16 v68, v54 offset:7216
	s_waitcnt lgkmcnt(0)
	s_load_dwordx16 s[56:71], s[54:55], 0x280
	s_load_dwordx8 s[88:95], s[54:55], 0x2c0
	s_load_dwordx4 s[96:99], s[54:55], 0x2e0
	s_load_dwordx4 s[20:23], s[54:55], 0x2f0
	v_cvt_f32_f16_e32 v54, v64
	v_pk_mul_f32 v[148:149], v[54:55], v[14:15] op_sel_hi:[0,1]
	v_exp_f32_e32 v148, v148
	v_exp_f32_e32 v149, v149
	v_pk_mul_f32 v[150:151], v[54:55], v[16:17] op_sel_hi:[0,1]
	v_exp_f32_e32 v150, v150
	v_exp_f32_e32 v151, v151
	v_fma_mix_f32 v58, v54, v56, 0 op_sel_hi:[0,1,0]
	v_pk_mul_f32 v[62:63], v[148:149], v[62:63]
	v_pk_fma_f32 v[62:63], v[58:59], s[36:37], v[62:63] op_sel_hi:[0, 1, 1]
	v_pk_fma_f32 v[70:71], s[72:73], v[62:63], 0 op_sel_hi:[1, 1, 0]
	v_pk_mul_f32 v[86:87], v[150:151], v[134:135]
	s_nop 0
	v_pk_fma_f32 v[134:135], v[58:59], s[38:39], v[86:87] op_sel_hi:[0, 1, 1]
	v_pk_mul_f32 v[72:73], v[54:55], v[10:11] op_sel_hi:[0,1]
	v_exp_f32_e32 v72, v72
	v_exp_f32_e32 v73, v73
	v_pk_mul_f32 v[86:87], v[54:55], v[12:13] op_sel_hi:[0,1]
	v_exp_f32_e32 v86, v86
	v_exp_f32_e32 v87, v87
	v_pk_mul_f32 v[72:73], v[72:73], v[136:137]
	v_pk_fma_f32 v[70:71], s[74:75], v[134:135], v[70:71]
	v_pk_fma_f32 v[136:137], v[58:59], s[40:41], v[72:73] op_sel_hi:[0, 1, 1]
	v_pk_mul_f32 v[72:73], v[86:87], v[138:139]
	v_pk_mul_f32 v[74:75], v[54:55], v[8:9] op_sel_hi:[0,1]
	v_pk_fma_f32 v[138:139], v[58:59], s[42:43], v[72:73] op_sel_hi:[0, 1, 1]
	v_pk_mul_f32 v[72:73], v[54:55], v[6:7] op_sel_hi:[0,1]
	v_exp_f32_e32 v72, v72
	v_exp_f32_e32 v73, v73
	v_exp_f32_e32 v74, v74
	v_exp_f32_e32 v75, v75
	v_pk_fma_f32 v[70:71], s[76:77], v[136:137], v[70:71]
	v_pk_mul_f32 v[72:73], v[72:73], v[140:141]
	v_pk_fma_f32 v[70:71], s[78:79], v[138:139], v[70:71]
	v_pk_fma_f32 v[140:141], v[58:59], s[44:45], v[72:73] op_sel_hi:[0, 1, 1]
	v_pk_mul_f32 v[72:73], v[74:75], v[142:143]
	v_pk_fma_f32 v[70:71], s[80:81], v[140:141], v[70:71]
	v_pk_fma_f32 v[142:143], v[58:59], s[46:47], v[72:73] op_sel_hi:[0, 1, 1]
	v_pk_mul_f32 v[72:73], v[54:55], v[2:3] op_sel_hi:[0,1]
	v_exp_f32_e32 v72, v72
	v_exp_f32_e32 v73, v73
	v_pk_mul_f32 v[54:55], v[54:55], v[4:5] op_sel_hi:[0,1]
	v_exp_f32_e32 v54, v54
	v_exp_f32_e32 v55, v55
	v_pk_mul_f32 v[72:73], v[72:73], v[144:145]
	v_pk_fma_f32 v[70:71], s[82:83], v[142:143], v[70:71]
	v_pk_fma_f32 v[144:145], v[58:59], s[48:49], v[72:73] op_sel_hi:[0, 1, 1]
	v_pk_mul_f32 v[54:55], v[54:55], v[146:147]
	v_pk_fma_f32 v[70:71], s[84:85], v[144:145], v[70:71]
	v_pk_fma_f32 v[54:55], v[58:59], s[50:51], v[54:55] op_sel_hi:[0, 1, 1]
	v_pk_fma_f32 v[58:59], s[86:87], v[54:55], v[70:71]
	s_nop 0
	v_add_f32_e32 v58, v58, v59
	v_fma_mix_f32 v58, v1, v56, v58 op_sel_hi:[0,1,0]
	v_fma_mixlo_f16 v58, v58, v60, 0 op_sel_hi:[0,1,0]
	ds_write_b16 v68, v58 offset:8256
	s_waitcnt lgkmcnt(0)
	s_load_dwordx16 s[36:51], s[54:55], 0x300
	s_load_dwordx16 s[72:87], s[54:55], 0x340
	v_cvt_f32_f16_sdwa v58, v64 dst_sel:DWORD dst_unused:UNUSED_PAD src0_sel:WORD_1
	v_pk_mul_f32 v[146:147], v[58:59], v[14:15] op_sel_hi:[0,1]
	v_exp_f32_e32 v146, v146
	v_exp_f32_e32 v147, v147
	v_pk_mul_f32 v[148:149], v[58:59], v[16:17] op_sel_hi:[0,1]
	v_exp_f32_e32 v148, v148
	v_exp_f32_e32 v149, v149
	v_fma_mix_f32 v64, v58, v56, 0 op_sel:[0,1,0] op_sel_hi:[0,1,0]
	v_pk_mul_f32 v[62:63], v[146:147], v[62:63]
	v_pk_fma_f32 v[62:63], v[64:65], s[56:57], v[62:63] op_sel_hi:[0, 1, 1]
	v_pk_fma_f32 v[102:103], s[88:89], v[62:63], 0 op_sel_hi:[1, 1, 0]
	v_pk_mul_f32 v[118:119], v[148:149], v[134:135]
	s_nop 0
	v_pk_fma_f32 v[134:135], v[64:65], s[58:59], v[118:119] op_sel_hi:[0, 1, 1]
	v_pk_mul_f32 v[104:105], v[58:59], v[10:11] op_sel_hi:[0,1]
	v_exp_f32_e32 v104, v104
	v_exp_f32_e32 v105, v105
	v_pk_mul_f32 v[118:119], v[58:59], v[12:13] op_sel_hi:[0,1]
	v_exp_f32_e32 v118, v118
	v_exp_f32_e32 v119, v119
	v_pk_mul_f32 v[104:105], v[104:105], v[136:137]
	v_pk_fma_f32 v[102:103], s[90:91], v[134:135], v[102:103]
	v_pk_fma_f32 v[136:137], v[64:65], s[60:61], v[104:105] op_sel_hi:[0, 1, 1]
	v_pk_mul_f32 v[104:105], v[118:119], v[138:139]
	v_pk_mul_f32 v[106:107], v[58:59], v[8:9] op_sel_hi:[0,1]
	v_pk_fma_f32 v[138:139], v[64:65], s[62:63], v[104:105] op_sel_hi:[0, 1, 1]
	v_pk_mul_f32 v[104:105], v[58:59], v[6:7] op_sel_hi:[0,1]
	v_exp_f32_e32 v104, v104
	v_exp_f32_e32 v105, v105
	v_exp_f32_e32 v106, v106
	v_exp_f32_e32 v107, v107
	v_pk_fma_f32 v[102:103], s[92:93], v[136:137], v[102:103]
	v_pk_mul_f32 v[104:105], v[104:105], v[140:141]
	v_pk_fma_f32 v[102:103], s[94:95], v[138:139], v[102:103]
	v_pk_fma_f32 v[140:141], v[64:65], s[64:65], v[104:105] op_sel_hi:[0, 1, 1]
	v_pk_mul_f32 v[104:105], v[106:107], v[142:143]
	v_pk_fma_f32 v[102:103], s[96:97], v[140:141], v[102:103]
	v_pk_fma_f32 v[142:143], v[64:65], s[66:67], v[104:105] op_sel_hi:[0, 1, 1]
	v_pk_mul_f32 v[104:105], v[58:59], v[2:3] op_sel_hi:[0,1]
	v_exp_f32_e32 v104, v104
	v_exp_f32_e32 v105, v105
	v_pk_mul_f32 v[58:59], v[58:59], v[4:5] op_sel_hi:[0,1]
	v_exp_f32_e32 v58, v58
	v_exp_f32_e32 v59, v59
	v_pk_mul_f32 v[104:105], v[104:105], v[144:145]
	v_pk_fma_f32 v[102:103], s[98:99], v[142:143], v[102:103]
	v_pk_fma_f32 v[144:145], v[64:65], s[68:69], v[104:105] op_sel_hi:[0, 1, 1]
	v_pk_mul_f32 v[54:55], v[58:59], v[54:55]
	v_pk_fma_f32 v[102:103], s[20:21], v[144:145], v[102:103]
	v_pk_fma_f32 v[54:55], v[64:65], s[70:71], v[54:55] op_sel_hi:[0, 1, 1]
	v_pk_fma_f32 v[58:59], s[22:23], v[54:55], v[102:103]
	s_nop 0
	v_add_f32_e32 v58, v58, v59
	v_fma_mix_f32 v56, v1, v56, v58 op_sel:[0,1,0] op_sel_hi:[0,1,0]
	v_fma_mixlo_f16 v56, v56, v60, 0 op_sel:[0,1,0] op_sel_hi:[0,1,0]
	ds_write_b16 v68, v56 offset:9296
	s_waitcnt lgkmcnt(0)
	s_load_dwordx16 s[56:71], s[54:55], 0x380
	s_load_dwordx8 s[88:95], s[54:55], 0x3c0
	s_load_dwordx4 s[96:99], s[54:55], 0x3e0
	s_load_dwordx4 s[20:23], s[54:55], 0x3f0
	v_cvt_f32_f16_e32 v56, v65
	v_pk_mul_f32 v[146:147], v[56:57], v[14:15] op_sel_hi:[0,1]
	v_exp_f32_e32 v146, v146
	v_exp_f32_e32 v147, v147
	v_pk_mul_f32 v[148:149], v[56:57], v[16:17] op_sel_hi:[0,1]
	v_exp_f32_e32 v148, v148
	v_exp_f32_e32 v149, v149
	v_fma_mix_f32 v58, v56, v57, 0 op_sel_hi:[0,1,0]
	v_pk_mul_f32 v[62:63], v[146:147], v[62:63]
	v_pk_fma_f32 v[62:63], v[58:59], s[36:37], v[62:63] op_sel_hi:[0, 1, 1]
	v_pk_fma_f32 v[70:71], s[72:73], v[62:63], 0 op_sel_hi:[1, 1, 0]
	v_pk_mul_f32 v[86:87], v[148:149], v[134:135]
	s_nop 0
	v_pk_fma_f32 v[134:135], v[58:59], s[38:39], v[86:87] op_sel_hi:[0, 1, 1]
	v_pk_mul_f32 v[72:73], v[56:57], v[10:11] op_sel_hi:[0,1]
	v_exp_f32_e32 v72, v72
	v_exp_f32_e32 v73, v73
	v_pk_mul_f32 v[86:87], v[56:57], v[12:13] op_sel_hi:[0,1]
	v_exp_f32_e32 v86, v86
	v_exp_f32_e32 v87, v87
	v_pk_mul_f32 v[72:73], v[72:73], v[136:137]
	v_pk_fma_f32 v[70:71], s[74:75], v[134:135], v[70:71]
	v_pk_fma_f32 v[136:137], v[58:59], s[40:41], v[72:73] op_sel_hi:[0, 1, 1]
	v_pk_mul_f32 v[72:73], v[86:87], v[138:139]
	v_pk_mul_f32 v[74:75], v[56:57], v[8:9] op_sel_hi:[0,1]
	v_pk_fma_f32 v[138:139], v[58:59], s[42:43], v[72:73] op_sel_hi:[0, 1, 1]
	v_pk_mul_f32 v[72:73], v[56:57], v[6:7] op_sel_hi:[0,1]
	v_exp_f32_e32 v72, v72
	v_exp_f32_e32 v73, v73
	v_exp_f32_e32 v74, v74
	v_exp_f32_e32 v75, v75
	v_pk_fma_f32 v[70:71], s[76:77], v[136:137], v[70:71]
	v_pk_mul_f32 v[72:73], v[72:73], v[140:141]
	v_pk_fma_f32 v[70:71], s[78:79], v[138:139], v[70:71]
	v_pk_fma_f32 v[140:141], v[58:59], s[44:45], v[72:73] op_sel_hi:[0, 1, 1]
	v_pk_mul_f32 v[72:73], v[74:75], v[142:143]
	v_pk_mul_f32 v[74:75], v[56:57], v[4:5] op_sel_hi:[0,1]
	v_pk_fma_f32 v[142:143], v[58:59], s[46:47], v[72:73] op_sel_hi:[0, 1, 1]
	v_pk_mul_f32 v[72:73], v[56:57], v[2:3] op_sel_hi:[0,1]
	v_exp_f32_e32 v72, v72
	v_exp_f32_e32 v73, v73
	v_exp_f32_e32 v74, v74
	v_exp_f32_e32 v75, v75
	v_pk_fma_f32 v[70:71], s[80:81], v[140:141], v[70:71]
	v_pk_mul_f32 v[72:73], v[72:73], v[144:145]
	v_pk_fma_f32 v[70:71], s[82:83], v[142:143], v[70:71]
	v_pk_fma_f32 v[144:145], v[58:59], s[48:49], v[72:73] op_sel_hi:[0, 1, 1]
	v_pk_mul_f32 v[54:55], v[74:75], v[54:55]
	v_pk_fma_f32 v[70:71], s[84:85], v[144:145], v[70:71]
	v_pk_fma_f32 v[54:55], v[58:59], s[50:51], v[54:55] op_sel_hi:[0, 1, 1]
	v_pk_fma_f32 v[58:59], s[86:87], v[54:55], v[70:71]
	s_nop 0
	v_add_f32_e32 v56, v58, v59
	v_fma_mix_f32 v56, v1, v57, v56 op_sel_hi:[0,1,0]
	v_fma_mixlo_f16 v56, v56, v61, 0 op_sel_hi:[0,1,0]
	ds_write_b16 v68, v56 offset:10336
	s_waitcnt lgkmcnt(0)
	s_load_dwordx16 s[36:51], s[54:55], 0x400
	s_load_dwordx16 s[72:87], s[54:55], 0x440
	v_cvt_f32_f16_sdwa v56, v65 dst_sel:DWORD dst_unused:UNUSED_PAD src0_sel:WORD_1
	v_pk_mul_f32 v[64:65], v[56:57], v[14:15] op_sel_hi:[0,1]
	v_pk_mul_f32 v[146:147], v[56:57], v[16:17] op_sel_hi:[0,1]
	v_exp_f32_e32 v64, v64
	v_exp_f32_e32 v65, v65
	v_exp_f32_e32 v146, v146
	v_exp_f32_e32 v147, v147
	v_fma_mix_f32 v58, v56, v57, 0 op_sel:[0,1,0] op_sel_hi:[0,1,0]
	v_pk_mul_f32 v[62:63], v[64:65], v[62:63]
	v_pk_mul_f32 v[64:65], v[146:147], v[134:135]
	v_pk_fma_f32 v[134:135], v[58:59], s[58:59], v[64:65] op_sel_hi:[0, 1, 1]
	v_pk_mul_f32 v[64:65], v[56:57], v[10:11] op_sel_hi:[0,1]
	v_pk_fma_f32 v[148:149], v[58:59], s[56:57], v[62:63] op_sel_hi:[0, 1, 1]
	v_exp_f32_e32 v64, v64
	v_exp_f32_e32 v65, v65
	v_pk_mul_f32 v[102:103], v[56:57], v[12:13] op_sel_hi:[0,1]
	v_exp_f32_e32 v102, v102
	v_exp_f32_e32 v103, v103
	v_pk_fma_f32 v[62:63], s[88:89], v[148:149], 0 op_sel_hi:[1, 1, 0]
	v_pk_mul_f32 v[64:65], v[64:65], v[136:137]
	v_pk_fma_f32 v[62:63], s[90:91], v[134:135], v[62:63]
	v_pk_fma_f32 v[136:137], v[58:59], s[60:61], v[64:65] op_sel_hi:[0, 1, 1]
	v_pk_mul_f32 v[64:65], v[102:103], v[138:139]
	v_pk_fma_f32 v[62:63], s[92:93], v[136:137], v[62:63]
	v_pk_fma_f32 v[122:123], v[58:59], s[62:63], v[64:65] op_sel_hi:[0, 1, 1]
	v_pk_mul_f32 v[64:65], v[56:57], v[6:7] op_sel_hi:[0,1]
	v_exp_f32_e32 v64, v64
	v_exp_f32_e32 v65, v65
	v_pk_mul_f32 v[102:103], v[56:57], v[8:9] op_sel_hi:[0,1]
	v_exp_f32_e32 v102, v102
	v_exp_f32_e32 v103, v103
	v_pk_mul_f32 v[64:65], v[64:65], v[140:141]
	v_pk_fma_f32 v[62:63], s[94:95], v[122:123], v[62:63]
	v_pk_fma_f32 v[124:125], v[58:59], s[64:65], v[64:65] op_sel_hi:[0, 1, 1]
	v_pk_mul_f32 v[64:65], v[102:103], v[142:143]
	v_pk_fma_f32 v[62:63], s[96:97], v[124:125], v[62:63]
	v_pk_fma_f32 v[126:127], v[58:59], s[66:67], v[64:65] op_sel_hi:[0, 1, 1]
	v_pk_mul_f32 v[64:65], v[56:57], v[2:3] op_sel_hi:[0,1]
	v_exp_f32_e32 v64, v64
	v_exp_f32_e32 v65, v65
	v_pk_mul_f32 v[102:103], v[56:57], v[4:5] op_sel_hi:[0,1]
	v_exp_f32_e32 v102, v102
	v_exp_f32_e32 v103, v103
	v_pk_mul_f32 v[64:65], v[64:65], v[144:145]
	v_pk_fma_f32 v[62:63], s[98:99], v[126:127], v[62:63]
	v_pk_fma_f32 v[128:129], v[58:59], s[68:69], v[64:65] op_sel_hi:[0, 1, 1]
	v_pk_mul_f32 v[54:55], v[102:103], v[54:55]
	v_pk_fma_f32 v[62:63], s[20:21], v[128:129], v[62:63]
	v_pk_fma_f32 v[130:131], v[58:59], s[70:71], v[54:55] op_sel_hi:[0, 1, 1]
	v_pk_fma_f32 v[54:55], s[22:23], v[130:131], v[62:63]
	s_nop 0
	v_add_f32_e32 v54, v54, v55
	v_fma_mix_f32 v54, v1, v57, v54 op_sel:[0,1,0] op_sel_hi:[0,1,0]
	v_fma_mixlo_f16 v54, v54, v61, 0 op_sel:[0,1,0] op_sel_hi:[0,1,0]
	ds_write_b16 v68, v54 offset:11376
	s_waitcnt lgkmcnt(0)
	s_load_dwordx16 s[56:71], s[54:55], 0x480
	s_load_dwordx8 s[88:95], s[54:55], 0x4c0
	s_load_dwordx4 s[96:99], s[54:55], 0x4e0
	s_load_dwordx4 s[20:23], s[54:55], 0x4f0
	s_waitcnt vmcnt(8)
	v_cvt_f32_f16_e32 v132, v50
	s_waitcnt vmcnt(7)
	v_pk_mul_f32 v[140:141], v[132:133], v[14:15] op_sel_hi:[0,1]
	v_exp_f32_e32 v140, v140
	v_exp_f32_e32 v141, v141
	v_pk_mul_f32 v[142:143], v[132:133], v[16:17] op_sel_hi:[0,1]
	v_exp_f32_e32 v142, v142
	v_exp_f32_e32 v143, v143
	v_fma_mix_f32 v138, v132, v42, 0 op_sel_hi:[0,1,0]
	v_pk_mul_f32 v[140:141], v[140:141], v[148:149]
	v_pk_fma_f32 v[140:141], v[138:139], s[36:37], v[140:141] op_sel_hi:[0, 1, 1]
	v_pk_fma_f32 v[70:71], s[72:73], v[140:141], 0 op_sel_hi:[1, 1, 0]
	v_pk_mul_f32 v[86:87], v[142:143], v[134:135]
	s_nop 0
	v_pk_fma_f32 v[134:135], v[138:139], s[38:39], v[86:87] op_sel_hi:[0, 1, 1]
	v_pk_mul_f32 v[72:73], v[132:133], v[10:11] op_sel_hi:[0,1]
	v_exp_f32_e32 v72, v72
	v_exp_f32_e32 v73, v73
	v_pk_mul_f32 v[86:87], v[132:133], v[12:13] op_sel_hi:[0,1]
	v_exp_f32_e32 v86, v86
	v_exp_f32_e32 v87, v87
	v_pk_mul_f32 v[72:73], v[72:73], v[136:137]
	v_pk_fma_f32 v[70:71], s[74:75], v[134:135], v[70:71]
	v_pk_fma_f32 v[136:137], v[138:139], s[40:41], v[72:73] op_sel_hi:[0, 1, 1]
	v_pk_mul_f32 v[72:73], v[86:87], v[122:123]
	v_pk_mul_f32 v[74:75], v[132:133], v[8:9] op_sel_hi:[0,1]
	v_pk_fma_f32 v[122:123], v[138:139], s[42:43], v[72:73] op_sel_hi:[0, 1, 1]
	v_pk_mul_f32 v[72:73], v[132:133], v[6:7] op_sel_hi:[0,1]
	v_exp_f32_e32 v72, v72
	v_exp_f32_e32 v73, v73
	v_exp_f32_e32 v74, v74
	v_exp_f32_e32 v75, v75
	v_pk_fma_f32 v[70:71], s[76:77], v[136:137], v[70:71]
	v_pk_mul_f32 v[72:73], v[72:73], v[124:125]
	v_pk_fma_f32 v[70:71], s[78:79], v[122:123], v[70:71]
	v_pk_fma_f32 v[124:125], v[138:139], s[44:45], v[72:73] op_sel_hi:[0, 1, 1]
	v_pk_mul_f32 v[72:73], v[74:75], v[126:127]
	v_pk_mul_f32 v[74:75], v[132:133], v[4:5] op_sel_hi:[0,1]
	v_pk_fma_f32 v[126:127], v[138:139], s[46:47], v[72:73] op_sel_hi:[0, 1, 1]
	v_pk_mul_f32 v[72:73], v[132:133], v[2:3] op_sel_hi:[0,1]
	v_exp_f32_e32 v72, v72
	v_exp_f32_e32 v73, v73
	v_exp_f32_e32 v74, v74
	v_exp_f32_e32 v75, v75
	v_pk_fma_f32 v[70:71], s[80:81], v[124:125], v[70:71]
	v_pk_mul_f32 v[72:73], v[72:73], v[128:129]
	v_pk_fma_f32 v[70:71], s[82:83], v[126:127], v[70:71]
	v_pk_fma_f32 v[128:129], v[138:139], s[48:49], v[72:73] op_sel_hi:[0, 1, 1]
	v_pk_mul_f32 v[72:73], v[74:75], v[130:131]
	v_pk_fma_f32 v[70:71], s[84:85], v[128:129], v[70:71]
	v_pk_fma_f32 v[130:131], v[138:139], s[50:51], v[72:73] op_sel_hi:[0, 1, 1]
	v_pk_fma_f32 v[70:71], s[86:87], v[130:131], v[70:71]
	s_nop 0
	v_add_f32_e32 v69, v70, v71
	v_fma_mix_f32 v69, v1, v42, v69 op_sel_hi:[0,1,0]
	s_waitcnt vmcnt(6)
	v_fma_mixlo_f16 v69, v69, v46, 0 op_sel_hi:[0,1,0]
	ds_write_b16 v68, v69 offset:12416
	s_waitcnt lgkmcnt(0)
	s_load_dwordx16 s[36:51], s[54:55], 0x500
	s_load_dwordx16 s[72:87], s[54:55], 0x540
	v_cvt_f32_f16_sdwa v50, v50 dst_sel:DWORD dst_unused:UNUSED_PAD src0_sel:WORD_1
	v_pk_mul_f32 v[138:139], v[50:51], v[14:15] op_sel_hi:[0,1]
	v_exp_f32_e32 v138, v138
	v_exp_f32_e32 v139, v139
	v_pk_mul_f32 v[142:143], v[50:51], v[16:17] op_sel_hi:[0,1]
	v_exp_f32_e32 v142, v142
	v_exp_f32_e32 v143, v143
	v_fma_mix_f32 v132, v50, v42, 0 op_sel:[0,1,0] op_sel_hi:[0,1,0]
	v_pk_mul_f32 v[138:139], v[138:139], v[140:141]
	v_pk_fma_f32 v[138:139], v[132:133], s[56:57], v[138:139] op_sel_hi:[0, 1, 1]
	v_pk_fma_f32 v[54:55], s[88:89], v[138:139], 0 op_sel_hi:[1, 1, 0]
	v_pk_mul_f32 v[106:107], v[142:143], v[134:135]
	s_nop 0
	v_pk_fma_f32 v[134:135], v[132:133], s[58:59], v[106:107] op_sel_hi:[0, 1, 1]
	v_pk_mul_f32 v[56:57], v[50:51], v[10:11] op_sel_hi:[0,1]
	v_exp_f32_e32 v56, v56
	v_exp_f32_e32 v57, v57
	v_pk_mul_f32 v[106:107], v[50:51], v[12:13] op_sel_hi:[0,1]
	v_exp_f32_e32 v106, v106
	v_exp_f32_e32 v107, v107
	v_pk_mul_f32 v[56:57], v[56:57], v[136:137]
	v_pk_fma_f32 v[54:55], s[90:91], v[134:135], v[54:55]
	v_pk_fma_f32 v[136:137], v[132:133], s[60:61], v[56:57] op_sel_hi:[0, 1, 1]
	v_pk_mul_f32 v[56:57], v[106:107], v[122:123]
	v_pk_mul_f32 v[58:59], v[50:51], v[8:9] op_sel_hi:[0,1]
	v_pk_fma_f32 v[122:123], v[132:133], s[62:63], v[56:57] op_sel_hi:[0, 1, 1]
	v_pk_mul_f32 v[56:57], v[50:51], v[6:7] op_sel_hi:[0,1]
	v_exp_f32_e32 v56, v56
	v_exp_f32_e32 v57, v57
	v_exp_f32_e32 v58, v58
	v_exp_f32_e32 v59, v59
	v_pk_fma_f32 v[54:55], s[92:93], v[136:137], v[54:55]
	v_pk_mul_f32 v[56:57], v[56:57], v[124:125]
	v_pk_fma_f32 v[54:55], s[94:95], v[122:123], v[54:55]
	v_pk_fma_f32 v[124:125], v[132:133], s[64:65], v[56:57] op_sel_hi:[0, 1, 1]
	v_pk_mul_f32 v[56:57], v[58:59], v[126:127]
	v_pk_mul_f32 v[58:59], v[50:51], v[4:5] op_sel_hi:[0,1]
	v_pk_fma_f32 v[126:127], v[132:133], s[66:67], v[56:57] op_sel_hi:[0, 1, 1]
	v_pk_mul_f32 v[56:57], v[50:51], v[2:3] op_sel_hi:[0,1]
	v_exp_f32_e32 v56, v56
	v_exp_f32_e32 v57, v57
	v_exp_f32_e32 v58, v58
	v_exp_f32_e32 v59, v59
	v_pk_fma_f32 v[54:55], s[96:97], v[124:125], v[54:55]
	v_pk_mul_f32 v[56:57], v[56:57], v[128:129]
	v_pk_fma_f32 v[54:55], s[98:99], v[126:127], v[54:55]
	v_pk_fma_f32 v[128:129], v[132:133], s[68:69], v[56:57] op_sel_hi:[0, 1, 1]
	v_pk_mul_f32 v[56:57], v[58:59], v[130:131]
	v_pk_fma_f32 v[54:55], s[20:21], v[128:129], v[54:55]
	v_pk_fma_f32 v[130:131], v[132:133], s[70:71], v[56:57] op_sel_hi:[0, 1, 1]
	v_pk_fma_f32 v[54:55], s[22:23], v[130:131], v[54:55]
	s_nop 0
	v_add_f32_e32 v50, v54, v55
	v_fma_mix_f32 v42, v1, v42, v50 op_sel:[0,1,0] op_sel_hi:[0,1,0]
	v_fma_mixlo_f16 v42, v42, v46, 0 op_sel:[0,1,0] op_sel_hi:[0,1,0]
	ds_write_b16 v68, v42 offset:13456
	s_waitcnt lgkmcnt(0)
	s_load_dwordx16 s[56:71], s[54:55], 0x580
	s_load_dwordx8 s[88:95], s[54:55], 0x5c0
	s_load_dwordx4 s[96:99], s[54:55], 0x5e0
	s_load_dwordx4 s[20:23], s[54:55], 0x5f0
	v_cvt_f32_f16_e32 v42, v51
	v_pk_mul_f32 v[132:133], v[42:43], v[14:15] op_sel_hi:[0,1]
	v_exp_f32_e32 v132, v132
	v_exp_f32_e32 v133, v133
	v_pk_mul_f32 v[140:141], v[42:43], v[16:17] op_sel_hi:[0,1]
	v_exp_f32_e32 v140, v140
	v_exp_f32_e32 v141, v141
	v_fma_mix_f32 v46, v42, v43, 0 op_sel_hi:[0,1,0]
	v_pk_mul_f32 v[132:133], v[132:133], v[138:139]
	v_pk_fma_f32 v[132:133], v[46:47], s[36:37], v[132:133] op_sel_hi:[0, 1, 1]
	v_pk_fma_f32 v[70:71], s[72:73], v[132:133], 0 op_sel_hi:[1, 1, 0]
	v_pk_mul_f32 v[86:87], v[140:141], v[134:135]
	s_nop 0
	v_pk_fma_f32 v[134:135], v[46:47], s[38:39], v[86:87] op_sel_hi:[0, 1, 1]
	v_pk_mul_f32 v[72:73], v[42:43], v[10:11] op_sel_hi:[0,1]
	v_exp_f32_e32 v72, v72
	v_exp_f32_e32 v73, v73
	v_pk_mul_f32 v[86:87], v[42:43], v[12:13] op_sel_hi:[0,1]
	v_exp_f32_e32 v86, v86
	v_exp_f32_e32 v87, v87
	v_pk_mul_f32 v[72:73], v[72:73], v[136:137]
	v_pk_fma_f32 v[70:71], s[74:75], v[134:135], v[70:71]
	v_pk_fma_f32 v[136:137], v[46:47], s[40:41], v[72:73] op_sel_hi:[0, 1, 1]
	v_pk_mul_f32 v[72:73], v[86:87], v[122:123]
	v_pk_mul_f32 v[74:75], v[42:43], v[8:9] op_sel_hi:[0,1]
	v_pk_fma_f32 v[122:123], v[46:47], s[42:43], v[72:73] op_sel_hi:[0, 1, 1]
	v_pk_mul_f32 v[72:73], v[42:43], v[6:7] op_sel_hi:[0,1]
	v_exp_f32_e32 v72, v72
	v_exp_f32_e32 v73, v73
	v_exp_f32_e32 v74, v74
	v_exp_f32_e32 v75, v75
	v_pk_fma_f32 v[70:71], s[76:77], v[136:137], v[70:71]
	v_pk_mul_f32 v[72:73], v[72:73], v[124:125]
	v_pk_fma_f32 v[70:71], s[78:79], v[122:123], v[70:71]
	v_pk_fma_f32 v[124:125], v[46:47], s[44:45], v[72:73] op_sel_hi:[0, 1, 1]
	v_pk_mul_f32 v[72:73], v[74:75], v[126:127]
	v_pk_mul_f32 v[74:75], v[42:43], v[4:5] op_sel_hi:[0,1]
	v_pk_fma_f32 v[126:127], v[46:47], s[46:47], v[72:73] op_sel_hi:[0, 1, 1]
	v_pk_mul_f32 v[72:73], v[42:43], v[2:3] op_sel_hi:[0,1]
	v_exp_f32_e32 v72, v72
	v_exp_f32_e32 v73, v73
	v_exp_f32_e32 v74, v74
	v_exp_f32_e32 v75, v75
	v_pk_fma_f32 v[70:71], s[80:81], v[124:125], v[70:71]
	v_pk_mul_f32 v[72:73], v[72:73], v[128:129]
	v_pk_fma_f32 v[70:71], s[82:83], v[126:127], v[70:71]
	v_pk_fma_f32 v[128:129], v[46:47], s[48:49], v[72:73] op_sel_hi:[0, 1, 1]
	v_pk_mul_f32 v[72:73], v[74:75], v[130:131]
	v_pk_fma_f32 v[70:71], s[84:85], v[128:129], v[70:71]
	v_pk_fma_f32 v[130:131], v[46:47], s[50:51], v[72:73] op_sel_hi:[0, 1, 1]
	v_pk_fma_f32 v[70:71], s[86:87], v[130:131], v[70:71]
	s_nop 0
	v_add_f32_e32 v42, v70, v71
	v_fma_mix_f32 v42, v1, v43, v42 op_sel_hi:[0,1,0]
	v_fma_mixlo_f16 v42, v42, v47, 0 op_sel_hi:[0,1,0]
	ds_write_b16 v68, v42 offset:14496
	s_waitcnt lgkmcnt(0)
	s_load_dwordx16 s[36:51], s[54:55], 0x600
	s_load_dwordx16 s[72:87], s[54:55], 0x640
	v_cvt_f32_f16_sdwa v42, v51 dst_sel:DWORD dst_unused:UNUSED_PAD src0_sel:WORD_1
	v_pk_mul_f32 v[50:51], v[42:43], v[14:15] op_sel_hi:[0,1]
	v_exp_f32_e32 v50, v50
	v_exp_f32_e32 v51, v51
	v_pk_mul_f32 v[138:139], v[42:43], v[16:17] op_sel_hi:[0,1]
	v_exp_f32_e32 v138, v138
	v_exp_f32_e32 v139, v139
	v_fma_mix_f32 v46, v42, v43, 0 op_sel:[0,1,0] op_sel_hi:[0,1,0]
	v_pk_mul_f32 v[50:51], v[50:51], v[132:133]
	v_pk_fma_f32 v[50:51], v[46:47], s[56:57], v[50:51] op_sel_hi:[0, 1, 1]
	v_pk_fma_f32 v[54:55], s[88:89], v[50:51], 0 op_sel_hi:[1, 1, 0]
	v_pk_mul_f32 v[106:107], v[138:139], v[134:135]
	s_nop 0
	v_pk_fma_f32 v[132:133], v[46:47], s[58:59], v[106:107] op_sel_hi:[0, 1, 1]
	v_pk_mul_f32 v[56:57], v[42:43], v[10:11] op_sel_hi:[0,1]
	v_exp_f32_e32 v56, v56
	v_exp_f32_e32 v57, v57
	v_pk_mul_f32 v[106:107], v[42:43], v[12:13] op_sel_hi:[0,1]
	v_exp_f32_e32 v106, v106
	v_exp_f32_e32 v107, v107
	v_pk_mul_f32 v[56:57], v[56:57], v[136:137]
	v_pk_fma_f32 v[54:55], s[90:91], v[132:133], v[54:55]
	v_pk_fma_f32 v[134:135], v[46:47], s[60:61], v[56:57] op_sel_hi:[0, 1, 1]
	v_pk_mul_f32 v[56:57], v[106:107], v[122:123]
	v_pk_mul_f32 v[58:59], v[42:43], v[8:9] op_sel_hi:[0,1]
	v_pk_fma_f32 v[122:123], v[46:47], s[62:63], v[56:57] op_sel_hi:[0, 1, 1]
	v_pk_mul_f32 v[56:57], v[42:43], v[6:7] op_sel_hi:[0,1]
	v_exp_f32_e32 v56, v56
	v_exp_f32_e32 v57, v57
	v_exp_f32_e32 v58, v58
	v_exp_f32_e32 v59, v59
	v_pk_fma_f32 v[54:55], s[92:93], v[134:135], v[54:55]
	v_pk_mul_f32 v[56:57], v[56:57], v[124:125]
	v_pk_fma_f32 v[54:55], s[94:95], v[122:123], v[54:55]
	v_pk_fma_f32 v[124:125], v[46:47], s[64:65], v[56:57] op_sel_hi:[0, 1, 1]
	v_pk_mul_f32 v[56:57], v[58:59], v[126:127]
	v_pk_mul_f32 v[58:59], v[42:43], v[4:5] op_sel_hi:[0,1]
	v_pk_fma_f32 v[126:127], v[46:47], s[66:67], v[56:57] op_sel_hi:[0, 1, 1]
	v_pk_mul_f32 v[56:57], v[42:43], v[2:3] op_sel_hi:[0,1]
	v_exp_f32_e32 v56, v56
	v_exp_f32_e32 v57, v57
	v_exp_f32_e32 v58, v58
	v_exp_f32_e32 v59, v59
	v_pk_fma_f32 v[54:55], s[96:97], v[124:125], v[54:55]
	v_pk_mul_f32 v[56:57], v[56:57], v[128:129]
	v_pk_fma_f32 v[54:55], s[98:99], v[126:127], v[54:55]
	v_pk_fma_f32 v[128:129], v[46:47], s[68:69], v[56:57] op_sel_hi:[0, 1, 1]
	v_pk_mul_f32 v[56:57], v[58:59], v[130:131]
	v_pk_fma_f32 v[54:55], s[20:21], v[128:129], v[54:55]
	v_pk_fma_f32 v[130:131], v[46:47], s[70:71], v[56:57] op_sel_hi:[0, 1, 1]
	v_pk_fma_f32 v[54:55], s[22:23], v[130:131], v[54:55]
	s_nop 0
	v_add_f32_e32 v42, v54, v55
	v_fma_mix_f32 v42, v1, v43, v42 op_sel:[0,1,0] op_sel_hi:[0,1,0]
	v_fma_mixlo_f16 v42, v42, v47, 0 op_sel:[0,1,0] op_sel_hi:[0,1,0]
	ds_write_b16 v68, v42 offset:15536
	s_waitcnt lgkmcnt(0)
	s_load_dwordx16 s[56:71], s[54:55], 0x680
	s_load_dwordx8 s[88:95], s[54:55], 0x6c0
	s_load_dwordx4 s[96:99], s[54:55], 0x6e0
	s_load_dwordx4 s[20:23], s[54:55], 0x6f0
	v_cvt_f32_f16_e32 v42, v52
	v_pk_mul_f32 v[136:137], v[42:43], v[14:15] op_sel_hi:[0,1]
	v_exp_f32_e32 v136, v136
	v_exp_f32_e32 v137, v137
	v_pk_mul_f32 v[138:139], v[42:43], v[16:17] op_sel_hi:[0,1]
	v_exp_f32_e32 v138, v138
	v_exp_f32_e32 v139, v139
	v_fma_mix_f32 v46, v42, v44, 0 op_sel_hi:[0,1,0]
	v_pk_mul_f32 v[50:51], v[136:137], v[50:51]
	v_pk_fma_f32 v[50:51], v[46:47], s[36:37], v[50:51] op_sel_hi:[0, 1, 1]
	v_pk_fma_f32 v[70:71], s[72:73], v[50:51], 0 op_sel_hi:[1, 1, 0]
	v_pk_mul_f32 v[86:87], v[138:139], v[132:133]
	s_nop 0
	v_pk_fma_f32 v[132:133], v[46:47], s[38:39], v[86:87] op_sel_hi:[0, 1, 1]
	v_pk_mul_f32 v[72:73], v[42:43], v[10:11] op_sel_hi:[0,1]
	v_exp_f32_e32 v72, v72
	v_exp_f32_e32 v73, v73
	v_pk_mul_f32 v[86:87], v[42:43], v[12:13] op_sel_hi:[0,1]
	v_exp_f32_e32 v86, v86
	v_exp_f32_e32 v87, v87
	v_pk_mul_f32 v[72:73], v[72:73], v[134:135]
	v_pk_fma_f32 v[70:71], s[74:75], v[132:133], v[70:71]
	v_pk_fma_f32 v[134:135], v[46:47], s[40:41], v[72:73] op_sel_hi:[0, 1, 1]
	v_pk_mul_f32 v[72:73], v[86:87], v[122:123]
	v_pk_mul_f32 v[74:75], v[42:43], v[8:9] op_sel_hi:[0,1]
	v_pk_fma_f32 v[122:123], v[46:47], s[42:43], v[72:73] op_sel_hi:[0, 1, 1]
	v_pk_mul_f32 v[72:73], v[42:43], v[6:7] op_sel_hi:[0,1]
	v_exp_f32_e32 v72, v72
	v_exp_f32_e32 v73, v73
	v_exp_f32_e32 v74, v74
	v_exp_f32_e32 v75, v75
	v_pk_fma_f32 v[70:71], s[76:77], v[134:135], v[70:71]
	v_pk_mul_f32 v[72:73], v[72:73], v[124:125]
	v_pk_fma_f32 v[70:71], s[78:79], v[122:123], v[70:71]
	v_pk_fma_f32 v[124:125], v[46:47], s[44:45], v[72:73] op_sel_hi:[0, 1, 1]
	v_pk_mul_f32 v[72:73], v[74:75], v[126:127]
	v_pk_fma_f32 v[70:71], s[80:81], v[124:125], v[70:71]
	v_pk_fma_f32 v[126:127], v[46:47], s[46:47], v[72:73] op_sel_hi:[0, 1, 1]
	v_pk_mul_f32 v[72:73], v[42:43], v[2:3] op_sel_hi:[0,1]
	v_exp_f32_e32 v72, v72
	v_exp_f32_e32 v73, v73
	v_pk_mul_f32 v[42:43], v[42:43], v[4:5] op_sel_hi:[0,1]
	v_exp_f32_e32 v42, v42
	v_exp_f32_e32 v43, v43
	v_pk_mul_f32 v[72:73], v[72:73], v[128:129]
	v_pk_fma_f32 v[70:71], s[82:83], v[126:127], v[70:71]
	v_pk_fma_f32 v[128:129], v[46:47], s[48:49], v[72:73] op_sel_hi:[0, 1, 1]
	v_pk_mul_f32 v[42:43], v[42:43], v[130:131]
	v_pk_fma_f32 v[70:71], s[84:85], v[128:129], v[70:71]
	v_pk_fma_f32 v[42:43], v[46:47], s[50:51], v[42:43] op_sel_hi:[0, 1, 1]
	v_pk_fma_f32 v[46:47], s[86:87], v[42:43], v[70:71]
	s_nop 0
	v_add_f32_e32 v46, v46, v47
	v_fma_mix_f32 v46, v1, v44, v46 op_sel_hi:[0,1,0]
	v_fma_mixlo_f16 v46, v46, v48, 0 op_sel_hi:[0,1,0]
	ds_write_b16 v68, v46 offset:16576
	s_waitcnt lgkmcnt(0)
	s_load_dwordx16 s[36:51], s[54:55], 0x700
	s_load_dwordx16 s[72:87], s[54:55], 0x740
	v_cvt_f32_f16_sdwa v46, v52 dst_sel:DWORD dst_unused:UNUSED_PAD src0_sel:WORD_1
	v_pk_mul_f32 v[130:131], v[46:47], v[14:15] op_sel_hi:[0,1]
	v_exp_f32_e32 v130, v130
	v_exp_f32_e32 v131, v131
	v_pk_mul_f32 v[136:137], v[46:47], v[16:17] op_sel_hi:[0,1]
	v_exp_f32_e32 v136, v136
	v_exp_f32_e32 v137, v137
	v_fma_mix_f32 v52, v46, v44, 0 op_sel:[0,1,0] op_sel_hi:[0,1,0]
	v_pk_mul_f32 v[50:51], v[130:131], v[50:51]
	v_pk_fma_f32 v[50:51], v[52:53], s[56:57], v[50:51] op_sel_hi:[0, 1, 1]
	v_pk_fma_f32 v[54:55], s[88:89], v[50:51], 0 op_sel_hi:[1, 1, 0]
	v_pk_mul_f32 v[106:107], v[136:137], v[132:133]
	s_nop 0
	v_pk_fma_f32 v[130:131], v[52:53], s[58:59], v[106:107] op_sel_hi:[0, 1, 1]
	v_pk_mul_f32 v[56:57], v[46:47], v[10:11] op_sel_hi:[0,1]
	v_exp_f32_e32 v56, v56
	v_exp_f32_e32 v57, v57
	v_pk_mul_f32 v[106:107], v[46:47], v[12:13] op_sel_hi:[0,1]
	v_exp_f32_e32 v106, v106
	v_exp_f32_e32 v107, v107
	v_pk_mul_f32 v[56:57], v[56:57], v[134:135]
	v_pk_fma_f32 v[54:55], s[90:91], v[130:131], v[54:55]
	v_pk_fma_f32 v[132:133], v[52:53], s[60:61], v[56:57] op_sel_hi:[0, 1, 1]
	v_pk_mul_f32 v[56:57], v[106:107], v[122:123]
	v_pk_mul_f32 v[58:59], v[46:47], v[8:9] op_sel_hi:[0,1]
	v_pk_fma_f32 v[122:123], v[52:53], s[62:63], v[56:57] op_sel_hi:[0, 1, 1]
	v_pk_mul_f32 v[56:57], v[46:47], v[6:7] op_sel_hi:[0,1]
	v_exp_f32_e32 v56, v56
	v_exp_f32_e32 v57, v57
	v_exp_f32_e32 v58, v58
	v_exp_f32_e32 v59, v59
	v_pk_fma_f32 v[54:55], s[92:93], v[132:133], v[54:55]
	v_pk_mul_f32 v[56:57], v[56:57], v[124:125]
	v_pk_fma_f32 v[54:55], s[94:95], v[122:123], v[54:55]
	v_pk_fma_f32 v[124:125], v[52:53], s[64:65], v[56:57] op_sel_hi:[0, 1, 1]
	v_pk_mul_f32 v[56:57], v[58:59], v[126:127]
	v_pk_fma_f32 v[54:55], s[96:97], v[124:125], v[54:55]
	v_pk_fma_f32 v[126:127], v[52:53], s[66:67], v[56:57] op_sel_hi:[0, 1, 1]
	v_pk_mul_f32 v[56:57], v[46:47], v[2:3] op_sel_hi:[0,1]
	v_exp_f32_e32 v56, v56
	v_exp_f32_e32 v57, v57
	v_pk_mul_f32 v[46:47], v[46:47], v[4:5] op_sel_hi:[0,1]
	v_exp_f32_e32 v46, v46
	v_exp_f32_e32 v47, v47
	v_pk_mul_f32 v[56:57], v[56:57], v[128:129]
	v_pk_fma_f32 v[54:55], s[98:99], v[126:127], v[54:55]
	v_pk_fma_f32 v[128:129], v[52:53], s[68:69], v[56:57] op_sel_hi:[0, 1, 1]
	v_pk_mul_f32 v[42:43], v[46:47], v[42:43]
	v_pk_fma_f32 v[54:55], s[20:21], v[128:129], v[54:55]
	v_pk_fma_f32 v[42:43], v[52:53], s[70:71], v[42:43] op_sel_hi:[0, 1, 1]
	v_pk_fma_f32 v[46:47], s[22:23], v[42:43], v[54:55]
	s_nop 0
	v_add_f32_e32 v46, v46, v47
	v_fma_mix_f32 v44, v1, v44, v46 op_sel:[0,1,0] op_sel_hi:[0,1,0]
	v_fma_mixlo_f16 v44, v44, v48, 0 op_sel:[0,1,0] op_sel_hi:[0,1,0]
	ds_write_b16 v68, v44 offset:17616
	s_waitcnt lgkmcnt(0)
	s_load_dwordx16 s[56:71], s[54:55], 0x780
	s_load_dwordx8 s[88:95], s[54:55], 0x7c0
	s_load_dwordx4 s[96:99], s[54:55], 0x7e0
	s_load_dwordx4 s[20:23], s[54:55], 0x7f0
	v_cvt_f32_f16_e32 v44, v53
	v_pk_mul_f32 v[134:135], v[44:45], v[14:15] op_sel_hi:[0,1]
	v_exp_f32_e32 v134, v134
	v_exp_f32_e32 v135, v135
	v_pk_mul_f32 v[136:137], v[44:45], v[16:17] op_sel_hi:[0,1]
	v_exp_f32_e32 v136, v136
	v_exp_f32_e32 v137, v137
	v_fma_mix_f32 v46, v44, v45, 0 op_sel_hi:[0,1,0]
	v_pk_mul_f32 v[50:51], v[134:135], v[50:51]
	v_pk_fma_f32 v[50:51], v[46:47], s[36:37], v[50:51] op_sel_hi:[0, 1, 1]
	v_pk_fma_f32 v[70:71], s[72:73], v[50:51], 0 op_sel_hi:[1, 1, 0]
	v_pk_mul_f32 v[86:87], v[136:137], v[130:131]
	s_nop 0
	v_pk_fma_f32 v[130:131], v[46:47], s[38:39], v[86:87] op_sel_hi:[0, 1, 1]
	v_pk_mul_f32 v[72:73], v[44:45], v[10:11] op_sel_hi:[0,1]
	v_exp_f32_e32 v72, v72
	v_exp_f32_e32 v73, v73
	v_pk_mul_f32 v[86:87], v[44:45], v[12:13] op_sel_hi:[0,1]
	v_exp_f32_e32 v86, v86
	v_exp_f32_e32 v87, v87
	v_pk_mul_f32 v[72:73], v[72:73], v[132:133]
	v_pk_fma_f32 v[70:71], s[74:75], v[130:131], v[70:71]
	v_pk_fma_f32 v[132:133], v[46:47], s[40:41], v[72:73] op_sel_hi:[0, 1, 1]
	v_pk_mul_f32 v[72:73], v[86:87], v[122:123]
	v_pk_mul_f32 v[74:75], v[44:45], v[8:9] op_sel_hi:[0,1]
	v_pk_fma_f32 v[122:123], v[46:47], s[42:43], v[72:73] op_sel_hi:[0, 1, 1]
	v_pk_mul_f32 v[72:73], v[44:45], v[6:7] op_sel_hi:[0,1]
	v_exp_f32_e32 v72, v72
	v_exp_f32_e32 v73, v73
	v_exp_f32_e32 v74, v74
	v_exp_f32_e32 v75, v75
	v_pk_fma_f32 v[70:71], s[76:77], v[132:133], v[70:71]
	v_pk_mul_f32 v[72:73], v[72:73], v[124:125]
	v_pk_fma_f32 v[70:71], s[78:79], v[122:123], v[70:71]
	v_pk_fma_f32 v[124:125], v[46:47], s[44:45], v[72:73] op_sel_hi:[0, 1, 1]
	v_pk_mul_f32 v[72:73], v[74:75], v[126:127]
	v_pk_mul_f32 v[74:75], v[44:45], v[4:5] op_sel_hi:[0,1]
	v_pk_fma_f32 v[126:127], v[46:47], s[46:47], v[72:73] op_sel_hi:[0, 1, 1]
	v_pk_mul_f32 v[72:73], v[44:45], v[2:3] op_sel_hi:[0,1]
	v_exp_f32_e32 v72, v72
	v_exp_f32_e32 v73, v73
	v_exp_f32_e32 v74, v74
	v_exp_f32_e32 v75, v75
	v_pk_fma_f32 v[70:71], s[80:81], v[124:125], v[70:71]
	v_pk_mul_f32 v[72:73], v[72:73], v[128:129]
	v_pk_fma_f32 v[70:71], s[82:83], v[126:127], v[70:71]
	v_pk_fma_f32 v[128:129], v[46:47], s[48:49], v[72:73] op_sel_hi:[0, 1, 1]
	v_pk_mul_f32 v[42:43], v[74:75], v[42:43]
	v_pk_fma_f32 v[70:71], s[84:85], v[128:129], v[70:71]
	v_pk_fma_f32 v[42:43], v[46:47], s[50:51], v[42:43] op_sel_hi:[0, 1, 1]
	v_pk_fma_f32 v[46:47], s[86:87], v[42:43], v[70:71]
	s_nop 0
	v_add_f32_e32 v44, v46, v47
	v_fma_mix_f32 v44, v1, v45, v44 op_sel_hi:[0,1,0]
	v_fma_mixlo_f16 v44, v44, v49, 0 op_sel_hi:[0,1,0]
	ds_write_b16 v68, v44 offset:18656
	s_waitcnt lgkmcnt(0)
	s_load_dwordx16 s[36:51], s[54:55], 0x800
	s_load_dwordx16 s[72:87], s[54:55], 0x840
	v_cvt_f32_f16_sdwa v44, v53 dst_sel:DWORD dst_unused:UNUSED_PAD src0_sel:WORD_1
	v_pk_mul_f32 v[52:53], v[44:45], v[14:15] op_sel_hi:[0,1]
	v_pk_mul_f32 v[134:135], v[44:45], v[16:17] op_sel_hi:[0,1]
	v_exp_f32_e32 v52, v52
	v_exp_f32_e32 v53, v53
	v_exp_f32_e32 v134, v134
	v_exp_f32_e32 v135, v135
	v_fma_mix_f32 v46, v44, v45, 0 op_sel:[0,1,0] op_sel_hi:[0,1,0]
	v_pk_mul_f32 v[50:51], v[52:53], v[50:51]
	v_pk_mul_f32 v[52:53], v[134:135], v[130:131]
	v_pk_fma_f32 v[130:131], v[46:47], s[58:59], v[52:53] op_sel_hi:[0, 1, 1]
	v_pk_mul_f32 v[52:53], v[44:45], v[10:11] op_sel_hi:[0,1]
	v_pk_fma_f32 v[136:137], v[46:47], s[56:57], v[50:51] op_sel_hi:[0, 1, 1]
	v_exp_f32_e32 v52, v52
	v_exp_f32_e32 v53, v53
	v_pk_mul_f32 v[54:55], v[44:45], v[12:13] op_sel_hi:[0,1]
	v_exp_f32_e32 v54, v54
	v_exp_f32_e32 v55, v55
	v_pk_fma_f32 v[50:51], s[88:89], v[136:137], 0 op_sel_hi:[1, 1, 0]
	v_pk_mul_f32 v[52:53], v[52:53], v[132:133]
	v_pk_fma_f32 v[50:51], s[90:91], v[130:131], v[50:51]
	v_pk_fma_f32 v[132:133], v[46:47], s[60:61], v[52:53] op_sel_hi:[0, 1, 1]
	v_pk_mul_f32 v[52:53], v[54:55], v[122:123]
	v_pk_fma_f32 v[50:51], s[92:93], v[132:133], v[50:51]
	v_pk_fma_f32 v[110:111], v[46:47], s[62:63], v[52:53] op_sel_hi:[0, 1, 1]
	v_pk_mul_f32 v[52:53], v[44:45], v[6:7] op_sel_hi:[0,1]
	v_exp_f32_e32 v52, v52
	v_exp_f32_e32 v53, v53
	v_pk_mul_f32 v[54:55], v[44:45], v[8:9] op_sel_hi:[0,1]
	v_exp_f32_e32 v54, v54
	v_exp_f32_e32 v55, v55
	v_pk_mul_f32 v[52:53], v[52:53], v[124:125]
	v_pk_fma_f32 v[50:51], s[94:95], v[110:111], v[50:51]
	v_pk_fma_f32 v[112:113], v[46:47], s[64:65], v[52:53] op_sel_hi:[0, 1, 1]
	v_pk_mul_f32 v[52:53], v[54:55], v[126:127]
	v_pk_fma_f32 v[50:51], s[96:97], v[112:113], v[50:51]
	v_pk_fma_f32 v[114:115], v[46:47], s[66:67], v[52:53] op_sel_hi:[0, 1, 1]
	v_pk_mul_f32 v[52:53], v[44:45], v[2:3] op_sel_hi:[0,1]
	v_exp_f32_e32 v52, v52
	v_exp_f32_e32 v53, v53
	v_pk_mul_f32 v[54:55], v[44:45], v[4:5] op_sel_hi:[0,1]
	v_exp_f32_e32 v54, v54
	v_exp_f32_e32 v55, v55
	v_pk_mul_f32 v[52:53], v[52:53], v[128:129]
	v_pk_fma_f32 v[50:51], s[98:99], v[114:115], v[50:51]
	v_pk_fma_f32 v[116:117], v[46:47], s[68:69], v[52:53] op_sel_hi:[0, 1, 1]
	v_pk_mul_f32 v[42:43], v[54:55], v[42:43]
	v_pk_fma_f32 v[50:51], s[20:21], v[116:117], v[50:51]
	v_pk_fma_f32 v[118:119], v[46:47], s[70:71], v[42:43] op_sel_hi:[0, 1, 1]
	v_pk_fma_f32 v[42:43], s[22:23], v[118:119], v[50:51]
	s_nop 0
	v_add_f32_e32 v42, v42, v43
	v_fma_mix_f32 v42, v1, v45, v42 op_sel:[0,1,0] op_sel_hi:[0,1,0]
	v_fma_mixlo_f16 v42, v42, v49, 0 op_sel:[0,1,0] op_sel_hi:[0,1,0]
	ds_write_b16 v68, v42 offset:19696
	s_waitcnt lgkmcnt(0)
	s_load_dwordx16 s[56:71], s[54:55], 0x880
	s_load_dwordx8 s[88:95], s[54:55], 0x8c0
	s_load_dwordx4 s[96:99], s[54:55], 0x8e0
	s_load_dwordx4 s[20:23], s[54:55], 0x8f0
	s_waitcnt vmcnt(5)
	v_cvt_f32_f16_e32 v120, v38
	s_waitcnt vmcnt(4)
	v_pk_mul_f32 v[124:125], v[120:121], v[14:15] op_sel_hi:[0,1]
	v_exp_f32_e32 v124, v124
	v_exp_f32_e32 v125, v125
	v_pk_mul_f32 v[126:127], v[120:121], v[16:17] op_sel_hi:[0,1]
	v_exp_f32_e32 v126, v126
	v_exp_f32_e32 v127, v127
	v_fma_mix_f32 v122, v120, v30, 0 op_sel_hi:[0,1,0]
	v_pk_mul_f32 v[124:125], v[124:125], v[136:137]
	v_pk_fma_f32 v[124:125], v[122:123], s[36:37], v[124:125] op_sel_hi:[0, 1, 1]
	v_pk_fma_f32 v[70:71], s[72:73], v[124:125], 0 op_sel_hi:[1, 1, 0]
	v_pk_mul_f32 v[86:87], v[126:127], v[130:131]
	s_nop 0
	v_pk_fma_f32 v[126:127], v[122:123], s[38:39], v[86:87] op_sel_hi:[0, 1, 1]
	v_pk_mul_f32 v[72:73], v[120:121], v[10:11] op_sel_hi:[0,1]
	v_exp_f32_e32 v72, v72
	v_exp_f32_e32 v73, v73
	v_pk_mul_f32 v[86:87], v[120:121], v[12:13] op_sel_hi:[0,1]
	v_exp_f32_e32 v86, v86
	v_exp_f32_e32 v87, v87
	v_pk_mul_f32 v[72:73], v[72:73], v[132:133]
	v_pk_fma_f32 v[70:71], s[74:75], v[126:127], v[70:71]
	v_pk_fma_f32 v[128:129], v[122:123], s[40:41], v[72:73] op_sel_hi:[0, 1, 1]
	v_pk_mul_f32 v[72:73], v[86:87], v[110:111]
	v_pk_mul_f32 v[74:75], v[120:121], v[8:9] op_sel_hi:[0,1]
	v_pk_fma_f32 v[110:111], v[122:123], s[42:43], v[72:73] op_sel_hi:[0, 1, 1]
	v_pk_mul_f32 v[72:73], v[120:121], v[6:7] op_sel_hi:[0,1]
	v_exp_f32_e32 v72, v72
	v_exp_f32_e32 v73, v73
	v_exp_f32_e32 v74, v74
	v_exp_f32_e32 v75, v75
	v_pk_fma_f32 v[70:71], s[76:77], v[128:129], v[70:71]
	v_pk_mul_f32 v[72:73], v[72:73], v[112:113]
	v_pk_fma_f32 v[70:71], s[78:79], v[110:111], v[70:71]
	v_pk_fma_f32 v[112:113], v[122:123], s[44:45], v[72:73] op_sel_hi:[0, 1, 1]
	v_pk_mul_f32 v[72:73], v[74:75], v[114:115]
	v_pk_mul_f32 v[74:75], v[120:121], v[4:5] op_sel_hi:[0,1]
	v_pk_fma_f32 v[114:115], v[122:123], s[46:47], v[72:73] op_sel_hi:[0, 1, 1]
	v_pk_mul_f32 v[72:73], v[120:121], v[2:3] op_sel_hi:[0,1]
	v_exp_f32_e32 v72, v72
	v_exp_f32_e32 v73, v73
	v_exp_f32_e32 v74, v74
	v_exp_f32_e32 v75, v75
	v_pk_fma_f32 v[70:71], s[80:81], v[112:113], v[70:71]
	v_pk_mul_f32 v[72:73], v[72:73], v[116:117]
	v_pk_fma_f32 v[70:71], s[82:83], v[114:115], v[70:71]
	v_pk_fma_f32 v[116:117], v[122:123], s[48:49], v[72:73] op_sel_hi:[0, 1, 1]
	v_pk_mul_f32 v[72:73], v[74:75], v[118:119]
	v_pk_fma_f32 v[70:71], s[84:85], v[116:117], v[70:71]
	v_pk_fma_f32 v[118:119], v[122:123], s[50:51], v[72:73] op_sel_hi:[0, 1, 1]
	v_pk_fma_f32 v[70:71], s[86:87], v[118:119], v[70:71]
	s_nop 0
	v_add_f32_e32 v69, v70, v71
	v_fma_mix_f32 v69, v1, v30, v69 op_sel_hi:[0,1,0]
	s_waitcnt vmcnt(3)
	v_fma_mixlo_f16 v69, v69, v34, 0 op_sel_hi:[0,1,0]
	ds_write_b16 v68, v69 offset:20736
	s_waitcnt lgkmcnt(0)
	s_load_dwordx16 s[36:51], s[54:55], 0x900
	s_load_dwordx16 s[72:87], s[54:55], 0x940
	v_cvt_f32_f16_sdwa v38, v38 dst_sel:DWORD dst_unused:UNUSED_PAD src0_sel:WORD_1
	v_pk_mul_f32 v[122:123], v[38:39], v[14:15] op_sel_hi:[0,1]
	v_exp_f32_e32 v122, v122
	v_exp_f32_e32 v123, v123
	v_pk_mul_f32 v[130:131], v[38:39], v[16:17] op_sel_hi:[0,1]
	v_exp_f32_e32 v130, v130
	v_exp_f32_e32 v131, v131
	v_fma_mix_f32 v120, v38, v30, 0 op_sel:[0,1,0] op_sel_hi:[0,1,0]
	v_pk_mul_f32 v[122:123], v[122:123], v[124:125]
	v_pk_fma_f32 v[122:123], v[120:121], s[56:57], v[122:123] op_sel_hi:[0, 1, 1]
	v_pk_fma_f32 v[42:43], s[88:89], v[122:123], 0 op_sel_hi:[1, 1, 0]
	v_pk_mul_f32 v[58:59], v[130:131], v[126:127]
	s_nop 0
	v_pk_fma_f32 v[124:125], v[120:121], s[58:59], v[58:59] op_sel_hi:[0, 1, 1]
	v_pk_mul_f32 v[44:45], v[38:39], v[10:11] op_sel_hi:[0,1]
	v_exp_f32_e32 v44, v44
	v_exp_f32_e32 v45, v45
	v_pk_mul_f32 v[58:59], v[38:39], v[12:13] op_sel_hi:[0,1]
	v_exp_f32_e32 v58, v58
	v_exp_f32_e32 v59, v59
	v_pk_mul_f32 v[44:45], v[44:45], v[128:129]
	v_pk_fma_f32 v[42:43], s[90:91], v[124:125], v[42:43]
	v_pk_fma_f32 v[126:127], v[120:121], s[60:61], v[44:45] op_sel_hi:[0, 1, 1]
	v_pk_mul_f32 v[44:45], v[58:59], v[110:111]
	v_pk_mul_f32 v[46:47], v[38:39], v[8:9] op_sel_hi:[0,1]
	v_pk_fma_f32 v[110:111], v[120:121], s[62:63], v[44:45] op_sel_hi:[0, 1, 1]
	v_pk_mul_f32 v[44:45], v[38:39], v[6:7] op_sel_hi:[0,1]
	v_exp_f32_e32 v44, v44
	v_exp_f32_e32 v45, v45
	v_exp_f32_e32 v46, v46
	v_exp_f32_e32 v47, v47
	v_pk_fma_f32 v[42:43], s[92:93], v[126:127], v[42:43]
	v_pk_mul_f32 v[44:45], v[44:45], v[112:113]
	v_pk_fma_f32 v[42:43], s[94:95], v[110:111], v[42:43]
	v_pk_fma_f32 v[112:113], v[120:121], s[64:65], v[44:45] op_sel_hi:[0, 1, 1]
	v_pk_mul_f32 v[44:45], v[46:47], v[114:115]
	v_pk_mul_f32 v[46:47], v[38:39], v[4:5] op_sel_hi:[0,1]
	v_pk_fma_f32 v[114:115], v[120:121], s[66:67], v[44:45] op_sel_hi:[0, 1, 1]
	v_pk_mul_f32 v[44:45], v[38:39], v[2:3] op_sel_hi:[0,1]
	v_exp_f32_e32 v44, v44
	v_exp_f32_e32 v45, v45
	v_exp_f32_e32 v46, v46
	v_exp_f32_e32 v47, v47
	v_pk_fma_f32 v[42:43], s[96:97], v[112:113], v[42:43]
	v_pk_mul_f32 v[44:45], v[44:45], v[116:117]
	v_pk_fma_f32 v[42:43], s[98:99], v[114:115], v[42:43]
	v_pk_fma_f32 v[116:117], v[120:121], s[68:69], v[44:45] op_sel_hi:[0, 1, 1]
	v_pk_mul_f32 v[44:45], v[46:47], v[118:119]
	v_pk_fma_f32 v[42:43], s[20:21], v[116:117], v[42:43]
	v_pk_fma_f32 v[118:119], v[120:121], s[70:71], v[44:45] op_sel_hi:[0, 1, 1]
	v_pk_fma_f32 v[42:43], s[22:23], v[118:119], v[42:43]
	s_nop 0
	v_add_f32_e32 v38, v42, v43
	v_fma_mix_f32 v30, v1, v30, v38 op_sel:[0,1,0] op_sel_hi:[0,1,0]
	v_fma_mixlo_f16 v30, v30, v34, 0 op_sel:[0,1,0] op_sel_hi:[0,1,0]
	ds_write_b16 v68, v30 offset:21776
	s_waitcnt lgkmcnt(0)
	s_load_dwordx16 s[56:71], s[54:55], 0x980
	s_load_dwordx8 s[88:95], s[54:55], 0x9c0
	s_load_dwordx4 s[96:99], s[54:55], 0x9e0
	s_load_dwordx4 s[20:23], s[54:55], 0x9f0
	v_cvt_f32_f16_e32 v30, v39
	v_pk_mul_f32 v[120:121], v[30:31], v[14:15] op_sel_hi:[0,1]
	v_exp_f32_e32 v120, v120
	v_exp_f32_e32 v121, v121
	v_pk_mul_f32 v[128:129], v[30:31], v[16:17] op_sel_hi:[0,1]
	v_exp_f32_e32 v128, v128
	v_exp_f32_e32 v129, v129
	v_fma_mix_f32 v34, v30, v31, 0 op_sel_hi:[0,1,0]
	v_pk_mul_f32 v[120:121], v[120:121], v[122:123]
	v_pk_fma_f32 v[120:121], v[34:35], s[36:37], v[120:121] op_sel_hi:[0, 1, 1]
	v_pk_fma_f32 v[70:71], s[72:73], v[120:121], 0 op_sel_hi:[1, 1, 0]
	v_pk_mul_f32 v[86:87], v[128:129], v[124:125]
	s_nop 0
	v_pk_fma_f32 v[122:123], v[34:35], s[38:39], v[86:87] op_sel_hi:[0, 1, 1]
	v_pk_mul_f32 v[72:73], v[30:31], v[10:11] op_sel_hi:[0,1]
	v_exp_f32_e32 v72, v72
	v_exp_f32_e32 v73, v73
	v_pk_mul_f32 v[86:87], v[30:31], v[12:13] op_sel_hi:[0,1]
	v_exp_f32_e32 v86, v86
	v_exp_f32_e32 v87, v87
	v_pk_mul_f32 v[72:73], v[72:73], v[126:127]
	v_pk_fma_f32 v[70:71], s[74:75], v[122:123], v[70:71]
	v_pk_fma_f32 v[124:125], v[34:35], s[40:41], v[72:73] op_sel_hi:[0, 1, 1]
	v_pk_mul_f32 v[72:73], v[86:87], v[110:111]
	v_pk_mul_f32 v[74:75], v[30:31], v[8:9] op_sel_hi:[0,1]
	v_pk_fma_f32 v[110:111], v[34:35], s[42:43], v[72:73] op_sel_hi:[0, 1, 1]
	v_pk_mul_f32 v[72:73], v[30:31], v[6:7] op_sel_hi:[0,1]
	v_exp_f32_e32 v72, v72
	v_exp_f32_e32 v73, v73
	v_exp_f32_e32 v74, v74
	v_exp_f32_e32 v75, v75
	v_pk_fma_f32 v[70:71], s[76:77], v[124:125], v[70:71]
	v_pk_mul_f32 v[72:73], v[72:73], v[112:113]
	v_pk_fma_f32 v[70:71], s[78:79], v[110:111], v[70:71]
	v_pk_fma_f32 v[112:113], v[34:35], s[44:45], v[72:73] op_sel_hi:[0, 1, 1]
	v_pk_mul_f32 v[72:73], v[74:75], v[114:115]
	v_pk_mul_f32 v[74:75], v[30:31], v[4:5] op_sel_hi:[0,1]
	v_pk_fma_f32 v[114:115], v[34:35], s[46:47], v[72:73] op_sel_hi:[0, 1, 1]
	v_pk_mul_f32 v[72:73], v[30:31], v[2:3] op_sel_hi:[0,1]
	v_exp_f32_e32 v72, v72
	v_exp_f32_e32 v73, v73
	v_exp_f32_e32 v74, v74
	v_exp_f32_e32 v75, v75
	v_pk_fma_f32 v[70:71], s[80:81], v[112:113], v[70:71]
	v_pk_mul_f32 v[72:73], v[72:73], v[116:117]
	v_pk_fma_f32 v[70:71], s[82:83], v[114:115], v[70:71]
	v_pk_fma_f32 v[116:117], v[34:35], s[48:49], v[72:73] op_sel_hi:[0, 1, 1]
	v_pk_mul_f32 v[72:73], v[74:75], v[118:119]
	v_pk_fma_f32 v[70:71], s[84:85], v[116:117], v[70:71]
	v_pk_fma_f32 v[118:119], v[34:35], s[50:51], v[72:73] op_sel_hi:[0, 1, 1]
	v_pk_fma_f32 v[70:71], s[86:87], v[118:119], v[70:71]
	s_nop 0
	v_add_f32_e32 v30, v70, v71
	v_fma_mix_f32 v30, v1, v31, v30 op_sel_hi:[0,1,0]
	v_fma_mixlo_f16 v30, v30, v35, 0 op_sel_hi:[0,1,0]
	ds_write_b16 v68, v30 offset:22816
	s_waitcnt lgkmcnt(0)
	s_load_dwordx16 s[36:51], s[54:55], 0xa00
	s_load_dwordx16 s[72:87], s[54:55], 0xa40
	v_cvt_f32_f16_sdwa v30, v39 dst_sel:DWORD dst_unused:UNUSED_PAD src0_sel:WORD_1
	v_pk_mul_f32 v[38:39], v[30:31], v[14:15] op_sel_hi:[0,1]
	v_exp_f32_e32 v38, v38
	v_exp_f32_e32 v39, v39
	v_pk_mul_f32 v[126:127], v[30:31], v[16:17] op_sel_hi:[0,1]
	v_exp_f32_e32 v126, v126
	v_exp_f32_e32 v127, v127
	v_fma_mix_f32 v34, v30, v31, 0 op_sel:[0,1,0] op_sel_hi:[0,1,0]
	v_pk_mul_f32 v[38:39], v[38:39], v[120:121]
	v_pk_fma_f32 v[38:39], v[34:35], s[56:57], v[38:39] op_sel_hi:[0, 1, 1]
	v_pk_fma_f32 v[42:43], s[88:89], v[38:39], 0 op_sel_hi:[1, 1, 0]
	v_pk_mul_f32 v[58:59], v[126:127], v[122:123]
	s_nop 0
	v_pk_fma_f32 v[120:121], v[34:35], s[58:59], v[58:59] op_sel_hi:[0, 1, 1]
	v_pk_mul_f32 v[44:45], v[30:31], v[10:11] op_sel_hi:[0,1]
	v_exp_f32_e32 v44, v44
	v_exp_f32_e32 v45, v45
	v_pk_mul_f32 v[58:59], v[30:31], v[12:13] op_sel_hi:[0,1]
	v_exp_f32_e32 v58, v58
	v_exp_f32_e32 v59, v59
	v_pk_mul_f32 v[44:45], v[44:45], v[124:125]
	v_pk_fma_f32 v[42:43], s[90:91], v[120:121], v[42:43]
	v_pk_fma_f32 v[122:123], v[34:35], s[60:61], v[44:45] op_sel_hi:[0, 1, 1]
	v_pk_mul_f32 v[44:45], v[58:59], v[110:111]
	v_pk_mul_f32 v[46:47], v[30:31], v[8:9] op_sel_hi:[0,1]
	v_pk_fma_f32 v[110:111], v[34:35], s[62:63], v[44:45] op_sel_hi:[0, 1, 1]
	v_pk_mul_f32 v[44:45], v[30:31], v[6:7] op_sel_hi:[0,1]
	v_exp_f32_e32 v44, v44
	v_exp_f32_e32 v45, v45
	v_exp_f32_e32 v46, v46
	v_exp_f32_e32 v47, v47
	v_pk_fma_f32 v[42:43], s[92:93], v[122:123], v[42:43]
	v_pk_mul_f32 v[44:45], v[44:45], v[112:113]
	v_pk_fma_f32 v[42:43], s[94:95], v[110:111], v[42:43]
	v_pk_fma_f32 v[112:113], v[34:35], s[64:65], v[44:45] op_sel_hi:[0, 1, 1]
	v_pk_mul_f32 v[44:45], v[46:47], v[114:115]
	v_pk_mul_f32 v[46:47], v[30:31], v[4:5] op_sel_hi:[0,1]
	v_pk_fma_f32 v[114:115], v[34:35], s[66:67], v[44:45] op_sel_hi:[0, 1, 1]
	v_pk_mul_f32 v[44:45], v[30:31], v[2:3] op_sel_hi:[0,1]
	v_exp_f32_e32 v44, v44
	v_exp_f32_e32 v45, v45
	v_exp_f32_e32 v46, v46
	v_exp_f32_e32 v47, v47
	v_pk_fma_f32 v[42:43], s[96:97], v[112:113], v[42:43]
	v_pk_mul_f32 v[44:45], v[44:45], v[116:117]
	v_pk_fma_f32 v[42:43], s[98:99], v[114:115], v[42:43]
	v_pk_fma_f32 v[116:117], v[34:35], s[68:69], v[44:45] op_sel_hi:[0, 1, 1]
	v_pk_mul_f32 v[44:45], v[46:47], v[118:119]
	v_pk_fma_f32 v[42:43], s[20:21], v[116:117], v[42:43]
	v_pk_fma_f32 v[118:119], v[34:35], s[70:71], v[44:45] op_sel_hi:[0, 1, 1]
	v_pk_fma_f32 v[42:43], s[22:23], v[118:119], v[42:43]
	s_nop 0
	v_add_f32_e32 v30, v42, v43
	v_fma_mix_f32 v30, v1, v31, v30 op_sel:[0,1,0] op_sel_hi:[0,1,0]
	v_fma_mixlo_f16 v30, v30, v35, 0 op_sel:[0,1,0] op_sel_hi:[0,1,0]
	ds_write_b16 v68, v30 offset:23856
	s_waitcnt lgkmcnt(0)
	s_load_dwordx16 s[56:71], s[54:55], 0xa80
	s_load_dwordx8 s[88:95], s[54:55], 0xac0
	s_load_dwordx4 s[96:99], s[54:55], 0xae0
	s_load_dwordx4 s[20:23], s[54:55], 0xaf0
	v_cvt_f32_f16_e32 v30, v40
	v_pk_mul_f32 v[124:125], v[30:31], v[14:15] op_sel_hi:[0,1]
	v_exp_f32_e32 v124, v124
	v_exp_f32_e32 v125, v125
	v_pk_mul_f32 v[126:127], v[30:31], v[16:17] op_sel_hi:[0,1]
	v_exp_f32_e32 v126, v126
	v_exp_f32_e32 v127, v127
	v_fma_mix_f32 v34, v30, v32, 0 op_sel_hi:[0,1,0]
	v_pk_mul_f32 v[38:39], v[124:125], v[38:39]
	v_pk_fma_f32 v[38:39], v[34:35], s[36:37], v[38:39] op_sel_hi:[0, 1, 1]
	v_pk_fma_f32 v[70:71], s[72:73], v[38:39], 0 op_sel_hi:[1, 1, 0]
	v_pk_mul_f32 v[86:87], v[126:127], v[120:121]
	s_nop 0
	v_pk_fma_f32 v[120:121], v[34:35], s[38:39], v[86:87] op_sel_hi:[0, 1, 1]
	v_pk_mul_f32 v[72:73], v[30:31], v[10:11] op_sel_hi:[0,1]
	v_exp_f32_e32 v72, v72
	v_exp_f32_e32 v73, v73
	v_pk_mul_f32 v[86:87], v[30:31], v[12:13] op_sel_hi:[0,1]
	v_exp_f32_e32 v86, v86
	v_exp_f32_e32 v87, v87
	v_pk_mul_f32 v[72:73], v[72:73], v[122:123]
	v_pk_fma_f32 v[70:71], s[74:75], v[120:121], v[70:71]
	v_pk_fma_f32 v[122:123], v[34:35], s[40:41], v[72:73] op_sel_hi:[0, 1, 1]
	v_pk_mul_f32 v[72:73], v[86:87], v[110:111]
	v_pk_mul_f32 v[74:75], v[30:31], v[8:9] op_sel_hi:[0,1]
	v_pk_fma_f32 v[110:111], v[34:35], s[42:43], v[72:73] op_sel_hi:[0, 1, 1]
	v_pk_mul_f32 v[72:73], v[30:31], v[6:7] op_sel_hi:[0,1]
	v_exp_f32_e32 v72, v72
	v_exp_f32_e32 v73, v73
	v_exp_f32_e32 v74, v74
	v_exp_f32_e32 v75, v75
	v_pk_fma_f32 v[70:71], s[76:77], v[122:123], v[70:71]
	v_pk_mul_f32 v[72:73], v[72:73], v[112:113]
	v_pk_fma_f32 v[70:71], s[78:79], v[110:111], v[70:71]
	v_pk_fma_f32 v[112:113], v[34:35], s[44:45], v[72:73] op_sel_hi:[0, 1, 1]
	v_pk_mul_f32 v[72:73], v[74:75], v[114:115]
	v_pk_fma_f32 v[70:71], s[80:81], v[112:113], v[70:71]
	v_pk_fma_f32 v[114:115], v[34:35], s[46:47], v[72:73] op_sel_hi:[0, 1, 1]
	v_pk_mul_f32 v[72:73], v[30:31], v[2:3] op_sel_hi:[0,1]
	v_exp_f32_e32 v72, v72
	v_exp_f32_e32 v73, v73
	v_pk_mul_f32 v[30:31], v[30:31], v[4:5] op_sel_hi:[0,1]
	v_exp_f32_e32 v30, v30
	v_exp_f32_e32 v31, v31
	v_pk_mul_f32 v[72:73], v[72:73], v[116:117]
	v_pk_fma_f32 v[70:71], s[82:83], v[114:115], v[70:71]
	v_pk_fma_f32 v[116:117], v[34:35], s[48:49], v[72:73] op_sel_hi:[0, 1, 1]
	v_pk_mul_f32 v[30:31], v[30:31], v[118:119]
	v_pk_fma_f32 v[70:71], s[84:85], v[116:117], v[70:71]
	v_pk_fma_f32 v[30:31], v[34:35], s[50:51], v[30:31] op_sel_hi:[0, 1, 1]
	v_pk_fma_f32 v[34:35], s[86:87], v[30:31], v[70:71]
	s_nop 0
	v_add_f32_e32 v34, v34, v35
	v_fma_mix_f32 v34, v1, v32, v34 op_sel_hi:[0,1,0]
	v_fma_mixlo_f16 v34, v34, v36, 0 op_sel_hi:[0,1,0]
	ds_write_b16 v68, v34 offset:24896
	s_waitcnt lgkmcnt(0)
	s_load_dwordx16 s[36:51], s[54:55], 0xb00
	s_load_dwordx16 s[72:87], s[54:55], 0xb40
	v_cvt_f32_f16_sdwa v34, v40 dst_sel:DWORD dst_unused:UNUSED_PAD src0_sel:WORD_1
	v_pk_mul_f32 v[118:119], v[34:35], v[14:15] op_sel_hi:[0,1]
	v_exp_f32_e32 v118, v118
	v_exp_f32_e32 v119, v119
	v_pk_mul_f32 v[124:125], v[34:35], v[16:17] op_sel_hi:[0,1]
	v_exp_f32_e32 v124, v124
	v_exp_f32_e32 v125, v125
	v_fma_mix_f32 v40, v34, v32, 0 op_sel:[0,1,0] op_sel_hi:[0,1,0]
	v_pk_mul_f32 v[38:39], v[118:119], v[38:39]
	v_pk_fma_f32 v[38:39], v[40:41], s[56:57], v[38:39] op_sel_hi:[0, 1, 1]
	v_pk_fma_f32 v[42:43], s[88:89], v[38:39], 0 op_sel_hi:[1, 1, 0]
	v_pk_mul_f32 v[58:59], v[124:125], v[120:121]
	s_nop 0
	v_pk_fma_f32 v[118:119], v[40:41], s[58:59], v[58:59] op_sel_hi:[0, 1, 1]
	v_pk_mul_f32 v[44:45], v[34:35], v[10:11] op_sel_hi:[0,1]
	v_exp_f32_e32 v44, v44
	v_exp_f32_e32 v45, v45
	v_pk_mul_f32 v[58:59], v[34:35], v[12:13] op_sel_hi:[0,1]
	v_exp_f32_e32 v58, v58
	v_exp_f32_e32 v59, v59
	v_pk_mul_f32 v[44:45], v[44:45], v[122:123]
	v_pk_fma_f32 v[42:43], s[90:91], v[118:119], v[42:43]
	v_pk_fma_f32 v[120:121], v[40:41], s[60:61], v[44:45] op_sel_hi:[0, 1, 1]
	v_pk_mul_f32 v[44:45], v[58:59], v[110:111]
	v_pk_mul_f32 v[46:47], v[34:35], v[8:9] op_sel_hi:[0,1]
	v_pk_fma_f32 v[110:111], v[40:41], s[62:63], v[44:45] op_sel_hi:[0, 1, 1]
	v_pk_mul_f32 v[44:45], v[34:35], v[6:7] op_sel_hi:[0,1]
	v_exp_f32_e32 v44, v44
	v_exp_f32_e32 v45, v45
	v_exp_f32_e32 v46, v46
	v_exp_f32_e32 v47, v47
	v_pk_fma_f32 v[42:43], s[92:93], v[120:121], v[42:43]
	v_pk_mul_f32 v[44:45], v[44:45], v[112:113]
	v_pk_fma_f32 v[42:43], s[94:95], v[110:111], v[42:43]
	v_pk_fma_f32 v[112:113], v[40:41], s[64:65], v[44:45] op_sel_hi:[0, 1, 1]
	v_pk_mul_f32 v[44:45], v[46:47], v[114:115]
	v_pk_fma_f32 v[42:43], s[96:97], v[112:113], v[42:43]
	v_pk_fma_f32 v[114:115], v[40:41], s[66:67], v[44:45] op_sel_hi:[0, 1, 1]
	v_pk_mul_f32 v[44:45], v[34:35], v[2:3] op_sel_hi:[0,1]
	v_exp_f32_e32 v44, v44
	v_exp_f32_e32 v45, v45
	v_pk_mul_f32 v[34:35], v[34:35], v[4:5] op_sel_hi:[0,1]
	v_exp_f32_e32 v34, v34
	v_exp_f32_e32 v35, v35
	v_pk_mul_f32 v[44:45], v[44:45], v[116:117]
	v_pk_fma_f32 v[42:43], s[98:99], v[114:115], v[42:43]
	v_pk_fma_f32 v[116:117], v[40:41], s[68:69], v[44:45] op_sel_hi:[0, 1, 1]
	v_pk_mul_f32 v[30:31], v[34:35], v[30:31]
	v_pk_fma_f32 v[42:43], s[20:21], v[116:117], v[42:43]
	v_pk_fma_f32 v[30:31], v[40:41], s[70:71], v[30:31] op_sel_hi:[0, 1, 1]
	v_pk_fma_f32 v[34:35], s[22:23], v[30:31], v[42:43]
	s_nop 0
	v_add_f32_e32 v34, v34, v35
	v_fma_mix_f32 v32, v1, v32, v34 op_sel:[0,1,0] op_sel_hi:[0,1,0]
	v_fma_mixlo_f16 v32, v32, v36, 0 op_sel:[0,1,0] op_sel_hi:[0,1,0]
	ds_write_b16 v68, v32 offset:25936
	s_waitcnt lgkmcnt(0)
	s_load_dwordx16 s[56:71], s[54:55], 0xb80
	s_load_dwordx8 s[88:95], s[54:55], 0xbc0
	s_load_dwordx4 s[96:99], s[54:55], 0xbe0
	s_load_dwordx4 s[20:23], s[54:55], 0xbf0
	v_cvt_f32_f16_e32 v32, v41
	v_pk_mul_f32 v[122:123], v[32:33], v[14:15] op_sel_hi:[0,1]
	v_exp_f32_e32 v122, v122
	v_exp_f32_e32 v123, v123
	v_pk_mul_f32 v[124:125], v[32:33], v[16:17] op_sel_hi:[0,1]
	v_exp_f32_e32 v124, v124
	v_exp_f32_e32 v125, v125
	v_fma_mix_f32 v34, v32, v33, 0 op_sel_hi:[0,1,0]
	v_pk_mul_f32 v[38:39], v[122:123], v[38:39]
	v_pk_fma_f32 v[38:39], v[34:35], s[36:37], v[38:39] op_sel_hi:[0, 1, 1]
	v_pk_fma_f32 v[70:71], s[72:73], v[38:39], 0 op_sel_hi:[1, 1, 0]
	v_pk_mul_f32 v[86:87], v[124:125], v[118:119]
	s_nop 0
	v_pk_fma_f32 v[118:119], v[34:35], s[38:39], v[86:87] op_sel_hi:[0, 1, 1]
	v_pk_mul_f32 v[72:73], v[32:33], v[10:11] op_sel_hi:[0,1]
	v_exp_f32_e32 v72, v72
	v_exp_f32_e32 v73, v73
	v_pk_mul_f32 v[86:87], v[32:33], v[12:13] op_sel_hi:[0,1]
	v_exp_f32_e32 v86, v86
	v_exp_f32_e32 v87, v87
	v_pk_mul_f32 v[72:73], v[72:73], v[120:121]
	v_pk_fma_f32 v[70:71], s[74:75], v[118:119], v[70:71]
	v_pk_fma_f32 v[120:121], v[34:35], s[40:41], v[72:73] op_sel_hi:[0, 1, 1]
	v_pk_mul_f32 v[72:73], v[86:87], v[110:111]
	v_pk_mul_f32 v[74:75], v[32:33], v[8:9] op_sel_hi:[0,1]
	v_pk_fma_f32 v[110:111], v[34:35], s[42:43], v[72:73] op_sel_hi:[0, 1, 1]
	v_pk_mul_f32 v[72:73], v[32:33], v[6:7] op_sel_hi:[0,1]
	v_exp_f32_e32 v72, v72
	v_exp_f32_e32 v73, v73
	v_exp_f32_e32 v74, v74
	v_exp_f32_e32 v75, v75
	v_pk_fma_f32 v[70:71], s[76:77], v[120:121], v[70:71]
	v_pk_mul_f32 v[72:73], v[72:73], v[112:113]
	v_pk_fma_f32 v[70:71], s[78:79], v[110:111], v[70:71]
	v_pk_fma_f32 v[112:113], v[34:35], s[44:45], v[72:73] op_sel_hi:[0, 1, 1]
	v_pk_mul_f32 v[72:73], v[74:75], v[114:115]
	v_pk_mul_f32 v[74:75], v[32:33], v[4:5] op_sel_hi:[0,1]
	v_pk_fma_f32 v[114:115], v[34:35], s[46:47], v[72:73] op_sel_hi:[0, 1, 1]
	v_pk_mul_f32 v[72:73], v[32:33], v[2:3] op_sel_hi:[0,1]
	v_exp_f32_e32 v72, v72
	v_exp_f32_e32 v73, v73
	v_exp_f32_e32 v74, v74
	v_exp_f32_e32 v75, v75
	v_pk_fma_f32 v[70:71], s[80:81], v[112:113], v[70:71]
	v_pk_mul_f32 v[72:73], v[72:73], v[116:117]
	v_pk_fma_f32 v[70:71], s[82:83], v[114:115], v[70:71]
	v_pk_fma_f32 v[116:117], v[34:35], s[48:49], v[72:73] op_sel_hi:[0, 1, 1]
	v_pk_mul_f32 v[30:31], v[74:75], v[30:31]
	v_pk_fma_f32 v[70:71], s[84:85], v[116:117], v[70:71]
	v_pk_fma_f32 v[30:31], v[34:35], s[50:51], v[30:31] op_sel_hi:[0, 1, 1]
	v_pk_fma_f32 v[34:35], s[86:87], v[30:31], v[70:71]
	s_nop 0
	v_add_f32_e32 v32, v34, v35
	v_fma_mix_f32 v32, v1, v33, v32 op_sel_hi:[0,1,0]
	v_fma_mixlo_f16 v32, v32, v37, 0 op_sel_hi:[0,1,0]
	ds_write_b16 v68, v32 offset:26976
	s_waitcnt lgkmcnt(0)
	s_load_dwordx16 s[36:51], s[54:55], 0xc00
	s_load_dwordx16 s[72:87], s[54:55], 0xc40
	v_cvt_f32_f16_sdwa v32, v41 dst_sel:DWORD dst_unused:UNUSED_PAD src0_sel:WORD_1
	v_pk_mul_f32 v[40:41], v[32:33], v[14:15] op_sel_hi:[0,1]
	v_pk_mul_f32 v[122:123], v[32:33], v[16:17] op_sel_hi:[0,1]
	v_exp_f32_e32 v40, v40
	v_exp_f32_e32 v41, v41
	v_exp_f32_e32 v122, v122
	v_exp_f32_e32 v123, v123
	v_fma_mix_f32 v34, v32, v33, 0 op_sel:[0,1,0] op_sel_hi:[0,1,0]
	v_pk_mul_f32 v[38:39], v[40:41], v[38:39]
	v_pk_mul_f32 v[40:41], v[122:123], v[118:119]
	v_pk_fma_f32 v[118:119], v[34:35], s[58:59], v[40:41] op_sel_hi:[0, 1, 1]
	v_pk_mul_f32 v[40:41], v[32:33], v[10:11] op_sel_hi:[0,1]
	v_pk_fma_f32 v[124:125], v[34:35], s[56:57], v[38:39] op_sel_hi:[0, 1, 1]
	v_exp_f32_e32 v40, v40
	v_exp_f32_e32 v41, v41
	v_pk_mul_f32 v[42:43], v[32:33], v[12:13] op_sel_hi:[0,1]
	v_exp_f32_e32 v42, v42
	v_exp_f32_e32 v43, v43
	v_pk_fma_f32 v[38:39], s[88:89], v[124:125], 0 op_sel_hi:[1, 1, 0]
	v_pk_mul_f32 v[40:41], v[40:41], v[120:121]
	v_pk_fma_f32 v[38:39], s[90:91], v[118:119], v[38:39]
	v_pk_fma_f32 v[120:121], v[34:35], s[60:61], v[40:41] op_sel_hi:[0, 1, 1]
	v_pk_mul_f32 v[40:41], v[42:43], v[110:111]
	v_pk_fma_f32 v[38:39], s[92:93], v[120:121], v[38:39]
	v_pk_fma_f32 v[62:63], v[34:35], s[62:63], v[40:41] op_sel_hi:[0, 1, 1]
	v_pk_mul_f32 v[40:41], v[32:33], v[6:7] op_sel_hi:[0,1]
	v_exp_f32_e32 v40, v40
	v_exp_f32_e32 v41, v41
	v_pk_mul_f32 v[42:43], v[32:33], v[8:9] op_sel_hi:[0,1]
	v_exp_f32_e32 v42, v42
	v_exp_f32_e32 v43, v43
	v_pk_mul_f32 v[40:41], v[40:41], v[112:113]
	v_pk_fma_f32 v[38:39], s[94:95], v[62:63], v[38:39]
	v_pk_fma_f32 v[64:65], v[34:35], s[64:65], v[40:41] op_sel_hi:[0, 1, 1]
	v_pk_mul_f32 v[40:41], v[42:43], v[114:115]
	v_pk_fma_f32 v[38:39], s[96:97], v[64:65], v[38:39]
	v_pk_fma_f32 v[102:103], v[34:35], s[66:67], v[40:41] op_sel_hi:[0, 1, 1]
	v_pk_mul_f32 v[40:41], v[32:33], v[2:3] op_sel_hi:[0,1]
	v_exp_f32_e32 v40, v40
	v_exp_f32_e32 v41, v41
	v_pk_mul_f32 v[42:43], v[32:33], v[4:5] op_sel_hi:[0,1]
	v_exp_f32_e32 v42, v42
	v_exp_f32_e32 v43, v43
	v_pk_mul_f32 v[40:41], v[40:41], v[116:117]
	v_pk_fma_f32 v[38:39], s[98:99], v[102:103], v[38:39]
	v_pk_fma_f32 v[104:105], v[34:35], s[68:69], v[40:41] op_sel_hi:[0, 1, 1]
	v_pk_mul_f32 v[30:31], v[42:43], v[30:31]
	v_pk_fma_f32 v[38:39], s[20:21], v[104:105], v[38:39]
	v_pk_fma_f32 v[106:107], v[34:35], s[70:71], v[30:31] op_sel_hi:[0, 1, 1]
	v_pk_fma_f32 v[30:31], s[22:23], v[106:107], v[38:39]
	s_nop 0
	v_add_f32_e32 v30, v30, v31
	v_fma_mix_f32 v30, v1, v33, v30 op_sel:[0,1,0] op_sel_hi:[0,1,0]
	v_fma_mixlo_f16 v30, v30, v37, 0 op_sel:[0,1,0] op_sel_hi:[0,1,0]
	ds_write_b16 v68, v30 offset:28016
	s_waitcnt lgkmcnt(0)
	s_load_dwordx16 s[56:71], s[54:55], 0xc80
	s_load_dwordx8 s[88:95], s[54:55], 0xcc0
	s_load_dwordx4 s[96:99], s[54:55], 0xce0
	s_load_dwordx4 s[20:23], s[54:55], 0xcf0
	s_waitcnt vmcnt(2)
	v_cvt_f32_f16_e32 v108, v26
	s_waitcnt vmcnt(1)
	v_pk_mul_f32 v[112:113], v[108:109], v[14:15] op_sel_hi:[0,1]
	v_exp_f32_e32 v112, v112
	v_exp_f32_e32 v113, v113
	v_pk_mul_f32 v[114:115], v[108:109], v[16:17] op_sel_hi:[0,1]
	v_exp_f32_e32 v114, v114
	v_exp_f32_e32 v115, v115
	v_fma_mix_f32 v110, v108, v18, 0 op_sel_hi:[0,1,0]
	v_pk_mul_f32 v[112:113], v[112:113], v[124:125]
	v_pk_fma_f32 v[112:113], v[110:111], s[36:37], v[112:113] op_sel_hi:[0, 1, 1]
	v_pk_fma_f32 v[70:71], s[72:73], v[112:113], 0 op_sel_hi:[1, 1, 0]
	v_pk_mul_f32 v[86:87], v[114:115], v[118:119]
	s_nop 0
	v_pk_fma_f32 v[114:115], v[110:111], s[38:39], v[86:87] op_sel_hi:[0, 1, 1]
	v_pk_mul_f32 v[72:73], v[108:109], v[10:11] op_sel_hi:[0,1]
	v_exp_f32_e32 v72, v72
	v_exp_f32_e32 v73, v73
	v_pk_mul_f32 v[86:87], v[108:109], v[12:13] op_sel_hi:[0,1]
	v_exp_f32_e32 v86, v86
	v_exp_f32_e32 v87, v87
	v_pk_mul_f32 v[72:73], v[72:73], v[120:121]
	v_pk_fma_f32 v[70:71], s[74:75], v[114:115], v[70:71]
	v_pk_fma_f32 v[116:117], v[110:111], s[40:41], v[72:73] op_sel_hi:[0, 1, 1]
	v_pk_mul_f32 v[62:63], v[86:87], v[62:63]
	v_pk_fma_f32 v[70:71], s[76:77], v[116:117], v[70:71]
	v_pk_fma_f32 v[118:119], v[110:111], s[42:43], v[62:63] op_sel_hi:[0, 1, 1]
	v_pk_fma_f32 v[62:63], s[78:79], v[118:119], v[70:71]
	v_pk_mul_f32 v[70:71], v[108:109], v[6:7] op_sel_hi:[0,1]
	v_exp_f32_e32 v70, v70
	v_exp_f32_e32 v71, v71
	v_pk_mul_f32 v[72:73], v[108:109], v[8:9] op_sel_hi:[0,1]
	v_exp_f32_e32 v72, v72
	v_exp_f32_e32 v73, v73
	v_pk_mul_f32 v[64:65], v[70:71], v[64:65]
	v_pk_mul_f32 v[70:71], v[108:109], v[4:5] op_sel_hi:[0,1]
	v_pk_fma_f32 v[120:121], v[110:111], s[44:45], v[64:65] op_sel_hi:[0, 1, 1]
	v_pk_mul_f32 v[64:65], v[72:73], v[102:103]
	v_exp_f32_e32 v70, v70
	v_pk_fma_f32 v[102:103], v[110:111], s[46:47], v[64:65] op_sel_hi:[0, 1, 1]
	v_pk_mul_f32 v[64:65], v[108:109], v[2:3] op_sel_hi:[0,1]
	v_exp_f32_e32 v64, v64
	v_exp_f32_e32 v65, v65
	v_exp_f32_e32 v71, v71
	v_pk_fma_f32 v[62:63], s[80:81], v[120:121], v[62:63]
	v_pk_mul_f32 v[64:65], v[64:65], v[104:105]
	v_pk_fma_f32 v[62:63], s[82:83], v[102:103], v[62:63]
	v_pk_fma_f32 v[104:105], v[110:111], s[48:49], v[64:65] op_sel_hi:[0, 1, 1]
	v_pk_mul_f32 v[64:65], v[70:71], v[106:107]
	v_pk_fma_f32 v[62:63], s[84:85], v[104:105], v[62:63]
	v_pk_fma_f32 v[98:99], v[110:111], s[50:51], v[64:65] op_sel_hi:[0, 1, 1]
	v_pk_fma_f32 v[62:63], s[86:87], v[98:99], v[62:63]
	s_nop 0
	v_add_f32_e32 v62, v62, v63
	v_fma_mix_f32 v62, v1, v18, v62 op_sel_hi:[0,1,0]
	s_waitcnt vmcnt(0)
	v_fma_mixlo_f16 v62, v62, v22, 0 op_sel_hi:[0,1,0]
	ds_write_b16 v68, v62 offset:29056
	v_lshrrev_b32_e32 v196, 6, v0
	v_and_b32_e32 v197, 48, v0
	v_lshl_or_b32 v196, v196, 7, v197
	v_and_b32_e32 v197, 15, v0
	v_or_b32_e32 v197, s28, v197
	v_lshl_or_b32 v196, v197, 10, v196
	v_add_u32_e32 v197, 0x4000, v196
	global_load_dwordx4 v[180:183], v196, s[4:5]
	global_load_dwordx4 v[184:187], v196, s[4:5] offset:64
	global_load_dwordx4 v[188:191], v197, s[4:5]
	global_load_dwordx4 v[192:195], v197, s[4:5] offset:64
	v_and_b32_e32 v196, 63, v0
	v_lshlrev_b32_e32 v196, 4, v196
	global_load_dwordx4 v[204:207], v196, s[6:7]
	global_load_dwordx4 v[208:211], v196, s[8:9]
	s_waitcnt lgkmcnt(0)
	s_load_dwordx16 s[36:51], s[54:55], 0xd00
	s_load_dwordx16 s[72:87], s[54:55], 0xd40
	v_cvt_f32_f16_sdwa v26, v26 dst_sel:DWORD dst_unused:UNUSED_PAD src0_sel:WORD_1
	v_pk_mul_f32 v[106:107], v[26:27], v[14:15] op_sel_hi:[0,1]
	v_exp_f32_e32 v106, v106
	v_exp_f32_e32 v107, v107
	v_pk_mul_f32 v[108:109], v[26:27], v[16:17] op_sel_hi:[0,1]
	v_exp_f32_e32 v108, v108
	v_exp_f32_e32 v109, v109
	v_fma_mix_f32 v100, v26, v18, 0 op_sel:[0,1,0] op_sel_hi:[0,1,0]
	v_pk_mul_f32 v[106:107], v[106:107], v[112:113]
	v_pk_fma_f32 v[106:107], v[100:101], s[56:57], v[106:107] op_sel_hi:[0, 1, 1]
	v_pk_fma_f32 v[30:31], s[88:89], v[106:107], 0 op_sel_hi:[1, 1, 0]
	v_pk_mul_f32 v[46:47], v[108:109], v[114:115]
	s_nop 0
	v_pk_fma_f32 v[108:109], v[100:101], s[58:59], v[46:47] op_sel_hi:[0, 1, 1]
	v_pk_mul_f32 v[32:33], v[26:27], v[10:11] op_sel_hi:[0,1]
	v_exp_f32_e32 v32, v32
	v_exp_f32_e32 v33, v33
	v_pk_mul_f32 v[46:47], v[26:27], v[12:13] op_sel_hi:[0,1]
	v_exp_f32_e32 v46, v46
	v_exp_f32_e32 v47, v47
	v_pk_mul_f32 v[32:33], v[32:33], v[116:117]
	v_pk_fma_f32 v[30:31], s[90:91], v[108:109], v[30:31]
	v_pk_fma_f32 v[110:111], v[100:101], s[60:61], v[32:33] op_sel_hi:[0, 1, 1]
	v_pk_mul_f32 v[32:33], v[46:47], v[118:119]
	v_pk_mul_f32 v[34:35], v[26:27], v[8:9] op_sel_hi:[0,1]
	v_pk_fma_f32 v[112:113], v[100:101], s[62:63], v[32:33] op_sel_hi:[0, 1, 1]
	v_pk_mul_f32 v[32:33], v[26:27], v[6:7] op_sel_hi:[0,1]
	v_exp_f32_e32 v32, v32
	v_exp_f32_e32 v33, v33
	v_exp_f32_e32 v34, v34
	v_exp_f32_e32 v35, v35
	v_pk_fma_f32 v[30:31], s[92:93], v[110:111], v[30:31]
	v_pk_mul_f32 v[32:33], v[32:33], v[120:121]
	v_pk_fma_f32 v[30:31], s[94:95], v[112:113], v[30:31]
	v_pk_fma_f32 v[114:115], v[100:101], s[64:65], v[32:33] op_sel_hi:[0, 1, 1]
	v_pk_mul_f32 v[32:33], v[34:35], v[102:103]
	v_pk_mul_f32 v[34:35], v[26:27], v[4:5] op_sel_hi:[0,1]
	v_pk_fma_f32 v[102:103], v[100:101], s[66:67], v[32:33] op_sel_hi:[0, 1, 1]
	v_pk_mul_f32 v[32:33], v[26:27], v[2:3] op_sel_hi:[0,1]
	v_exp_f32_e32 v32, v32
	v_exp_f32_e32 v33, v33
	v_exp_f32_e32 v34, v34
	v_exp_f32_e32 v35, v35
	v_pk_fma_f32 v[30:31], s[96:97], v[114:115], v[30:31]
	v_pk_mul_f32 v[32:33], v[32:33], v[104:105]
	v_pk_fma_f32 v[30:31], s[98:99], v[102:103], v[30:31]
	v_pk_fma_f32 v[104:105], v[100:101], s[68:69], v[32:33] op_sel_hi:[0, 1, 1]
	v_pk_mul_f32 v[32:33], v[34:35], v[98:99]
	v_pk_fma_f32 v[30:31], s[20:21], v[104:105], v[30:31]
	v_pk_fma_f32 v[98:99], v[100:101], s[70:71], v[32:33] op_sel_hi:[0, 1, 1]
	v_pk_fma_f32 v[30:31], s[22:23], v[98:99], v[30:31]
	s_nop 0
	v_add_f32_e32 v26, v30, v31
	v_fma_mix_f32 v18, v1, v18, v26 op_sel:[0,1,0] op_sel_hi:[0,1,0]
	v_fma_mixlo_f16 v18, v18, v22, 0 op_sel:[0,1,0] op_sel_hi:[0,1,0]
	ds_write_b16 v68, v18 offset:30096
	s_waitcnt lgkmcnt(0)
	s_load_dwordx16 s[56:71], s[54:55], 0xd80
	s_load_dwordx8 s[88:95], s[54:55], 0xdc0
	s_load_dwordx4 s[96:99], s[54:55], 0xde0
	s_load_dwordx4 s[20:23], s[54:55], 0xdf0
	v_cvt_f32_f16_e32 v18, v27
	v_pk_mul_f32 v[100:101], v[18:19], v[14:15] op_sel_hi:[0,1]
	v_exp_f32_e32 v100, v100
	v_exp_f32_e32 v101, v101
	v_pk_mul_f32 v[116:117], v[18:19], v[16:17] op_sel_hi:[0,1]
	v_exp_f32_e32 v116, v116
	v_exp_f32_e32 v117, v117
	v_fma_mix_f32 v22, v18, v19, 0 op_sel_hi:[0,1,0]
	v_pk_mul_f32 v[100:101], v[100:101], v[106:107]
	v_pk_fma_f32 v[100:101], v[22:23], s[36:37], v[100:101] op_sel_hi:[0, 1, 1]
	v_pk_fma_f32 v[62:63], s[72:73], v[100:101], 0 op_sel_hi:[1, 1, 0]
	v_pk_mul_f32 v[82:83], v[116:117], v[108:109]
	s_nop 0
	v_pk_fma_f32 v[106:107], v[22:23], s[38:39], v[82:83] op_sel_hi:[0, 1, 1]
	v_pk_mul_f32 v[64:65], v[18:19], v[10:11] op_sel_hi:[0,1]
	v_exp_f32_e32 v64, v64
	v_exp_f32_e32 v65, v65
	v_pk_mul_f32 v[82:83], v[18:19], v[12:13] op_sel_hi:[0,1]
	v_exp_f32_e32 v82, v82
	v_exp_f32_e32 v83, v83
	v_pk_mul_f32 v[64:65], v[64:65], v[110:111]
	v_pk_fma_f32 v[62:63], s[74:75], v[106:107], v[62:63]
	v_pk_fma_f32 v[108:109], v[22:23], s[40:41], v[64:65] op_sel_hi:[0, 1, 1]
	v_pk_mul_f32 v[64:65], v[82:83], v[112:113]
	v_pk_mul_f32 v[70:71], v[18:19], v[8:9] op_sel_hi:[0,1]
	v_pk_fma_f32 v[110:111], v[22:23], s[42:43], v[64:65] op_sel_hi:[0, 1, 1]
	v_pk_mul_f32 v[64:65], v[18:19], v[6:7] op_sel_hi:[0,1]
	v_exp_f32_e32 v64, v64
	v_exp_f32_e32 v65, v65
	v_exp_f32_e32 v70, v70
	v_exp_f32_e32 v71, v71
	v_pk_fma_f32 v[62:63], s[76:77], v[108:109], v[62:63]
	v_pk_mul_f32 v[64:65], v[64:65], v[114:115]
	v_pk_fma_f32 v[62:63], s[78:79], v[110:111], v[62:63]
	v_pk_fma_f32 v[112:113], v[22:23], s[44:45], v[64:65] op_sel_hi:[0, 1, 1]
	v_pk_mul_f32 v[64:65], v[70:71], v[102:103]
	v_pk_mul_f32 v[70:71], v[18:19], v[4:5] op_sel_hi:[0,1]
	v_pk_fma_f32 v[102:103], v[22:23], s[46:47], v[64:65] op_sel_hi:[0, 1, 1]
	v_pk_mul_f32 v[64:65], v[18:19], v[2:3] op_sel_hi:[0,1]
	v_exp_f32_e32 v64, v64
	v_exp_f32_e32 v65, v65
	v_exp_f32_e32 v70, v70
	v_exp_f32_e32 v71, v71
	v_pk_fma_f32 v[62:63], s[80:81], v[112:113], v[62:63]
	v_pk_mul_f32 v[64:65], v[64:65], v[104:105]
	v_pk_fma_f32 v[62:63], s[82:83], v[102:103], v[62:63]
	v_pk_fma_f32 v[104:105], v[22:23], s[48:49], v[64:65] op_sel_hi:[0, 1, 1]
	v_pk_mul_f32 v[64:65], v[70:71], v[98:99]
	v_pk_fma_f32 v[62:63], s[84:85], v[104:105], v[62:63]
	v_pk_fma_f32 v[98:99], v[22:23], s[50:51], v[64:65] op_sel_hi:[0, 1, 1]
	v_pk_fma_f32 v[62:63], s[86:87], v[98:99], v[62:63]
	s_nop 0
	v_add_f32_e32 v18, v62, v63
	v_fma_mix_f32 v18, v1, v19, v18 op_sel_hi:[0,1,0]
	v_fma_mixlo_f16 v18, v18, v23, 0 op_sel_hi:[0,1,0]
	ds_write_b16 v68, v18 offset:31136
	s_waitcnt lgkmcnt(0)
	s_load_dwordx16 s[36:51], s[54:55], 0xe00
	s_load_dwordx16 s[72:87], s[54:55], 0xe40
	v_cvt_f32_f16_sdwa v18, v27 dst_sel:DWORD dst_unused:UNUSED_PAD src0_sel:WORD_1
	v_pk_mul_f32 v[26:27], v[18:19], v[14:15] op_sel_hi:[0,1]
	v_exp_f32_e32 v26, v26
	v_exp_f32_e32 v27, v27
	v_pk_mul_f32 v[114:115], v[18:19], v[16:17] op_sel_hi:[0,1]
	v_exp_f32_e32 v114, v114
	v_exp_f32_e32 v115, v115
	v_fma_mix_f32 v22, v18, v19, 0 op_sel:[0,1,0] op_sel_hi:[0,1,0]
	v_pk_mul_f32 v[26:27], v[26:27], v[100:101]
	v_pk_fma_f32 v[26:27], v[22:23], s[56:57], v[26:27] op_sel_hi:[0, 1, 1]
	v_pk_fma_f32 v[30:31], s[88:89], v[26:27], 0 op_sel_hi:[1, 1, 0]
	v_pk_mul_f32 v[46:47], v[114:115], v[106:107]
	s_nop 0
	v_pk_fma_f32 v[100:101], v[22:23], s[58:59], v[46:47] op_sel_hi:[0, 1, 1]
	v_pk_mul_f32 v[32:33], v[18:19], v[10:11] op_sel_hi:[0,1]
	v_exp_f32_e32 v32, v32
	v_exp_f32_e32 v33, v33
	v_pk_mul_f32 v[46:47], v[18:19], v[12:13] op_sel_hi:[0,1]
	v_exp_f32_e32 v46, v46
	v_exp_f32_e32 v47, v47
	v_pk_mul_f32 v[32:33], v[32:33], v[108:109]
	v_pk_fma_f32 v[30:31], s[90:91], v[100:101], v[30:31]
	v_pk_fma_f32 v[106:107], v[22:23], s[60:61], v[32:33] op_sel_hi:[0, 1, 1]
	v_pk_mul_f32 v[32:33], v[46:47], v[110:111]
	v_pk_mul_f32 v[34:35], v[18:19], v[8:9] op_sel_hi:[0,1]
	v_pk_fma_f32 v[108:109], v[22:23], s[62:63], v[32:33] op_sel_hi:[0, 1, 1]
	v_pk_mul_f32 v[32:33], v[18:19], v[6:7] op_sel_hi:[0,1]
	v_exp_f32_e32 v32, v32
	v_exp_f32_e32 v33, v33
	v_exp_f32_e32 v34, v34
	v_exp_f32_e32 v35, v35
	v_pk_fma_f32 v[30:31], s[92:93], v[106:107], v[30:31]
	v_pk_mul_f32 v[32:33], v[32:33], v[112:113]
	v_pk_fma_f32 v[30:31], s[94:95], v[108:109], v[30:31]
	v_pk_fma_f32 v[110:111], v[22:23], s[64:65], v[32:33] op_sel_hi:[0, 1, 1]
	v_pk_mul_f32 v[32:33], v[34:35], v[102:103]
	v_pk_mul_f32 v[34:35], v[18:19], v[4:5] op_sel_hi:[0,1]
	v_pk_fma_f32 v[102:103], v[22:23], s[66:67], v[32:33] op_sel_hi:[0, 1, 1]
	v_pk_mul_f32 v[32:33], v[18:19], v[2:3] op_sel_hi:[0,1]
	v_exp_f32_e32 v32, v32
	v_exp_f32_e32 v33, v33
	v_exp_f32_e32 v34, v34
	v_exp_f32_e32 v35, v35
	v_pk_fma_f32 v[30:31], s[96:97], v[110:111], v[30:31]
	v_pk_mul_f32 v[32:33], v[32:33], v[104:105]
	v_pk_fma_f32 v[30:31], s[98:99], v[102:103], v[30:31]
	v_pk_fma_f32 v[104:105], v[22:23], s[68:69], v[32:33] op_sel_hi:[0, 1, 1]
	v_pk_mul_f32 v[32:33], v[34:35], v[98:99]
	v_pk_fma_f32 v[30:31], s[20:21], v[104:105], v[30:31]
	v_pk_fma_f32 v[98:99], v[22:23], s[70:71], v[32:33] op_sel_hi:[0, 1, 1]
	v_pk_fma_f32 v[30:31], s[22:23], v[98:99], v[30:31]
	s_nop 0
	v_add_f32_e32 v18, v30, v31
	v_fma_mix_f32 v18, v1, v19, v18 op_sel:[0,1,0] op_sel_hi:[0,1,0]
	v_fma_mixlo_f16 v18, v18, v23, 0 op_sel:[0,1,0] op_sel_hi:[0,1,0]
	ds_write_b16 v68, v18 offset:32176
	s_waitcnt lgkmcnt(0)
	s_load_dwordx16 s[56:71], s[54:55], 0xe80
	s_load_dwordx8 s[88:95], s[54:55], 0xec0
	s_load_dwordx4 s[96:99], s[54:55], 0xee0
	s_load_dwordx4 s[20:23], s[54:55], 0xef0
	v_cvt_f32_f16_e32 v18, v28
	v_pk_mul_f32 v[112:113], v[18:19], v[14:15] op_sel_hi:[0,1]
	v_exp_f32_e32 v112, v112
	v_exp_f32_e32 v113, v113
	v_pk_mul_f32 v[114:115], v[18:19], v[16:17] op_sel_hi:[0,1]
	v_exp_f32_e32 v114, v114
	v_exp_f32_e32 v115, v115
	v_fma_mix_f32 v22, v18, v20, 0 op_sel_hi:[0,1,0]
	v_pk_mul_f32 v[26:27], v[112:113], v[26:27]
	v_pk_fma_f32 v[26:27], v[22:23], s[36:37], v[26:27] op_sel_hi:[0, 1, 1]
	v_pk_fma_f32 v[62:63], s[72:73], v[26:27], 0 op_sel_hi:[1, 1, 0]
	v_pk_mul_f32 v[82:83], v[114:115], v[100:101]
	s_nop 0
	v_pk_fma_f32 v[100:101], v[22:23], s[38:39], v[82:83] op_sel_hi:[0, 1, 1]
	v_pk_mul_f32 v[64:65], v[18:19], v[10:11] op_sel_hi:[0,1]
	v_exp_f32_e32 v64, v64
	v_exp_f32_e32 v65, v65
	v_pk_mul_f32 v[82:83], v[18:19], v[12:13] op_sel_hi:[0,1]
	v_exp_f32_e32 v82, v82
	v_exp_f32_e32 v83, v83
	v_pk_mul_f32 v[64:65], v[64:65], v[106:107]
	v_pk_fma_f32 v[62:63], s[74:75], v[100:101], v[62:63]
	v_pk_fma_f32 v[106:107], v[22:23], s[40:41], v[64:65] op_sel_hi:[0, 1, 1]
	v_pk_mul_f32 v[64:65], v[82:83], v[108:109]
	v_pk_mul_f32 v[70:71], v[18:19], v[8:9] op_sel_hi:[0,1]
	v_pk_fma_f32 v[108:109], v[22:23], s[42:43], v[64:65] op_sel_hi:[0, 1, 1]
	v_pk_mul_f32 v[64:65], v[18:19], v[6:7] op_sel_hi:[0,1]
	v_exp_f32_e32 v64, v64
	v_exp_f32_e32 v65, v65
	v_exp_f32_e32 v70, v70
	v_exp_f32_e32 v71, v71
	v_pk_fma_f32 v[62:63], s[76:77], v[106:107], v[62:63]
	v_pk_mul_f32 v[64:65], v[64:65], v[110:111]
	v_pk_fma_f32 v[62:63], s[78:79], v[108:109], v[62:63]
	v_pk_fma_f32 v[110:111], v[22:23], s[44:45], v[64:65] op_sel_hi:[0, 1, 1]
	v_pk_mul_f32 v[64:65], v[70:71], v[102:103]
	v_pk_fma_f32 v[62:63], s[80:81], v[110:111], v[62:63]
	v_pk_fma_f32 v[102:103], v[22:23], s[46:47], v[64:65] op_sel_hi:[0, 1, 1]
	v_pk_mul_f32 v[64:65], v[18:19], v[2:3] op_sel_hi:[0,1]
	v_exp_f32_e32 v64, v64
	v_exp_f32_e32 v65, v65
	v_pk_mul_f32 v[18:19], v[18:19], v[4:5] op_sel_hi:[0,1]
	v_exp_f32_e32 v18, v18
	v_exp_f32_e32 v19, v19
	v_pk_mul_f32 v[64:65], v[64:65], v[104:105]
	v_pk_fma_f32 v[62:63], s[82:83], v[102:103], v[62:63]
	v_pk_fma_f32 v[104:105], v[22:23], s[48:49], v[64:65] op_sel_hi:[0, 1, 1]
	v_pk_mul_f32 v[18:19], v[18:19], v[98:99]
	v_pk_fma_f32 v[62:63], s[84:85], v[104:105], v[62:63]
	v_pk_fma_f32 v[18:19], v[22:23], s[50:51], v[18:19] op_sel_hi:[0, 1, 1]
	v_pk_fma_f32 v[22:23], s[86:87], v[18:19], v[62:63]
	s_nop 0
	v_add_f32_e32 v22, v22, v23
	v_fma_mix_f32 v22, v1, v20, v22 op_sel_hi:[0,1,0]
	v_fma_mixlo_f16 v22, v22, v24, 0 op_sel_hi:[0,1,0]
	ds_write_b16 v68, v22 offset:33216
	s_waitcnt lgkmcnt(0)
	s_load_dwordx16 s[36:51], s[54:55], 0xf00
	s_load_dwordx16 s[72:87], s[54:55], 0xf40
	v_cvt_f32_f16_sdwa v22, v28 dst_sel:DWORD dst_unused:UNUSED_PAD src0_sel:WORD_1
	v_pk_mul_f32 v[98:99], v[22:23], v[14:15] op_sel_hi:[0,1]
	v_exp_f32_e32 v98, v98
	v_exp_f32_e32 v99, v99
	v_pk_mul_f32 v[112:113], v[22:23], v[16:17] op_sel_hi:[0,1]
	v_exp_f32_e32 v112, v112
	v_exp_f32_e32 v113, v113
	v_fma_mix_f32 v28, v22, v20, 0 op_sel:[0,1,0] op_sel_hi:[0,1,0]
	v_pk_mul_f32 v[26:27], v[98:99], v[26:27]
	v_pk_fma_f32 v[26:27], v[28:29], s[56:57], v[26:27] op_sel_hi:[0, 1, 1]
	v_pk_fma_f32 v[30:31], s[88:89], v[26:27], 0 op_sel_hi:[1, 1, 0]
	v_pk_mul_f32 v[46:47], v[112:113], v[100:101]
	s_nop 0
	v_pk_fma_f32 v[98:99], v[28:29], s[58:59], v[46:47] op_sel_hi:[0, 1, 1]
	v_pk_mul_f32 v[32:33], v[22:23], v[10:11] op_sel_hi:[0,1]
	v_exp_f32_e32 v32, v32
	v_exp_f32_e32 v33, v33
	v_pk_mul_f32 v[46:47], v[22:23], v[12:13] op_sel_hi:[0,1]
	v_exp_f32_e32 v46, v46
	v_exp_f32_e32 v47, v47
	v_pk_mul_f32 v[32:33], v[32:33], v[106:107]
	v_pk_fma_f32 v[30:31], s[90:91], v[98:99], v[30:31]
	v_pk_fma_f32 v[100:101], v[28:29], s[60:61], v[32:33] op_sel_hi:[0, 1, 1]
	v_pk_mul_f32 v[32:33], v[46:47], v[108:109]
	v_pk_mul_f32 v[34:35], v[22:23], v[8:9] op_sel_hi:[0,1]
	v_pk_fma_f32 v[106:107], v[28:29], s[62:63], v[32:33] op_sel_hi:[0, 1, 1]
	v_pk_mul_f32 v[32:33], v[22:23], v[6:7] op_sel_hi:[0,1]
	v_exp_f32_e32 v32, v32
	v_exp_f32_e32 v33, v33
	v_exp_f32_e32 v34, v34
	v_exp_f32_e32 v35, v35
	v_pk_fma_f32 v[30:31], s[92:93], v[100:101], v[30:31]
	v_pk_mul_f32 v[32:33], v[32:33], v[110:111]
	v_pk_fma_f32 v[30:31], s[94:95], v[106:107], v[30:31]
	v_pk_fma_f32 v[108:109], v[28:29], s[64:65], v[32:33] op_sel_hi:[0, 1, 1]
	v_pk_mul_f32 v[32:33], v[34:35], v[102:103]
	v_pk_fma_f32 v[30:31], s[96:97], v[108:109], v[30:31]
	v_pk_fma_f32 v[102:103], v[28:29], s[66:67], v[32:33] op_sel_hi:[0, 1, 1]
	v_pk_mul_f32 v[32:33], v[22:23], v[2:3] op_sel_hi:[0,1]
	v_exp_f32_e32 v32, v32
	v_exp_f32_e32 v33, v33
	v_pk_mul_f32 v[22:23], v[22:23], v[4:5] op_sel_hi:[0,1]
	v_exp_f32_e32 v22, v22
	v_exp_f32_e32 v23, v23
	v_pk_mul_f32 v[32:33], v[32:33], v[104:105]
	v_pk_fma_f32 v[30:31], s[98:99], v[102:103], v[30:31]
	v_pk_fma_f32 v[104:105], v[28:29], s[68:69], v[32:33] op_sel_hi:[0, 1, 1]
	v_pk_mul_f32 v[18:19], v[22:23], v[18:19]
	v_pk_fma_f32 v[30:31], s[20:21], v[104:105], v[30:31]
	v_pk_fma_f32 v[18:19], v[28:29], s[70:71], v[18:19] op_sel_hi:[0, 1, 1]
	v_pk_fma_f32 v[22:23], s[22:23], v[18:19], v[30:31]
	s_nop 0
	v_add_f32_e32 v22, v22, v23
	v_fma_mix_f32 v20, v1, v20, v22 op_sel:[0,1,0] op_sel_hi:[0,1,0]
	v_fma_mixlo_f16 v20, v20, v24, 0 op_sel:[0,1,0] op_sel_hi:[0,1,0]
	ds_write_b16 v68, v20 offset:34256
	s_waitcnt lgkmcnt(0)
	s_load_dwordx16 s[56:71], s[54:55], 0xf80
	s_load_dwordx8 s[88:95], s[54:55], 0xfc0
	s_load_dwordx4 s[96:99], s[54:55], 0xfe0
	s_load_dwordx4 s[20:23], s[54:55], 0xff0
	v_cvt_f32_f16_e32 v20, v29
	v_pk_mul_f32 v[110:111], v[20:21], v[14:15] op_sel_hi:[0,1]
	v_exp_f32_e32 v110, v110
	v_exp_f32_e32 v111, v111
	v_pk_mul_f32 v[112:113], v[20:21], v[16:17] op_sel_hi:[0,1]
	v_exp_f32_e32 v112, v112
	v_exp_f32_e32 v113, v113
	v_fma_mix_f32 v22, v20, v21, 0 op_sel_hi:[0,1,0]
	v_pk_mul_f32 v[26:27], v[110:111], v[26:27]
	v_pk_fma_f32 v[26:27], v[22:23], s[36:37], v[26:27] op_sel_hi:[0, 1, 1]
	v_pk_fma_f32 v[62:63], s[72:73], v[26:27], 0 op_sel_hi:[1, 1, 0]
	v_pk_mul_f32 v[82:83], v[112:113], v[98:99]
	s_nop 0
	v_pk_fma_f32 v[64:65], v[22:23], s[38:39], v[82:83] op_sel_hi:[0, 1, 1]
	v_pk_mul_f32 v[82:83], v[20:21], v[10:11] op_sel_hi:[0,1]
	v_pk_fma_f32 v[62:63], s[74:75], v[64:65], v[62:63]
	v_exp_f32_e32 v82, v82
	v_exp_f32_e32 v83, v83
	v_pk_mul_f32 v[84:85], v[20:21], v[12:13] op_sel_hi:[0,1]
	v_exp_f32_e32 v84, v84
	v_exp_f32_e32 v85, v85
	v_pk_mul_f32 v[82:83], v[82:83], v[100:101]
	s_nop 0
	v_pk_fma_f32 v[70:71], v[22:23], s[40:41], v[82:83] op_sel_hi:[0, 1, 1]
	v_pk_mul_f32 v[82:83], v[84:85], v[106:107]
	v_pk_mul_f32 v[84:85], v[20:21], v[8:9] op_sel_hi:[0,1]
	v_pk_fma_f32 v[72:73], v[22:23], s[42:43], v[82:83] op_sel_hi:[0, 1, 1]
	v_pk_mul_f32 v[82:83], v[20:21], v[6:7] op_sel_hi:[0,1]
	v_exp_f32_e32 v82, v82
	v_exp_f32_e32 v83, v83
	v_exp_f32_e32 v84, v84
	v_exp_f32_e32 v85, v85
	v_pk_fma_f32 v[62:63], s[76:77], v[70:71], v[62:63]
	v_pk_mul_f32 v[82:83], v[82:83], v[108:109]
	v_pk_fma_f32 v[62:63], s[78:79], v[72:73], v[62:63]
	v_pk_fma_f32 v[74:75], v[22:23], s[44:45], v[82:83] op_sel_hi:[0, 1, 1]
	v_pk_mul_f32 v[82:83], v[84:85], v[102:103]
	v_pk_mul_f32 v[84:85], v[20:21], v[4:5] op_sel_hi:[0,1]
	v_pk_fma_f32 v[76:77], v[22:23], s[46:47], v[82:83] op_sel_hi:[0, 1, 1]
	v_pk_mul_f32 v[82:83], v[20:21], v[2:3] op_sel_hi:[0,1]
	v_exp_f32_e32 v82, v82
	v_exp_f32_e32 v83, v83
	v_exp_f32_e32 v84, v84
	v_exp_f32_e32 v85, v85
	v_pk_fma_f32 v[62:63], s[80:81], v[74:75], v[62:63]
	v_pk_mul_f32 v[82:83], v[82:83], v[104:105]
	v_pk_fma_f32 v[62:63], s[82:83], v[76:77], v[62:63]
	v_pk_fma_f32 v[78:79], v[22:23], s[48:49], v[82:83] op_sel_hi:[0, 1, 1]
	v_pk_mul_f32 v[18:19], v[84:85], v[18:19]
	v_pk_fma_f32 v[62:63], s[84:85], v[78:79], v[62:63]
	v_pk_fma_f32 v[18:19], v[22:23], s[50:51], v[18:19] op_sel_hi:[0, 1, 1]
	v_pk_fma_f32 v[22:23], s[86:87], v[18:19], v[62:63]
	s_nop 0
	v_add_f32_e32 v20, v22, v23
	v_fma_mix_f32 v20, v1, v21, v20 op_sel_hi:[0,1,0]
	v_fma_mixlo_f16 v20, v20, v25, 0 op_sel_hi:[0,1,0]
	ds_write_b16 v68, v20 offset:35296
	s_waitcnt lgkmcnt(0)
	v_cvt_f32_f16_sdwa v20, v29 dst_sel:DWORD dst_unused:UNUSED_PAD src0_sel:WORD_1
	v_pk_mul_f32 v[14:15], v[20:21], v[14:15] op_sel_hi:[0,1]
	v_exp_f32_e32 v14, v14
	v_exp_f32_e32 v15, v15
	v_pk_mul_f32 v[16:17], v[20:21], v[16:17] op_sel_hi:[0,1]
	v_exp_f32_e32 v16, v16
	v_exp_f32_e32 v17, v17
	v_pk_mul_f32 v[10:11], v[20:21], v[10:11] op_sel_hi:[0,1]
	v_exp_f32_e32 v10, v10
	v_exp_f32_e32 v11, v11
	v_pk_mul_f32 v[12:13], v[20:21], v[12:13] op_sel_hi:[0,1]
	v_exp_f32_e32 v12, v12
	v_exp_f32_e32 v13, v13
	v_pk_mul_f32 v[6:7], v[20:21], v[6:7] op_sel_hi:[0,1]
	v_fma_mix_f32 v22, v20, v21, 0 op_sel:[0,1,0] op_sel_hi:[0,1,0]
	v_pk_mul_f32 v[14:15], v[14:15], v[26:27]
	v_exp_f32_e32 v6, v6
	v_exp_f32_e32 v7, v7
	v_pk_mul_f32 v[8:9], v[20:21], v[8:9] op_sel_hi:[0,1]
	v_pk_fma_f32 v[14:15], v[22:23], s[56:57], v[14:15] op_sel_hi:[0, 1, 1]
	v_pk_mul_f32 v[16:17], v[16:17], v[64:65]
	v_exp_f32_e32 v8, v8
	v_exp_f32_e32 v9, v9
	v_pk_mul_f32 v[2:3], v[20:21], v[2:3] op_sel_hi:[0,1]
	v_pk_fma_f32 v[14:15], s[88:89], v[14:15], 0 op_sel_hi:[1, 1, 0]
	v_pk_fma_f32 v[16:17], v[22:23], s[58:59], v[16:17] op_sel_hi:[0, 1, 1]
	v_pk_mul_f32 v[10:11], v[10:11], v[70:71]
	v_exp_f32_e32 v2, v2
	v_exp_f32_e32 v3, v3
	v_pk_mul_f32 v[4:5], v[20:21], v[4:5] op_sel_hi:[0,1]
	v_pk_fma_f32 v[14:15], s[90:91], v[16:17], v[14:15]
	v_pk_fma_f32 v[10:11], v[22:23], s[60:61], v[10:11] op_sel_hi:[0, 1, 1]
	v_pk_mul_f32 v[12:13], v[12:13], v[72:73]
	v_exp_f32_e32 v4, v4
	v_exp_f32_e32 v5, v5
	v_pk_fma_f32 v[10:11], s[92:93], v[10:11], v[14:15]
	v_pk_fma_f32 v[12:13], v[22:23], s[62:63], v[12:13] op_sel_hi:[0, 1, 1]
	v_pk_mul_f32 v[6:7], v[6:7], v[74:75]
	v_pk_fma_f32 v[10:11], s[94:95], v[12:13], v[10:11]
	v_pk_fma_f32 v[6:7], v[22:23], s[64:65], v[6:7] op_sel_hi:[0, 1, 1]
	v_pk_mul_f32 v[8:9], v[8:9], v[76:77]
	v_pk_fma_f32 v[6:7], s[96:97], v[6:7], v[10:11]
	v_pk_fma_f32 v[8:9], v[22:23], s[66:67], v[8:9] op_sel_hi:[0, 1, 1]
	v_pk_mul_f32 v[2:3], v[2:3], v[78:79]
	v_pk_fma_f32 v[6:7], s[98:99], v[8:9], v[6:7]
	v_pk_fma_f32 v[2:3], v[22:23], s[68:69], v[2:3] op_sel_hi:[0, 1, 1]
	v_pk_mul_f32 v[4:5], v[4:5], v[18:19]
	v_pk_fma_f32 v[2:3], s[20:21], v[2:3], v[6:7]
	v_pk_fma_f32 v[4:5], v[22:23], s[70:71], v[4:5] op_sel_hi:[0, 1, 1]
	v_pk_fma_f32 v[2:3], s[22:23], v[4:5], v[2:3]
	s_nop 0
	v_add_f32_e32 v2, v2, v3
	v_fma_mix_f32 v1, v1, v21, v2 op_sel:[0,1,0] op_sel_hi:[0,1,0]
	v_fma_mixlo_f16 v1, v1, v25, 0 op_sel:[0,1,0] op_sel_hi:[0,1,0]
	ds_write_b16 v68, v1 offset:36336
	v_lshlrev_b32_e32 v1, 9, v0
	v_and_b32_e32 v2, 0x38000, v1
	v_mov_b32_e32 v3, v67
	v_and_b32_e32 v1, 63, v0
	s_bfe_u32 s14, s2, 0x40003
	v_lshl_add_u64 v[2:3], s[18:19], 0, v[2:3]
	v_lshlrev_b32_e32 v58, 4, v1
	v_mov_b32_e32 v59, v67
	s_lshl_b32 s13, s14, 6
	v_lshl_add_u64 v[20:21], v[2:3], 0, v[58:59]
	s_lshl_b32 s26, s14, 10
	s_add_i32 s12, s13, 64
	v_lshl_add_u64 v[2:3], v[20:21], 0, s[26:27]
	s_and_b32 s15, s12, 0x3c0
	v_add_co_u32_e32 v4, vcc, s52, v2
	s_lshl_b32 s26, s15, 4
	s_lshl_b32 s12, s12, 4
	v_addc_co_u32_e32 v5, vcc, 0, v3, vcc
	global_load_dwordx4 v[28:31], v[2:3], off
	global_load_dwordx4 v[32:35], v[4:5], off
	v_lshl_add_u64 v[2:3], v[20:21], 0, s[26:27]
	s_or_b32 s26, s12, 0x4000
	s_add_i32 s12, s13, 0x80
	s_and_b32 s15, s12, 0x3c0
	v_lshl_add_u64 v[4:5], v[20:21], 0, s[26:27]
	s_lshl_b32 s26, s15, 4
	s_lshl_b32 s12, s12, 4
	global_load_dwordx4 v[36:39], v[2:3], off
	global_load_dwordx4 v[40:43], v[4:5], off
	v_lshl_add_u64 v[2:3], v[20:21], 0, s[26:27]
	s_or_b32 s26, s12, 0x4000
	s_add_i32 s12, s13, 0xc0
	s_and_b32 s15, s12, 0x3c0
	v_lshl_add_u64 v[4:5], v[20:21], 0, s[26:27]
	s_lshl_b32 s26, s15, 4
	s_lshl_b32 s12, s12, 4
	global_load_dwordx4 v[44:47], v[2:3], off
	global_load_dwordx4 v[48:51], v[4:5], off
	v_lshl_add_u64 v[2:3], v[20:21], 0, s[26:27]
	s_or_b32 s26, s12, 0x4000
	s_add_i32 s12, s13, 0x100
	s_and_b32 s15, s12, 0x3c0
	v_lshl_add_u64 v[4:5], v[20:21], 0, s[26:27]
	s_lshl_b32 s26, s15, 4
	s_lshl_b32 s12, s12, 4
	global_load_dwordx4 v[52:55], v[2:3], off
	global_load_dwordx4 v[60:63], v[4:5], off
	v_lshl_add_u64 v[2:3], v[20:21], 0, s[26:27]
	s_or_b32 s26, s12, 0x4000
	s_add_i32 s12, s13, 0x140
	s_and_b32 s15, s12, 0x3c0
	v_lshl_add_u64 v[4:5], v[20:21], 0, s[26:27]
	s_lshl_b32 s26, s15, 4
	s_lshl_b32 s12, s12, 4
	global_load_dwordx4 v[68:71], v[2:3], off
	global_load_dwordx4 v[72:75], v[4:5], off
	v_lshl_add_u64 v[2:3], v[20:21], 0, s[26:27]
	s_or_b32 s26, s12, 0x4000
	s_add_i32 s12, s13, 0x180
	s_and_b32 s15, s12, 0x3c0
	v_lshl_add_u64 v[4:5], v[20:21], 0, s[26:27]
	s_lshl_b32 s26, s15, 4
	s_lshl_b32 s12, s12, 4
	global_load_dwordx4 v[76:79], v[2:3], off
	global_load_dwordx4 v[82:85], v[4:5], off
	v_lshl_add_u64 v[2:3], v[20:21], 0, s[26:27]
	s_or_b32 s26, s12, 0x4000
	s_add_i32 s12, s13, 0x1c0
	s_and_b32 s15, s12, 0x3c0
	v_lshl_add_u64 v[4:5], v[20:21], 0, s[26:27]
	s_lshl_b32 s26, s15, 4
	s_lshl_b32 s12, s12, 4
	v_lshl_add_u64 v[18:19], v[20:21], 0, s[26:27]
	s_or_b32 s26, s12, 0x4000
	s_xor_b32 s15, s13, 0x200
	v_lshl_add_u64 v[22:23], v[20:21], 0, s[26:27]
	s_lshl_b32 s26, s15, 4
	global_load_dwordx4 v[14:17], v[2:3], off
	global_load_dwordx4 v[10:13], v[4:5], off
	global_load_dwordx4 v[6:9], v[18:19], off
	s_nop 0
	global_load_dwordx4 v[2:5], v[22:23], off
	v_lshl_add_u64 v[18:19], v[20:21], 0, s[26:27]
	v_add_co_u32_e32 v22, vcc, s52, v18
	s_waitcnt lgkmcnt(0)
	s_barrier
	v_addc_co_u32_e32 v23, vcc, 0, v19, vcc
	global_load_dwordx4 v[86:89], v[18:19], off
	global_load_dwordx4 v[90:93], v[22:23], off
	v_lshrrev_b32_e32 v118, 6, v0
	v_lshlrev_b32_e32 v22, 7, v118
	v_mov_b32_e32 v23, v67
	v_and_b32_e32 v81, 15, v0
	v_lshl_add_u64 v[24:25], s[4:5], 0, v[22:23]
	v_and_b32_e32 v18, 48, v0
	v_mov_b32_e32 v19, v67
	s_movk_i32 s12, 0x410
	v_lshl_add_u64 v[56:57], v[24:25], 0, v[18:19]
	v_mad_u32_u24 v19, v81, s12, v18
	v_add_u32_e32 v23, s13, v19
	ds_read_b128 v[94:97], v23 offset:4096
	ds_read_b128 v[98:101], v23 offset:20736
	v_or_b32_e32 v26, s28, v81
	v_mov_b32_e32 v27, v67
	v_lshlrev_b64 v[24:25], 10, v[26:27]
	v_or_b32_e32 v26, 16, v26
	v_lshlrev_b64 v[26:27], 10, v[26:27]
	v_lshrrev_b32_e32 v23, 1, v0
	v_lshl_add_u64 v[24:25], v[56:57], 0, v[24:25]
	v_lshl_add_u64 v[26:27], v[56:57], 0, v[26:27]
	v_and_b32_e32 v80, 24, v23
	s_lshl_b32 s14, s14, 5
	s_setprio 1
	s_waitcnt vmcnt(17) lgkmcnt(1)
	v_mfma_f32_16x16x32_f16 v[102:105], v[28:31], v[94:97], 0
	s_waitcnt lgkmcnt(0)
	v_mfma_f32_16x16x32_f16 v[28:31], v[28:31], v[98:101], 0
	s_waitcnt vmcnt(16)
	v_mfma_f32_16x16x32_f16 v[94:97], v[32:35], v[94:97], 0
	v_mfma_f32_16x16x32_f16 v[32:35], v[32:35], v[98:101], 0
	s_setprio 0
	s_add_i32 s16, s13, 0x240
	s_and_b32 s17, s16, 0x3c0
	s_lshl_b32 s26, s17, 4
	s_lshl_b32 s16, s16, 4
	v_lshl_add_u64 v[56:57], v[20:21], 0, s[26:27]
	s_or_b32 s26, s16, 0x4000
	v_lshl_add_u64 v[64:65], v[20:21], 0, s[26:27]
	global_load_dwordx4 v[98:101], v[56:57], off
	global_load_dwordx4 v[106:109], v[64:65], off
	s_add_i32 s16, s14, 32
	s_and_b32 s16, s16, 0x1e0
	v_lshl_add_u32 v23, s16, 1, v19
	ds_read_b128 v[110:113], v23 offset:4096
	ds_read_b128 v[114:117], v23 offset:20736
	s_setprio 1
	s_waitcnt vmcnt(17) lgkmcnt(1)
	v_mfma_f32_16x16x32_f16 v[102:105], v[36:39], v[110:113], v[102:105]
	s_waitcnt lgkmcnt(0)
	v_mfma_f32_16x16x32_f16 v[28:31], v[36:39], v[114:117], v[28:31]
	s_waitcnt vmcnt(16)
	v_mfma_f32_16x16x32_f16 v[36:39], v[40:43], v[110:113], v[94:97]
	v_mfma_f32_16x16x32_f16 v[32:35], v[40:43], v[114:117], v[32:35]
	s_setprio 0
	s_add_i32 s16, s13, 0x280
	s_and_b32 s17, s16, 0x3c0
	s_lshl_b32 s26, s17, 4
	s_lshl_b32 s16, s16, 4
	v_lshl_add_u64 v[56:57], v[20:21], 0, s[26:27]
	s_or_b32 s26, s16, 0x4000
	v_lshl_add_u64 v[64:65], v[20:21], 0, s[26:27]
	global_load_dwordx4 v[40:43], v[56:57], off
	global_load_dwordx4 v[94:97], v[64:65], off
	s_add_i32 s16, s14, 64
	s_and_b32 s16, s16, 0x1e0
	v_lshl_add_u32 v23, s16, 1, v19
	ds_read_b128 v[110:113], v23 offset:4096
	ds_read_b128 v[114:117], v23 offset:20736
	s_setprio 1
	s_waitcnt vmcnt(17) lgkmcnt(1)
	v_mfma_f32_16x16x32_f16 v[102:105], v[44:47], v[110:113], v[102:105]
	s_waitcnt lgkmcnt(0)
	v_mfma_f32_16x16x32_f16 v[28:31], v[44:47], v[114:117], v[28:31]
	s_waitcnt vmcnt(16)
	v_mfma_f32_16x16x32_f16 v[36:39], v[48:51], v[110:113], v[36:39]
	v_mfma_f32_16x16x32_f16 v[32:35], v[48:51], v[114:117], v[32:35]
	s_setprio 0
	s_add_i32 s16, s13, 0x2c0
	s_and_b32 s17, s16, 0x3c0
	s_lshl_b32 s26, s17, 4
	s_lshl_b32 s16, s16, 4
	v_lshl_add_u64 v[56:57], v[20:21], 0, s[26:27]
	s_or_b32 s26, s16, 0x4000
	v_lshl_add_u64 v[64:65], v[20:21], 0, s[26:27]
	global_load_dwordx4 v[44:47], v[56:57], off
	global_load_dwordx4 v[48:51], v[64:65], off
	s_add_i32 s16, s14, 0x60
	s_and_b32 s16, s16, 0x1e0
	v_lshl_add_u32 v23, s16, 1, v19
	ds_read_b128 v[110:113], v23 offset:4096
	ds_read_b128 v[114:117], v23 offset:20736
	s_setprio 1
	s_waitcnt vmcnt(17) lgkmcnt(1)
	v_mfma_f32_16x16x32_f16 v[102:105], v[52:55], v[110:113], v[102:105]
	s_waitcnt lgkmcnt(0)
	v_mfma_f32_16x16x32_f16 v[28:31], v[52:55], v[114:117], v[28:31]
	s_waitcnt vmcnt(16)
	v_mfma_f32_16x16x32_f16 v[36:39], v[60:63], v[110:113], v[36:39]
	v_mfma_f32_16x16x32_f16 v[32:35], v[60:63], v[114:117], v[32:35]
	s_setprio 0
	s_add_i32 s16, s13, 0x300
	s_and_b32 s17, s16, 0x3c0
	s_lshl_b32 s26, s17, 4
	s_lshl_b32 s16, s16, 4
	v_lshl_add_u64 v[56:57], v[20:21], 0, s[26:27]
	s_or_b32 s26, s16, 0x4000
	v_lshl_add_u64 v[64:65], v[20:21], 0, s[26:27]
	global_load_dwordx4 v[52:55], v[56:57], off
	global_load_dwordx4 v[60:63], v[64:65], off
	s_add_i32 s16, s14, 0x80
	s_and_b32 s16, s16, 0x1e0
	v_lshl_add_u32 v23, s16, 1, v19
	ds_read_b128 v[110:113], v23 offset:4096
	ds_read_b128 v[114:117], v23 offset:20736
	s_setprio 1
	s_waitcnt vmcnt(17) lgkmcnt(1)
	v_mfma_f32_16x16x32_f16 v[102:105], v[68:71], v[110:113], v[102:105]
	s_waitcnt lgkmcnt(0)
	v_mfma_f32_16x16x32_f16 v[28:31], v[68:71], v[114:117], v[28:31]
	s_waitcnt vmcnt(16)
	v_mfma_f32_16x16x32_f16 v[36:39], v[72:75], v[110:113], v[36:39]
	v_mfma_f32_16x16x32_f16 v[32:35], v[72:75], v[114:117], v[32:35]
	s_setprio 0
	s_add_i32 s16, s13, 0x340
	s_and_b32 s17, s16, 0x3c0
	s_lshl_b32 s26, s17, 4
	s_lshl_b32 s16, s16, 4
	v_lshl_add_u64 v[56:57], v[20:21], 0, s[26:27]
	s_or_b32 s26, s16, 0x4000
	v_lshl_add_u64 v[64:65], v[20:21], 0, s[26:27]
	global_load_dwordx4 v[68:71], v[56:57], off
	global_load_dwordx4 v[72:75], v[64:65], off
	s_add_i32 s16, s14, 0xa0
	s_and_b32 s16, s16, 0x1e0
	v_lshl_add_u32 v23, s16, 1, v19
	ds_read_b128 v[110:113], v23 offset:4096
	ds_read_b128 v[114:117], v23 offset:20736
	s_setprio 1
	s_waitcnt vmcnt(17) lgkmcnt(1)
	v_mfma_f32_16x16x32_f16 v[102:105], v[76:79], v[110:113], v[102:105]
	s_waitcnt lgkmcnt(0)
	v_mfma_f32_16x16x32_f16 v[28:31], v[76:79], v[114:117], v[28:31]
	s_waitcnt vmcnt(16)
	v_mfma_f32_16x16x32_f16 v[36:39], v[82:85], v[110:113], v[36:39]
	v_mfma_f32_16x16x32_f16 v[32:35], v[82:85], v[114:117], v[32:35]
	s_setprio 0
	s_add_i32 s16, s13, 0x380
	s_and_b32 s17, s16, 0x3c0
	s_lshl_b32 s26, s17, 4
	s_lshl_b32 s16, s16, 4
	v_lshl_add_u64 v[56:57], v[20:21], 0, s[26:27]
	s_or_b32 s26, s16, 0x4000
	v_lshl_add_u64 v[64:65], v[20:21], 0, s[26:27]
	global_load_dwordx4 v[76:79], v[56:57], off
	global_load_dwordx4 v[82:85], v[64:65], off
	s_add_i32 s16, s14, 0xc0
	s_and_b32 s16, s16, 0x1e0
	v_lshl_add_u32 v23, s16, 1, v19
	ds_read_b128 v[110:113], v23 offset:4096
	ds_read_b128 v[114:117], v23 offset:20736
	s_setprio 1
	s_waitcnt vmcnt(17) lgkmcnt(1)
	v_mfma_f32_16x16x32_f16 v[102:105], v[14:17], v[110:113], v[102:105]
	s_waitcnt lgkmcnt(0)
	v_mfma_f32_16x16x32_f16 v[14:17], v[14:17], v[114:117], v[28:31]
	s_waitcnt vmcnt(16)
	v_mfma_f32_16x16x32_f16 v[28:31], v[10:13], v[110:113], v[36:39]
	v_mfma_f32_16x16x32_f16 v[10:13], v[10:13], v[114:117], v[32:35]
	s_setprio 0
	s_addk_i32 s13, 0x3c0
	s_and_b32 s16, s13, 0x3c0
	s_lshl_b32 s26, s16, 4
	s_lshl_b32 s13, s13, 4
	v_lshl_add_u64 v[56:57], v[20:21], 0, s[26:27]
	s_or_b32 s26, s13, 0x4000
	v_lshl_add_u64 v[20:21], v[20:21], 0, s[26:27]
	global_load_dwordx4 v[32:35], v[56:57], off
	global_load_dwordx4 v[36:39], v[20:21], off
	s_add_i32 s13, s14, 0xe0
	s_and_b32 s13, s13, 0x1e0
	v_lshl_add_u32 v20, s13, 1, v19
	ds_read_b128 v[110:113], v20 offset:4096
	ds_read_b128 v[114:117], v20 offset:20736
	s_setprio 1
	s_waitcnt vmcnt(17) lgkmcnt(1)
	v_mfma_f32_16x16x32_f16 v[102:105], v[6:9], v[110:113], v[102:105]
	s_waitcnt lgkmcnt(0)
	v_mfma_f32_16x16x32_f16 v[6:9], v[6:9], v[114:117], v[14:17]
	s_waitcnt vmcnt(16)
	v_mfma_f32_16x16x32_f16 v[14:17], v[2:5], v[110:113], v[28:31]
	v_mfma_f32_16x16x32_f16 v[2:5], v[2:5], v[114:117], v[10:13]
	s_setprio 0
	v_add_u32_e32 v20, s15, v19
	s_nop 0
	ds_read_b128 v[10:13], v20 offset:4096
	ds_read_b128 v[28:31], v20 offset:20736
	s_setprio 1
	s_waitcnt vmcnt(15) lgkmcnt(1)
	v_mfma_f32_16x16x32_f16 v[102:105], v[86:89], v[10:13], v[102:105]
	s_waitcnt lgkmcnt(0)
	v_mfma_f32_16x16x32_f16 v[6:9], v[86:89], v[28:31], v[6:9]
	s_waitcnt vmcnt(14)
	v_mfma_f32_16x16x32_f16 v[10:13], v[90:93], v[10:13], v[14:17]
	v_mfma_f32_16x16x32_f16 v[2:5], v[90:93], v[28:31], v[2:5]
	s_setprio 0
	s_add_i32 s13, s14, 0x120
	s_and_b32 s13, s13, 0x1e0
	v_lshl_add_u32 v20, s13, 1, v19
	ds_read_b128 v[14:17], v20 offset:4096
	ds_read_b128 v[28:31], v20 offset:20736
	s_setprio 1
	s_waitcnt vmcnt(13) lgkmcnt(1)
	v_mfma_f32_16x16x32_f16 v[86:89], v[98:101], v[14:17], v[102:105]
	s_waitcnt lgkmcnt(0)
	v_mfma_f32_16x16x32_f16 v[6:9], v[98:101], v[28:31], v[6:9]
	s_waitcnt vmcnt(12)
	v_mfma_f32_16x16x32_f16 v[10:13], v[106:109], v[14:17], v[10:13]
	v_mfma_f32_16x16x32_f16 v[2:5], v[106:109], v[28:31], v[2:5]
	s_setprio 0
	s_add_i32 s13, s14, 0x140
	s_and_b32 s13, s13, 0x1e0
	v_lshl_add_u32 v20, s13, 1, v19
	ds_read_b128 v[14:17], v20 offset:4096
	ds_read_b128 v[28:31], v20 offset:20736
	s_setprio 1
	s_waitcnt vmcnt(11) lgkmcnt(1)
	v_mfma_f32_16x16x32_f16 v[86:89], v[40:43], v[14:17], v[86:89]
	s_waitcnt lgkmcnt(0)
	v_mfma_f32_16x16x32_f16 v[6:9], v[40:43], v[28:31], v[6:9]
	s_waitcnt vmcnt(10)
	v_mfma_f32_16x16x32_f16 v[10:13], v[94:97], v[14:17], v[10:13]
	v_mfma_f32_16x16x32_f16 v[2:5], v[94:97], v[28:31], v[2:5]
	s_setprio 0
	s_add_i32 s13, s14, 0x160
	s_and_b32 s13, s13, 0x1e0
	v_lshl_add_u32 v20, s13, 1, v19
	ds_read_b128 v[14:17], v20 offset:4096
	ds_read_b128 v[28:31], v20 offset:20736
	s_setprio 1
	s_waitcnt vmcnt(9) lgkmcnt(1)
	v_mfma_f32_16x16x32_f16 v[40:43], v[44:47], v[14:17], v[86:89]
	s_waitcnt lgkmcnt(0)
	v_mfma_f32_16x16x32_f16 v[6:9], v[44:47], v[28:31], v[6:9]
	s_waitcnt vmcnt(8)
	v_mfma_f32_16x16x32_f16 v[10:13], v[48:51], v[14:17], v[10:13]
	v_mfma_f32_16x16x32_f16 v[2:5], v[48:51], v[28:31], v[2:5]
	s_setprio 0
	s_add_i32 s13, s14, 0x180
	s_and_b32 s13, s13, 0x1e0
	v_lshl_add_u32 v20, s13, 1, v19
	ds_read_b128 v[14:17], v20 offset:4096
	ds_read_b128 v[28:31], v20 offset:20736
	s_setprio 1
	s_waitcnt vmcnt(7) lgkmcnt(1)
	v_mfma_f32_16x16x32_f16 v[40:43], v[52:55], v[14:17], v[40:43]
	s_waitcnt lgkmcnt(0)
	v_mfma_f32_16x16x32_f16 v[6:9], v[52:55], v[28:31], v[6:9]
	s_waitcnt vmcnt(6)
	v_mfma_f32_16x16x32_f16 v[10:13], v[60:63], v[14:17], v[10:13]
	v_mfma_f32_16x16x32_f16 v[2:5], v[60:63], v[28:31], v[2:5]
	s_setprio 0
	s_add_i32 s13, s14, 0x1a0
	s_and_b32 s13, s13, 0x1e0
	v_lshl_add_u32 v20, s13, 1, v19
	ds_read_b128 v[14:17], v20 offset:4096
	ds_read_b128 v[28:31], v20 offset:20736
	s_setprio 1
	s_waitcnt vmcnt(5) lgkmcnt(1)
	v_mfma_f32_16x16x32_f16 v[40:43], v[68:71], v[14:17], v[40:43]
	s_waitcnt lgkmcnt(0)
	v_mfma_f32_16x16x32_f16 v[6:9], v[68:71], v[28:31], v[6:9]
	s_waitcnt vmcnt(4)
	v_mfma_f32_16x16x32_f16 v[10:13], v[72:75], v[14:17], v[10:13]
	v_mfma_f32_16x16x32_f16 v[2:5], v[72:75], v[28:31], v[2:5]
	s_setprio 0
	s_add_i32 s13, s14, 0x1c0
	s_and_b32 s13, s13, 0x1e0
	v_lshl_add_u32 v20, s13, 1, v19
	ds_read_b128 v[14:17], v20 offset:4096
	ds_read_b128 v[28:31], v20 offset:20736
	s_setprio 1
	s_waitcnt vmcnt(3) lgkmcnt(1)
	v_mfma_f32_16x16x32_f16 v[40:43], v[76:79], v[14:17], v[40:43]
	s_waitcnt lgkmcnt(0)
	v_mfma_f32_16x16x32_f16 v[6:9], v[76:79], v[28:31], v[6:9]
	s_waitcnt vmcnt(2)
	v_mfma_f32_16x16x32_f16 v[10:13], v[82:85], v[14:17], v[10:13]
	v_mfma_f32_16x16x32_f16 v[2:5], v[82:85], v[28:31], v[2:5]
	s_setprio 0
	s_addk_i32 s14, 0x1e0
	s_and_b32 s13, s14, 0x1e0
	v_lshl_add_u32 v20, s13, 1, v19
	ds_read_b128 v[14:17], v20 offset:4096
	ds_read_b128 v[28:31], v20 offset:20736
	s_setprio 1
	s_waitcnt vmcnt(1) lgkmcnt(1)
	v_mfma_f32_16x16x32_f16 v[40:43], v[32:35], v[14:17], v[40:43]
	s_waitcnt lgkmcnt(0)
	v_mfma_f32_16x16x32_f16 v[6:9], v[32:35], v[28:31], v[6:9]
	s_waitcnt vmcnt(0)
	v_mfma_f32_16x16x32_f16 v[10:13], v[36:39], v[14:17], v[10:13]
	v_mfma_f32_16x16x32_f16 v[2:5], v[36:39], v[28:31], v[2:5]
	s_setprio 0
	v_add_u32_e32 v19, v19, v22
	v_lshlrev_b32_e32 v20, 15, v118
	v_mov_b32_e32 v21, v67
	s_bfe_u32 s22, s2, 0x30003
	v_lshl_add_u64 v[20:21], s[10:11], 0, v[20:21]
	s_lshl_b32 s26, s22, 10
	v_lshl_add_u64 v[64:65], v[20:21], 0, v[58:59]
	v_lshl_add_u64 v[52:53], v[64:65], 0, s[26:27]
	v_add_co_u32_e32 v76, vcc, s29, v52
	s_lshl_b32 s53, s22, 6
	s_nop 0
	v_addc_co_u32_e32 v77, vcc, 0, v53, vcc
	s_mov_b32 s14, 0x14000
	v_mov_b32_e32 v22, 0x14000
	v_mul_u32_u24_e32 v23, 0x210, v81
	s_add_i32 s38, s53, 64
	v_lshlrev_b32_e32 v83, 2, v118
	s_movk_i32 s16, 0x1040
	s_movk_i32 s18, 0x840
	v_lshl_or_b32 v1, v1, 3, v22
	v_add3_u32 v84, v23, v18, s14
	s_and_b32 s14, s38, 0x1c0
	s_movk_i32 s20, 0x210
	s_mov_b32 s19, s27
	v_mad_u32_u24 v56, v118, s16, v58
	v_or_b32_e32 v22, 1, v83
	v_mad_u32_u24 v98, v118, s18, v1
	s_lshl_b32 s18, s14, 4
	v_mad_u32_u24 v99, v22, s12, v58
	v_mad_u32_u24 v85, v22, s20, v1
	v_lshl_add_u64 v[54:55], v[64:65], 0, s[18:19]
	s_add_i32 s12, s53, 0xc0
	s_and_b32 s2, s3, 0x7ffffff
	s_lshl_b32 s3, s22, 5
	s_and_b32 s39, s12, 0x1c0
	s_lshl_b32 s14, s39, 4
	s_add_i32 s39, s3, 32
	s_and_b32 s39, s39, 0xe0
	v_lshl_add_u32 v82, s39, 1, v84
	s_add_i32 s11, s53, 0x80
	s_lshl_b32 s16, s38, 4
	s_mov_b32 s21, s27
	s_and_b32 s30, s11, 0x1c0
	s_lshl_b32 s11, s11, 4
	s_or_b32 s20, s16, 0x2000
	s_mov_b32 s23, s27
	s_mov_b32 s31, s27
	s_mov_b32 s35, s27
	s_or_b32 s22, s16, 0x6000
	s_lshl_b32 s30, s30, 4
	s_or_b32 s34, s11, 0x2000
	v_lshl_add_u64 v[26:27], v[64:65], 0, s[20:21]
	v_lshl_add_u64 v[28:29], v[64:65], 0, s[22:23]
	v_lshl_add_u64 v[30:31], v[64:65], 0, s[30:31]
	v_lshl_add_u64 v[32:33], v[64:65], 0, s[34:35]
	s_mov_b64 s[40:41], 0x40000
	v_lshl_add_u64 v[60:61], v[64:65], 0, s[40:41]
	s_mov_b32 s37, s27
	s_or_b32 s36, s11, 0x6000
	v_lshl_add_u64 v[74:75], v[64:65], 0, s[36:37]
	s_mov_b32 s15, s27
	s_lshl_b32 s12, s12, 4
	v_lshl_add_u64 v[70:71], v[64:65], 0, s[14:15]
	s_mov_b32 s17, s27
	s_or_b32 s16, s12, 0x2000
	s_mov_b32 s13, s27
	s_or_b32 s12, s12, 0x6000
	v_lshl_add_u64 v[72:73], v[64:65], 0, s[16:17]
	v_lshl_add_u64 v[68:69], v[64:65], 0, s[12:13]
	v_add_u32_e32 v1, s53, v84
	s_xor_b32 s10, s26, 0x1000
	s_mov_b32 s11, s27
	s_mov_b32 s49, s27
	s_mov_b32 s51, s27
	s_mov_b32 s47, s27
	v_pk_add_f32 v[14:15], v[180:181], v[40:41]
	v_pk_add_f32 v[16:17], v[182:183], v[42:43]
	v_pk_add_f32 v[10:11], v[184:185], v[10:11]
	v_pk_add_f32 v[12:13], v[186:187], v[12:13]
	v_pk_add_f32 v[6:7], v[188:189], v[6:7]
	v_pk_add_f32 v[8:9], v[190:191], v[8:9]
	v_pk_add_f32 v[2:3], v[192:193], v[2:3]
	v_pk_add_f32 v[4:5], v[194:195], v[4:5]
	ds_write_b128 v19, v[14:17] offset:37376
	ds_write_b128 v19, v[10:13] offset:37440
	ds_write_b128 v19, v[6:9] offset:54016
	ds_write_b128 v19, v[2:5] offset:54080
	v_mov_b64_e32 v[34:35], v[204:205]
	v_mov_b64_e32 v[36:37], v[206:207]
	v_mov_b64_e32 v[38:39], v[208:209]
	v_mov_b64_e32 v[40:41], v[210:211]
	v_add_co_u32_e32 v2, vcc, s52, v52
	s_waitcnt lgkmcnt(0)
	s_nop 0
	v_addc_co_u32_e32 v3, vcc, 0, v53, vcc
	v_add_co_u32_e32 v4, vcc, s33, v52
	s_barrier
	s_nop 0
	v_addc_co_u32_e32 v5, vcc, 0, v53, vcc
	global_load_dwordx4 v[14:17], v[2:3], off
	global_load_dwordx4 v[18:21], v[4:5], off
	global_load_dwordx4 v[22:25], v[52:53], off
	global_load_dwordx4 v[10:13], v[54:55], off
	ds_read_b128 v[2:5], v56 offset:37376
	ds_read_b128 v[6:9], v99 offset:37376
	v_add_co_u32_e32 v78, vcc, s52, v54
	s_mov_b32 s43, s27
	s_waitcnt lgkmcnt(1)
	v_add_f32_e32 v42, v2, v3
	v_add_f32_e32 v42, v42, v4
	v_add_f32_e32 v42, v42, v5
	v_addc_co_u32_e32 v79, vcc, 0, v55, vcc
	s_nop 0
	v_add_f32_dpp v42, v42, v42 quad_perm:[1,0,3,2] row_mask:0xf bank_mask:0xf bound_ctrl:1
	s_mov_b32 s45, s27
	s_mov_b32 s41, s27
	v_add_f32_dpp v42, v42, v42 quad_perm:[2,3,0,1] row_mask:0xf bank_mask:0xf bound_ctrl:1
	v_lshl_add_u64 v[62:63], v[64:65], 0, s[10:11]
	v_lshl_add_u64 v[58:59], s[4:5], 0, v[58:59]
	v_add_f32_dpp v42, v42, v42 row_half_mirror row_mask:0xf bank_mask:0xf bound_ctrl:1
	v_lshl_add_u64 v[152:153], v[60:61], 0, s[26:27]
	v_lshl_add_u64 v[154:155], v[60:61], 0, s[18:19]
	v_add_f32_dpp v42, v42, v42 row_mirror row_mask:0xf bank_mask:0xf bound_ctrl:1
	v_lshl_add_u64 v[156:157], v[60:61], 0, s[20:21]
	v_readlane_b32 s8, v42, 16
	v_readlane_b32 s9, v42, 48
	v_readlane_b32 s6, v42, 0
	v_readlane_b32 s7, v42, 32
	v_mov_b32_e32 v42, s8
	v_mov_b32_e32 v43, s9
	v_pk_add_f32 v[42:43], s[6:7], v[42:43]
	s_mov_b32 s6, 0x3b800000
	v_add_f32_e32 v42, v42, v43
	v_mul_f32_e32 v42, 0x3b800000, v42
	v_pk_add_f32 v[86:87], v[2:3], v[42:43] op_sel_hi:[1,0] neg_lo:[0,1] neg_hi:[0,1]
	v_pk_add_f32 v[88:89], v[4:5], v[42:43] op_sel_hi:[1,0] neg_lo:[0,1] neg_hi:[0,1]
	v_pk_mul_f32 v[42:43], v[86:87], v[86:87]
	v_pk_mul_f32 v[44:45], v[88:89], v[88:89]
	v_add_f32_e32 v42, v42, v43
	v_add_f32_e32 v42, v44, v42
	s_waitcnt lgkmcnt(0)
	v_add_f32_e32 v44, v6, v7
	v_add_f32_e32 v42, v45, v42
	v_add_f32_e32 v44, v44, v8
	v_add_f32_e32 v44, v44, v9
	v_add_f32_dpp v42, v42, v42 quad_perm:[1,0,3,2] row_mask:0xf bank_mask:0xf bound_ctrl:1
	v_lshl_add_u64 v[158:159], v[60:61], 0, s[22:23]
	v_add_f32_dpp v44, v44, v44 quad_perm:[1,0,3,2] row_mask:0xf bank_mask:0xf bound_ctrl:1
	v_add_f32_dpp v42, v42, v42 quad_perm:[2,3,0,1] row_mask:0xf bank_mask:0xf bound_ctrl:1
	v_lshl_add_u64 v[160:161], v[60:61], 0, s[30:31]
	v_add_f32_dpp v44, v44, v44 quad_perm:[2,3,0,1] row_mask:0xf bank_mask:0xf bound_ctrl:1
	v_add_f32_dpp v42, v42, v42 row_half_mirror row_mask:0xf bank_mask:0xf bound_ctrl:1
	v_lshl_add_u64 v[162:163], v[60:61], 0, s[34:35]
	v_add_f32_dpp v44, v44, v44 row_half_mirror row_mask:0xf bank_mask:0xf bound_ctrl:1
	v_add_f32_dpp v42, v42, v42 row_mirror row_mask:0xf bank_mask:0xf bound_ctrl:1
	v_lshl_add_u64 v[164:165], v[60:61], 0, s[36:37]
	v_readlane_b32 s7, v42, 16
	v_readlane_b32 s39, v42, 48
	v_add_f32_dpp v44, v44, v44 row_mirror row_mask:0xf bank_mask:0xf bound_ctrl:1
	v_readlane_b32 s8, v42, 0
	v_readlane_b32 s9, v42, 32
	v_mov_b32_e32 v42, s7
	v_mov_b32_e32 v43, s39
	v_readlane_b32 s7, v44, 16
	v_readlane_b32 s39, v44, 48
	v_pk_add_f32 v[42:43], s[8:9], v[42:43]
	v_readlane_b32 s8, v44, 0
	v_readlane_b32 s9, v44, 32
	v_mov_b32_e32 v44, s7
	v_mov_b32_e32 v45, s39
	v_pk_add_f32 v[44:45], s[8:9], v[44:45]
	s_nop 0
	v_add_f32_e32 v44, v44, v45
	v_mul_f32_e32 v44, 0x3b800000, v44
	v_pk_add_f32 v[90:91], v[6:7], v[44:45] op_sel_hi:[1,0] neg_lo:[0,1] neg_hi:[0,1]
	v_pk_add_f32 v[92:93], v[8:9], v[44:45] op_sel_hi:[1,0] neg_lo:[0,1] neg_hi:[0,1]
	v_pk_mul_f32 v[46:47], v[90:91], v[90:91]
	v_pk_mul_f32 v[44:45], v[92:93], v[92:93]
	v_add_f32_e32 v46, v46, v47
	v_add_f32_e32 v44, v44, v46
	v_add_f32_e32 v44, v45, v44
	v_mov_b32_e32 v47, v42
	s_nop 0
	v_add_f32_dpp v44, v44, v44 quad_perm:[1,0,3,2] row_mask:0xf bank_mask:0xf bound_ctrl:1
	s_nop 1
	v_add_f32_dpp v44, v44, v44 quad_perm:[2,3,0,1] row_mask:0xf bank_mask:0xf bound_ctrl:1
	s_nop 1
	v_add_f32_dpp v44, v44, v44 row_half_mirror row_mask:0xf bank_mask:0xf bound_ctrl:1
	s_nop 1
	v_add_f32_dpp v44, v44, v44 row_mirror row_mask:0xf bank_mask:0xf bound_ctrl:1
	s_nop 0
	v_readlane_b32 s7, v44, 16
	v_readlane_b32 s39, v44, 48
	v_readlane_b32 s8, v44, 0
	v_readlane_b32 s9, v44, 32
	v_mov_b32_e32 v44, s7
	v_mov_b32_e32 v45, s39
	v_pk_add_f32 v[44:45], s[8:9], v[44:45]
	s_mov_b32 s8, 0x3727c5ac
	v_mov_b32_e32 v46, v44
	v_mov_b32_e32 v42, v45
	v_pk_add_f32 v[42:43], v[46:47], v[42:43]
	v_mov_b64_e32 v[94:95], s[8:9]
	v_pk_fma_f32 v[96:97], v[42:43], s[6:7], v[94:95] op_sel_hi:[1,0,0]
	s_mov_b32 s7, 0x800000
	v_mul_f32_e32 v42, 0x4b800000, v97
	v_cmp_gt_f32_e32 vcc, s7, v97
	s_nop 1
	v_cndmask_b32_e32 v42, v97, v42, vcc
	v_rsq_f32_e32 v97, v42
	global_load_dwordx4 v[54:57], v[26:27], off
	global_load_dwordx4 v[50:53], v[28:29], off
	global_load_dwordx4 v[46:49], v[30:31], off
	global_load_dwordx4 v[42:45], v[32:33], off
	v_mul_f32_e32 v26, 0x45800000, v97
	v_cndmask_b32_e32 v26, v97, v26, vcc
	v_pk_mul_f32 v[28:29], v[86:87], v[26:27] op_sel_hi:[1,0]
	v_cmp_gt_f32_e32 vcc, s7, v96
	s_waitcnt vmcnt(8)
	v_pk_fma_f32 v[28:29], v[34:35], v[28:29], v[38:39]
	v_pk_mul_f32 v[26:27], v[88:89], v[26:27] op_sel_hi:[1,0]
	v_cvt_pk_f16_f32 v28, v28, v29
	v_mul_f32_e32 v29, 0x4b800000, v96
	v_cndmask_b32_e32 v29, v96, v29, vcc
	v_rsq_f32_e32 v32, v29
	v_pk_fma_f32 v[26:27], v[36:37], v[26:27], v[40:41]
	s_nop 0
	v_cvt_pk_f16_f32 v29, v26, v27
	v_mul_f32_e32 v26, 0x45800000, v32
	v_cndmask_b32_e32 v26, v32, v26, vcc
	ds_write_b64 v98, v[28:29]
	v_pk_mul_f32 v[28:29], v[90:91], v[26:27] op_sel_hi:[1,0]
	v_pk_mul_f32 v[26:27], v[92:93], v[26:27] op_sel_hi:[1,0]
	v_pk_fma_f32 v[28:29], v[34:35], v[28:29], v[38:39]
	v_pk_fma_f32 v[26:27], v[36:37], v[26:27], v[40:41]
	v_cvt_pk_f16_f32 v28, v28, v29
	v_cvt_pk_f16_f32 v29, v26, v27
	ds_write_b64 v85, v[28:29]
	ds_read_b128 v[26:29], v99 offset:38416
	v_add_co_u32_e32 v102, vcc, s52, v30
	s_nop 1
	v_addc_co_u32_e32 v103, vcc, 0, v31, vcc
	ds_read_b128 v[30:33], v99 offset:39456
	s_waitcnt lgkmcnt(1)
	v_add_f32_e32 v86, v26, v27
	v_add_f32_e32 v86, v86, v28
	v_add_f32_e32 v86, v86, v29
	s_nop 1
	v_add_f32_dpp v86, v86, v86 quad_perm:[1,0,3,2] row_mask:0xf bank_mask:0xf bound_ctrl:1
	s_nop 1
	v_add_f32_dpp v86, v86, v86 quad_perm:[2,3,0,1] row_mask:0xf bank_mask:0xf bound_ctrl:1
	s_nop 1
	v_add_f32_dpp v86, v86, v86 row_half_mirror row_mask:0xf bank_mask:0xf bound_ctrl:1
	s_nop 1
	v_add_f32_dpp v86, v86, v86 row_mirror row_mask:0xf bank_mask:0xf bound_ctrl:1
	s_nop 0
	v_readlane_b32 s39, v86, 16
	v_readlane_b32 s40, v86, 48
	v_readlane_b32 s8, v86, 0
	v_readlane_b32 s9, v86, 32
	v_mov_b32_e32 v86, s39
	v_mov_b32_e32 v87, s40
	v_pk_add_f32 v[86:87], s[8:9], v[86:87]
	s_nop 0
	v_add_f32_e32 v86, v86, v87
	v_mul_f32_e32 v86, 0x3b800000, v86
	v_pk_add_f32 v[104:105], v[26:27], v[86:87] op_sel_hi:[1,0] neg_lo:[0,1] neg_hi:[0,1]
	v_pk_add_f32 v[106:107], v[28:29], v[86:87] op_sel_hi:[1,0] neg_lo:[0,1] neg_hi:[0,1]
	v_pk_mul_f32 v[88:89], v[104:105], v[104:105]
	v_pk_mul_f32 v[86:87], v[106:107], v[106:107]
	v_add_f32_e32 v88, v88, v89
	v_add_f32_e32 v86, v86, v88
	s_waitcnt lgkmcnt(0)
	v_add_f32_e32 v88, v30, v31
	v_add_f32_e32 v86, v87, v86
	v_add_f32_e32 v88, v88, v32
	v_add_f32_e32 v88, v88, v33
	v_add_f32_dpp v86, v86, v86 quad_perm:[1,0,3,2] row_mask:0xf bank_mask:0xf bound_ctrl:1
	s_nop 0
	v_add_f32_dpp v88, v88, v88 quad_perm:[1,0,3,2] row_mask:0xf bank_mask:0xf bound_ctrl:1
	v_add_f32_dpp v86, v86, v86 quad_perm:[2,3,0,1] row_mask:0xf bank_mask:0xf bound_ctrl:1
	s_nop 0
	v_add_f32_dpp v88, v88, v88 quad_perm:[2,3,0,1] row_mask:0xf bank_mask:0xf bound_ctrl:1
	v_add_f32_dpp v86, v86, v86 row_half_mirror row_mask:0xf bank_mask:0xf bound_ctrl:1
	s_nop 0
	v_add_f32_dpp v88, v88, v88 row_half_mirror row_mask:0xf bank_mask:0xf bound_ctrl:1
	v_add_f32_dpp v86, v86, v86 row_mirror row_mask:0xf bank_mask:0xf bound_ctrl:1
	s_nop 0
	v_readlane_b32 s39, v86, 16
	v_readlane_b32 s40, v86, 48
	v_add_f32_dpp v88, v88, v88 row_mirror row_mask:0xf bank_mask:0xf bound_ctrl:1
	v_readlane_b32 s8, v86, 0
	v_readlane_b32 s9, v86, 32
	v_mov_b32_e32 v86, s39
	v_mov_b32_e32 v87, s40
	v_readlane_b32 s39, v88, 16
	v_readlane_b32 s40, v88, 48
	v_pk_add_f32 v[86:87], s[8:9], v[86:87]
	v_readlane_b32 s8, v88, 0
	v_readlane_b32 s9, v88, 32
	v_mov_b32_e32 v88, s39
	v_mov_b32_e32 v89, s40
	v_pk_add_f32 v[88:89], s[8:9], v[88:89]
	s_nop 0
	v_add_f32_e32 v88, v88, v89
	v_mul_f32_e32 v88, 0x3b800000, v88
	v_pk_add_f32 v[108:109], v[30:31], v[88:89] op_sel_hi:[1,0] neg_lo:[0,1] neg_hi:[0,1]
	v_pk_add_f32 v[110:111], v[32:33], v[88:89] op_sel_hi:[1,0] neg_lo:[0,1] neg_hi:[0,1]
	v_pk_mul_f32 v[90:91], v[108:109], v[108:109]
	v_pk_mul_f32 v[88:89], v[110:111], v[110:111]
	v_add_f32_e32 v90, v90, v91
	v_add_f32_e32 v88, v88, v90
	v_add_f32_e32 v88, v89, v88
	v_mov_b32_e32 v91, v86
	s_nop 0
	v_add_f32_dpp v88, v88, v88 quad_perm:[1,0,3,2] row_mask:0xf bank_mask:0xf bound_ctrl:1
	s_nop 1
	v_add_f32_dpp v88, v88, v88 quad_perm:[2,3,0,1] row_mask:0xf bank_mask:0xf bound_ctrl:1
	s_nop 1
	v_add_f32_dpp v88, v88, v88 row_half_mirror row_mask:0xf bank_mask:0xf bound_ctrl:1
	s_nop 1
	v_add_f32_dpp v88, v88, v88 row_mirror row_mask:0xf bank_mask:0xf bound_ctrl:1
	s_nop 0
	v_readlane_b32 s39, v88, 16
	v_readlane_b32 s40, v88, 48
	v_readlane_b32 s8, v88, 0
	v_readlane_b32 s9, v88, 32
	v_mov_b32_e32 v88, s39
	v_mov_b32_e32 v89, s40
	v_pk_add_f32 v[88:89], s[8:9], v[88:89]
	s_mov_b32 s9, s27
	v_mov_b32_e32 v90, v88
	v_mov_b32_e32 v86, v89
	v_pk_add_f32 v[86:87], v[90:91], v[86:87]
	s_mov_b32 s39, s27
	v_pk_fma_f32 v[112:113], v[86:87], s[6:7], v[94:95] op_sel_hi:[1,0,0]
	s_add_i32 s6, s53, 0x140
	v_mul_f32_e32 v86, 0x4b800000, v113
	v_cmp_gt_f32_e32 vcc, s7, v113
	s_nop 1
	v_cndmask_b32_e32 v86, v113, v86, vcc
	v_rsq_f32_e32 v113, v86
	global_load_dwordx4 v[86:89], v[78:79], off
	global_load_dwordx4 v[90:93], v[102:103], off
	global_load_dwordx4 v[94:97], v[76:77], off
	global_load_dwordx4 v[98:101], v[74:75], off
	v_mul_f32_e32 v74, 0x45800000, v113
	v_cndmask_b32_e32 v74, v113, v74, vcc
	v_pk_mul_f32 v[76:77], v[104:105], v[74:75] op_sel_hi:[1,0]
	v_mul_f32_e32 v75, 0x4b800000, v112
	v_cmp_gt_f32_e32 vcc, s7, v112
	v_pk_fma_f32 v[76:77], v[34:35], v[76:77], v[38:39]
	s_and_b32 s7, s6, 0x1c0
	v_cndmask_b32_e32 v75, v112, v75, vcc
	v_rsq_f32_e32 v78, v75
	v_pk_mul_f32 v[74:75], v[106:107], v[74:75] op_sel_hi:[1,0]
	v_cvt_pk_f16_f32 v76, v76, v77
	v_pk_fma_f32 v[74:75], v[36:37], v[74:75], v[40:41]
	s_lshl_b32 s6, s6, 4
	v_cvt_pk_f16_f32 v77, v74, v75
	v_mul_f32_e32 v74, 0x45800000, v78
	v_cndmask_b32_e32 v74, v78, v74, vcc
	v_pk_mul_f32 v[78:79], v[108:109], v[74:75] op_sel_hi:[1,0]
	s_or_b32 s50, s6, 0x2000
	v_pk_fma_f32 v[34:35], v[34:35], v[78:79], v[38:39]
	v_pk_mul_f32 v[38:39], v[110:111], v[74:75] op_sel_hi:[1,0]
	v_add_co_u32_e32 v78, vcc, s52, v70
	v_pk_fma_f32 v[36:37], v[36:37], v[38:39], v[40:41]
	v_cvt_pk_f16_f32 v34, v34, v35
	v_cvt_pk_f16_f32 v35, v36, v37
	v_addc_co_u32_e32 v79, vcc, 0, v71, vcc
	ds_write2_b64 v85, v[76:77], v[34:35] offset0:66 offset1:132
	s_waitcnt lgkmcnt(0)
	s_barrier
	global_load_dwordx4 v[34:37], v[70:71], off
	global_load_dwordx4 v[38:41], v[72:73], off
	s_nop 0
	global_load_dwordx4 v[70:73], v[78:79], off
	global_load_dwordx4 v[74:77], v[68:69], off
	s_or_b32 s46, s6, 0x6000
	s_sub_i32 s6, s38, s3
	s_and_b32 s6, s6, 0xe0
	v_lshl_add_u32 v172, s6, 1, v84
	s_add_i32 s6, s53, 0x180
	s_lshl_b32 s48, s7, 4
	s_and_b32 s7, s6, 0x1c0
	s_lshl_b32 s6, s6, 4
	s_or_b32 s44, s6, 0x2000
	s_or_b32 s40, s6, 0x6000
	s_add_i32 s6, s3, 0x60
	s_and_b32 s6, s6, 0xe0
	v_lshl_add_u32 v173, s6, 1, v84
	s_add_i32 s6, s53, 0x1c0
	s_xor_b32 s53, s53, 0x100
	v_add_u32_e32 v174, s53, v84
	s_add_i32 s53, s3, 0xa0
	s_lshl_b32 s42, s7, 4
	s_and_b32 s7, s6, 0x1c0
	s_lshl_b32 s6, s6, 4
	s_and_b32 s53, s53, 0xe0
	s_lshl_b32 s8, s7, 4
	s_or_b32 s38, s6, 0x2000
	s_or_b32 s6, s6, 0x6000
	s_mov_b32 s7, s27
	v_lshl_add_u32 v175, s53, 1, v84
	s_add_i32 s53, s3, 0xc0
	s_addk_i32 s3, 0xe0
	v_lshl_add_u64 v[68:69], v[64:65], 0, s[48:49]
	v_lshl_add_u64 v[78:79], v[64:65], 0, s[50:51]
	v_lshl_add_u64 v[138:139], v[64:65], 0, s[46:47]
	v_lshl_add_u64 v[140:141], v[64:65], 0, s[42:43]
	v_lshl_add_u64 v[142:143], v[64:65], 0, s[44:45]
	v_lshl_add_u64 v[144:145], v[64:65], 0, s[40:41]
	v_lshl_add_u64 v[146:147], v[64:65], 0, s[8:9]
	v_lshl_add_u64 v[148:149], v[64:65], 0, s[38:39]
	v_lshl_add_u64 v[150:151], v[64:65], 0, s[6:7]
	s_and_b32 s53, s53, 0xe0
	s_and_b32 s3, s3, 0xe0
	v_add_u32_e32 v64, s28, v83
	v_mov_b32_e32 v65, v67
	v_lshl_add_u32 v176, s53, 1, v84
	v_lshl_add_u32 v177, s3, 1, v84
	v_lshlrev_b64 v[84:85], 10, v[64:65]
	ds_read_b128 v[102:105], v1
	ds_read_b128 v[106:109], v1 offset:8448
	v_lshl_add_u64 v[166:167], v[58:59], 0, v[84:85]
	v_or_b32_e32 v84, 1, v64
	v_mov_b32_e32 v85, v67
	v_lshlrev_b64 v[84:85], 10, v[84:85]
	v_lshl_add_u64 v[168:169], v[58:59], 0, v[84:85]
	v_or_b32_e32 v84, 2, v64
	v_mov_b32_e32 v85, v67
	v_or_b32_e32 v64, 3, v64
	v_lshlrev_b64 v[84:85], 10, v[84:85]
	v_lshlrev_b64 v[64:65], 10, v[64:65]
	v_lshl_add_u64 v[170:171], v[58:59], 0, v[84:85]
	v_lshl_add_u64 v[58:59], v[58:59], 0, v[64:65]
	s_setprio 1
	s_waitcnt vmcnt(13) lgkmcnt(1)
	v_mfma_f32_16x16x32_f16 v[110:113], v[102:105], v[22:25], 0
	s_waitcnt lgkmcnt(0)
	v_mfma_f32_16x16x32_f16 v[22:25], v[106:109], v[22:25], 0
	s_waitcnt vmcnt(5)
	v_mfma_f32_16x16x32_f16 v[114:117], v[102:105], v[94:97], 0
	v_mfma_f32_16x16x32_f16 v[94:97], v[106:109], v[94:97], 0
	v_mfma_f32_16x16x32_f16 v[118:121], v[102:105], v[14:17], 0
	v_mfma_f32_16x16x32_f16 v[14:17], v[106:109], v[14:17], 0
	v_mfma_f32_16x16x32_f16 v[102:105], v[102:105], v[18:21], 0
	v_mfma_f32_16x16x32_f16 v[18:21], v[106:109], v[18:21], 0
	s_setprio 0
	v_add_co_u32_e32 v64, vcc, s29, v62
	global_load_dwordx4 v[106:109], v[62:63], off
	s_nop 0
	v_addc_co_u32_e32 v65, vcc, 0, v63, vcc
	v_add_co_u32_e32 v84, vcc, s52, v62
	s_nop 1
	v_addc_co_u32_e32 v85, vcc, 0, v63, vcc
	v_add_co_u32_e32 v62, vcc, s33, v62
	global_load_dwordx4 v[122:125], v[64:65], off
	global_load_dwordx4 v[126:129], v[84:85], off
	v_addc_co_u32_e32 v63, vcc, 0, v63, vcc
	global_load_dwordx4 v[62:65], v[62:63], off
	ds_read_b128 v[130:133], v82
	ds_read_b128 v[134:137], v82 offset:8448
	s_setprio 1
	s_waitcnt lgkmcnt(1)
	v_mfma_f32_16x16x32_f16 v[110:113], v[130:133], v[10:13], v[110:113]
	s_waitcnt lgkmcnt(0)
	v_mfma_f32_16x16x32_f16 v[10:13], v[134:137], v[10:13], v[22:25]
	v_mfma_f32_16x16x32_f16 v[22:25], v[130:133], v[54:57], v[114:117]
	v_mfma_f32_16x16x32_f16 v[54:57], v[134:137], v[54:57], v[94:97]
	v_mfma_f32_16x16x32_f16 v[94:97], v[130:133], v[86:89], v[118:121]
	v_mfma_f32_16x16x32_f16 v[14:17], v[134:137], v[86:89], v[14:17]
	v_mfma_f32_16x16x32_f16 v[84:87], v[130:133], v[50:53], v[102:105]
	v_mfma_f32_16x16x32_f16 v[18:21], v[134:137], v[50:53], v[18:21]
	s_setprio 0
	global_load_dwordx4 v[50:53], v[68:69], off
	global_load_dwordx4 v[102:105], v[78:79], off
	v_add_co_u32_e32 v68, vcc, s52, v68
	s_nop 1
	v_addc_co_u32_e32 v69, vcc, 0, v69, vcc
	global_load_dwordx4 v[114:117], v[68:69], off
	global_load_dwordx4 v[118:121], v[138:139], off
	ds_read_b128 v[130:133], v172
	ds_read_b128 v[134:137], v172 offset:8448
	s_setprio 1
	s_waitcnt lgkmcnt(1)
	v_mfma_f32_16x16x32_f16 v[110:113], v[130:133], v[46:49], v[110:113]
	s_waitcnt lgkmcnt(0)
	v_mfma_f32_16x16x32_f16 v[10:13], v[134:137], v[46:49], v[10:13]
	v_mfma_f32_16x16x32_f16 v[22:25], v[130:133], v[42:45], v[22:25]
	v_mfma_f32_16x16x32_f16 v[42:45], v[134:137], v[42:45], v[54:57]
	v_mfma_f32_16x16x32_f16 v[46:49], v[130:133], v[90:93], v[94:97]
	v_mfma_f32_16x16x32_f16 v[14:17], v[134:137], v[90:93], v[14:17]
	s_waitcnt vmcnt(12)
	v_mfma_f32_16x16x32_f16 v[54:57], v[130:133], v[98:101], v[84:87]
	v_mfma_f32_16x16x32_f16 v[18:21], v[134:137], v[98:101], v[18:21]
	s_setprio 0
	v_add_co_u32_e32 v68, vcc, s52, v140
	global_load_dwordx4 v[84:87], v[140:141], off
	global_load_dwordx4 v[88:91], v[142:143], off
	v_addc_co_u32_e32 v69, vcc, 0, v141, vcc
	global_load_dwordx4 v[92:95], v[68:69], off
	global_load_dwordx4 v[96:99], v[144:145], off
	ds_read_b128 v[130:133], v173
	ds_read_b128 v[134:137], v173 offset:8448
	s_setprio 1
	s_waitcnt vmcnt(15) lgkmcnt(1)
	v_mfma_f32_16x16x32_f16 v[110:113], v[130:133], v[34:37], v[110:113]
	s_waitcnt lgkmcnt(0)
	v_mfma_f32_16x16x32_f16 v[10:13], v[134:137], v[34:37], v[10:13]
	s_waitcnt vmcnt(14)
	v_mfma_f32_16x16x32_f16 v[22:25], v[130:133], v[38:41], v[22:25]
	v_mfma_f32_16x16x32_f16 v[34:37], v[134:137], v[38:41], v[42:45]
	s_waitcnt vmcnt(13)
	v_mfma_f32_16x16x32_f16 v[38:41], v[130:133], v[70:73], v[46:49]
	v_mfma_f32_16x16x32_f16 v[14:17], v[134:137], v[70:73], v[14:17]
	s_waitcnt vmcnt(12)
	v_mfma_f32_16x16x32_f16 v[42:45], v[130:133], v[74:77], v[54:57]
	v_mfma_f32_16x16x32_f16 v[18:21], v[134:137], v[74:77], v[18:21]
	s_setprio 0
	v_add_co_u32_e32 v68, vcc, s52, v146
	global_load_dwordx4 v[46:49], v[146:147], off
	global_load_dwordx4 v[54:57], v[148:149], off
	v_addc_co_u32_e32 v69, vcc, 0, v147, vcc
	global_load_dwordx4 v[68:71], v[68:69], off
	s_nop 0
	global_load_dwordx4 v[72:75], v[150:151], off
	ds_read_b128 v[76:79], v174
	ds_read_b128 v[130:133], v174 offset:8448
	s_setprio 1
	s_waitcnt vmcnt(15) lgkmcnt(1)
	v_mfma_f32_16x16x32_f16 v[110:113], v[76:79], v[106:109], v[110:113]
	s_waitcnt lgkmcnt(0)
	v_mfma_f32_16x16x32_f16 v[10:13], v[130:133], v[106:109], v[10:13]
	s_waitcnt vmcnt(14)
	v_mfma_f32_16x16x32_f16 v[22:25], v[76:79], v[122:125], v[22:25]
	v_mfma_f32_16x16x32_f16 v[34:37], v[130:133], v[122:125], v[34:37]
	s_waitcnt vmcnt(13)
	v_mfma_f32_16x16x32_f16 v[38:41], v[76:79], v[126:129], v[38:41]
	v_mfma_f32_16x16x32_f16 v[14:17], v[130:133], v[126:129], v[14:17]
	s_waitcnt vmcnt(12)
	v_mfma_f32_16x16x32_f16 v[42:45], v[76:79], v[62:65], v[42:45]
	v_mfma_f32_16x16x32_f16 v[18:21], v[130:133], v[62:65], v[18:21]
	s_setprio 0
	ds_read_b128 v[62:65], v175
	ds_read_b128 v[76:79], v175 offset:8448
	s_setprio 1
	s_waitcnt vmcnt(11) lgkmcnt(1)
	v_mfma_f32_16x16x32_f16 v[106:109], v[62:65], v[50:53], v[110:113]
	s_waitcnt lgkmcnt(0)
	v_mfma_f32_16x16x32_f16 v[10:13], v[76:79], v[50:53], v[10:13]
	s_waitcnt vmcnt(10)
	v_mfma_f32_16x16x32_f16 v[22:25], v[62:65], v[102:105], v[22:25]
	v_mfma_f32_16x16x32_f16 v[34:37], v[76:79], v[102:105], v[34:37]
	s_waitcnt vmcnt(9)
	v_mfma_f32_16x16x32_f16 v[38:41], v[62:65], v[114:117], v[38:41]
	v_mfma_f32_16x16x32_f16 v[14:17], v[76:79], v[114:117], v[14:17]
	s_waitcnt vmcnt(8)
	v_mfma_f32_16x16x32_f16 v[42:45], v[62:65], v[118:121], v[42:45]
	v_mfma_f32_16x16x32_f16 v[18:21], v[76:79], v[118:121], v[18:21]
	s_setprio 0
	ds_read_b128 v[50:53], v176
	ds_read_b128 v[62:65], v176 offset:8448
	s_setprio 1
	s_waitcnt vmcnt(7) lgkmcnt(1)
	v_mfma_f32_16x16x32_f16 v[76:79], v[50:53], v[84:87], v[106:109]
	s_waitcnt lgkmcnt(0)
	v_mfma_f32_16x16x32_f16 v[10:13], v[62:65], v[84:87], v[10:13]
	s_waitcnt vmcnt(6)
	v_mfma_f32_16x16x32_f16 v[22:25], v[50:53], v[88:91], v[22:25]
	v_mfma_f32_16x16x32_f16 v[34:37], v[62:65], v[88:91], v[34:37]
	s_waitcnt vmcnt(5)
	v_mfma_f32_16x16x32_f16 v[38:41], v[50:53], v[92:95], v[38:41]
	v_mfma_f32_16x16x32_f16 v[14:17], v[62:65], v[92:95], v[14:17]
	s_waitcnt vmcnt(4)
	v_mfma_f32_16x16x32_f16 v[42:45], v[50:53], v[96:99], v[42:45]
	v_mfma_f32_16x16x32_f16 v[18:21], v[62:65], v[96:99], v[18:21]
	s_setprio 0
	ds_read_b128 v[50:53], v177
	ds_read_b128 v[62:65], v177 offset:8448
	s_setprio 1
	s_waitcnt vmcnt(3) lgkmcnt(1)
	v_mfma_f32_16x16x32_f16 v[76:79], v[50:53], v[46:49], v[76:79]
	s_waitcnt lgkmcnt(0)
	v_mfma_f32_16x16x32_f16 v[10:13], v[62:65], v[46:49], v[10:13]
	s_waitcnt vmcnt(2)
	v_mfma_f32_16x16x32_f16 v[22:25], v[50:53], v[54:57], v[22:25]
	v_mfma_f32_16x16x32_f16 v[34:37], v[62:65], v[54:57], v[34:37]
	s_waitcnt vmcnt(1)
	v_mfma_f32_16x16x32_f16 v[38:41], v[50:53], v[68:71], v[38:41]
	v_mfma_f32_16x16x32_f16 v[14:17], v[62:65], v[68:71], v[14:17]
	s_waitcnt vmcnt(0)
	v_mfma_f32_16x16x32_f16 v[42:45], v[50:53], v[72:75], v[42:45]
	v_mfma_f32_16x16x32_f16 v[18:21], v[62:65], v[72:75], v[18:21]
	s_setprio 0
	v_add_co_u32_e32 v108, vcc, s29, v152
	v_and_b32_e32 v67, 0x1c0, v0
	s_nop 0
	v_addc_co_u32_e32 v109, vcc, 0, v153, vcc
	v_add_co_u32_e32 v46, vcc, s52, v152
	s_movk_i32 s4, 0x50
	s_nop 0
	v_addc_co_u32_e32 v47, vcc, 0, v153, vcc
	v_add_co_u32_e32 v68, vcc, s33, v152
	v_or_b32_e32 v116, 16, v67
	s_nop 0
	v_addc_co_u32_e32 v69, vcc, 0, v153, vcc
	v_add_co_u32_e32 v110, vcc, s52, v154
	global_load_dwordx4 v[46:49], v[46:47], off
	s_nop 0
	global_load_dwordx4 v[50:53], v[68:69], off
	global_load_dwordx4 v[54:57], v[152:153], off
	global_load_dwordx4 v[62:65], v[154:155], off
	v_addc_co_u32_e32 v111, vcc, 0, v155, vcc
	v_add_co_u32_e32 v112, vcc, s52, v160
	global_load_dwordx4 v[68:71], v[156:157], off
	global_load_dwordx4 v[72:75], v[158:159], off
	global_load_dwordx4 v[84:87], v[160:161], off
	global_load_dwordx4 v[88:91], v[162:163], off
	v_addc_co_u32_e32 v113, vcc, 0, v161, vcc
	global_load_dwordx4 v[92:95], v[110:111], off
	global_load_dwordx4 v[96:99], v[112:113], off
	global_load_dwordx4 v[100:103], v[108:109], off
	global_load_dwordx4 v[104:107], v[164:165], off
	s_nop 0
	global_store_dwordx4 v[166:167], v[2:5], off sc0 sc1
	global_store_dwordx4 v[168:169], v[6:9], off sc0 sc1
	global_store_dwordx4 v[170:171], v[26:29], off sc0 sc1
	global_store_dwordx4 v[58:59], v[30:33], off sc0 sc1
	v_and_b32_e32 v4, 0x1cf, v0
	v_cvt_pk_f16_f32 v3, v78, v79
	v_cvt_pk_f16_f32 v2, v76, v77
	v_mad_u32_u24 v4, v4, s4, v80
	v_or_b32_e32 v5, v116, v81
	v_or_b32_e32 v117, 32, v67
	ds_write_b64 v4, v[2:3]
	v_cvt_pk_f16_f32 v3, v24, v25
	v_cvt_pk_f16_f32 v2, v22, v23
	v_mad_u32_u24 v5, v5, s4, v80
	v_or_b32_e32 v6, v117, v81
	v_or_b32_e32 v118, 48, v67
	ds_write_b64 v5, v[2:3]
	v_cvt_pk_f16_f32 v3, v40, v41
	v_cvt_pk_f16_f32 v2, v38, v39
	v_mad_u32_u24 v6, v6, s4, v80
	v_or_b32_e32 v7, v118, v81
	ds_write_b64 v6, v[2:3]
	v_cvt_pk_f16_f32 v3, v44, v45
	v_cvt_pk_f16_f32 v2, v42, v43
	v_mad_u32_u24 v7, v7, s4, v80
	ds_write_b64 v7, v[2:3]
	v_cvt_pk_f16_f32 v3, v12, v13
	v_cvt_pk_f16_f32 v2, v10, v11
	ds_write_b64 v4, v[2:3] offset:32
	v_cvt_pk_f16_f32 v3, v36, v37
	v_cvt_pk_f16_f32 v2, v34, v35
	ds_write_b64 v5, v[2:3] offset:32
	v_cvt_pk_f16_f32 v3, v16, v17
	v_cvt_pk_f16_f32 v2, v14, v15
	v_lshl_add_u64 v[10:11], v[60:61], 0, s[14:15]
	ds_write_b64 v6, v[2:3] offset:32
	v_cvt_pk_f16_f32 v2, v18, v19
	v_add_co_u32_e32 v18, vcc, s52, v10
	v_cvt_pk_f16_f32 v3, v20, v21
	v_lshl_add_u64 v[12:13], v[60:61], 0, s[16:17]
	v_addc_co_u32_e32 v19, vcc, 0, v11, vcc
	ds_write_b64 v7, v[2:3] offset:32
	s_waitcnt lgkmcnt(0)
	s_barrier
	global_load_dwordx4 v[2:5], v[10:11], off
	global_load_dwordx4 v[6:9], v[12:13], off
	v_lshl_add_u64 v[20:21], v[60:61], 0, s[12:13]
	global_load_dwordx4 v[10:13], v[18:19], off
	global_load_dwordx4 v[14:17], v[20:21], off
	ds_read_b128 v[18:21], v1
	ds_read_b128 v[22:25], v1 offset:8448
	s_mov_b32 s3, s27
	s_setprio 1
	s_waitcnt vmcnt(17) lgkmcnt(1)
	v_mfma_f32_16x16x32_f16 v[26:29], v[18:21], v[54:57], 0
	s_waitcnt lgkmcnt(0)
	v_mfma_f32_16x16x32_f16 v[30:33], v[22:25], v[54:57], 0
	s_waitcnt vmcnt(9)
	v_mfma_f32_16x16x32_f16 v[34:37], v[18:21], v[100:103], 0
	v_mfma_f32_16x16x32_f16 v[38:41], v[22:25], v[100:103], 0
	v_mfma_f32_16x16x32_f16 v[42:45], v[18:21], v[46:49], 0
	v_mfma_f32_16x16x32_f16 v[46:49], v[22:25], v[46:49], 0
	v_mfma_f32_16x16x32_f16 v[18:21], v[18:21], v[50:53], 0
	v_mfma_f32_16x16x32_f16 v[22:25], v[22:25], v[50:53], 0
	s_setprio 0
	v_lshl_add_u64 v[58:59], v[60:61], 0, s[10:11]
	v_add_co_u32_e32 v76, vcc, s29, v58
	s_nop 1
	v_addc_co_u32_e32 v77, vcc, 0, v59, vcc
	v_add_co_u32_e32 v108, vcc, s52, v58
	global_load_dwordx4 v[50:53], v[58:59], off
	global_load_dwordx4 v[54:57], v[76:77], off
	v_addc_co_u32_e32 v109, vcc, 0, v59, vcc
	v_add_co_u32_e32 v58, vcc, s33, v58
	s_nop 1
	v_addc_co_u32_e32 v59, vcc, 0, v59, vcc
	global_load_dwordx4 v[76:79], v[108:109], off
	global_load_dwordx4 v[100:103], v[58:59], off
	ds_read_b128 v[108:111], v82
	ds_read_b128 v[112:115], v82 offset:8448
	s_setprio 1
	s_waitcnt lgkmcnt(1)
	v_mfma_f32_16x16x32_f16 v[26:29], v[108:111], v[62:65], v[26:29]
	s_waitcnt lgkmcnt(0)
	v_mfma_f32_16x16x32_f16 v[30:33], v[112:115], v[62:65], v[30:33]
	v_mfma_f32_16x16x32_f16 v[34:37], v[108:111], v[68:71], v[34:37]
	v_mfma_f32_16x16x32_f16 v[38:41], v[112:115], v[68:71], v[38:41]
	v_mfma_f32_16x16x32_f16 v[42:45], v[108:111], v[92:95], v[42:45]
	v_mfma_f32_16x16x32_f16 v[46:49], v[112:115], v[92:95], v[46:49]
	v_mfma_f32_16x16x32_f16 v[18:21], v[108:111], v[72:75], v[18:21]
	v_mfma_f32_16x16x32_f16 v[22:25], v[112:115], v[72:75], v[22:25]
	s_setprio 0
	v_lshl_add_u64 v[58:59], v[60:61], 0, s[48:49]
	v_lshl_add_u64 v[72:73], v[60:61], 0, s[50:51]
	global_load_dwordx4 v[62:65], v[58:59], off
	global_load_dwordx4 v[68:71], v[72:73], off
	v_add_co_u32_e32 v58, vcc, s52, v58
	v_lshl_add_u64 v[82:83], v[60:61], 0, s[46:47]
	s_nop 0
	v_addc_co_u32_e32 v59, vcc, 0, v59, vcc
	global_load_dwordx4 v[72:75], v[58:59], off
	global_load_dwordx4 v[92:95], v[82:83], off
	ds_read_b128 v[108:111], v172
	ds_read_b128 v[112:115], v172 offset:8448
	s_setprio 1
	s_waitcnt lgkmcnt(1)
	v_mfma_f32_16x16x32_f16 v[26:29], v[108:111], v[84:87], v[26:29]
	s_waitcnt lgkmcnt(0)
	v_mfma_f32_16x16x32_f16 v[30:33], v[112:115], v[84:87], v[30:33]
	v_mfma_f32_16x16x32_f16 v[34:37], v[108:111], v[88:91], v[34:37]
	v_mfma_f32_16x16x32_f16 v[38:41], v[112:115], v[88:91], v[38:41]
	v_mfma_f32_16x16x32_f16 v[42:45], v[108:111], v[96:99], v[42:45]
	v_mfma_f32_16x16x32_f16 v[46:49], v[112:115], v[96:99], v[46:49]
	s_waitcnt vmcnt(16)
	v_mfma_f32_16x16x32_f16 v[18:21], v[108:111], v[104:107], v[18:21]
	v_mfma_f32_16x16x32_f16 v[22:25], v[112:115], v[104:107], v[22:25]
	s_setprio 0
	v_lshl_add_u64 v[58:59], v[60:61], 0, s[42:43]
	v_lshl_add_u64 v[90:91], v[60:61], 0, s[44:45]
	global_load_dwordx4 v[82:85], v[58:59], off
	global_load_dwordx4 v[86:89], v[90:91], off
	v_add_co_u32_e32 v58, vcc, s52, v58
	v_lshl_add_u64 v[90:91], v[60:61], 0, s[40:41]
	s_nop 0
	v_addc_co_u32_e32 v59, vcc, 0, v59, vcc
	global_load_dwordx4 v[96:99], v[58:59], off
	global_load_dwordx4 v[104:107], v[90:91], off
	ds_read_b128 v[108:111], v173
	ds_read_b128 v[112:115], v173 offset:8448
	s_setprio 1
	s_waitcnt vmcnt(15) lgkmcnt(1)
	v_mfma_f32_16x16x32_f16 v[26:29], v[108:111], v[2:5], v[26:29]
	s_waitcnt lgkmcnt(0)
	v_mfma_f32_16x16x32_f16 v[2:5], v[112:115], v[2:5], v[30:33]
	s_waitcnt vmcnt(14)
	v_mfma_f32_16x16x32_f16 v[30:33], v[108:111], v[6:9], v[34:37]
	v_mfma_f32_16x16x32_f16 v[6:9], v[112:115], v[6:9], v[38:41]
	s_waitcnt vmcnt(13)
	v_mfma_f32_16x16x32_f16 v[34:37], v[108:111], v[10:13], v[42:45]
	v_mfma_f32_16x16x32_f16 v[10:13], v[112:115], v[10:13], v[46:49]
	s_waitcnt vmcnt(12)
	v_mfma_f32_16x16x32_f16 v[18:21], v[108:111], v[14:17], v[18:21]
	v_mfma_f32_16x16x32_f16 v[14:17], v[112:115], v[14:17], v[22:25]
	s_setprio 0
	v_lshl_add_u64 v[42:43], v[60:61], 0, s[8:9]
	v_add_co_u32_e32 v58, vcc, s52, v42
	v_lshl_add_u64 v[44:45], v[60:61], 0, s[38:39]
	s_nop 0
	v_addc_co_u32_e32 v59, vcc, 0, v43, vcc
	global_load_dwordx4 v[22:25], v[42:43], off
	global_load_dwordx4 v[38:41], v[44:45], off
	v_lshl_add_u64 v[60:61], v[60:61], 0, s[6:7]
	global_load_dwordx4 v[42:45], v[58:59], off
	global_load_dwordx4 v[46:49], v[60:61], off
	ds_read_b128 v[58:61], v174
	ds_read_b128 v[108:111], v174 offset:8448
	s_setprio 1
	s_waitcnt vmcnt(15) lgkmcnt(1)
	v_mfma_f32_16x16x32_f16 v[26:29], v[58:61], v[50:53], v[26:29]
	s_waitcnt lgkmcnt(0)
	v_mfma_f32_16x16x32_f16 v[2:5], v[108:111], v[50:53], v[2:5]
	s_waitcnt vmcnt(14)
	v_mfma_f32_16x16x32_f16 v[30:33], v[58:61], v[54:57], v[30:33]
	v_mfma_f32_16x16x32_f16 v[6:9], v[108:111], v[54:57], v[6:9]
	s_waitcnt vmcnt(13)
	v_mfma_f32_16x16x32_f16 v[34:37], v[58:61], v[76:79], v[34:37]
	v_mfma_f32_16x16x32_f16 v[10:13], v[108:111], v[76:79], v[10:13]
	s_waitcnt vmcnt(12)
	v_mfma_f32_16x16x32_f16 v[18:21], v[58:61], v[100:103], v[18:21]
	v_mfma_f32_16x16x32_f16 v[14:17], v[108:111], v[100:103], v[14:17]
	s_setprio 0
	ds_read_b128 v[50:53], v175
	ds_read_b128 v[54:57], v175 offset:8448
	s_setprio 1
	s_waitcnt vmcnt(11) lgkmcnt(1)
	v_mfma_f32_16x16x32_f16 v[26:29], v[50:53], v[62:65], v[26:29]
	s_waitcnt lgkmcnt(0)
	v_mfma_f32_16x16x32_f16 v[2:5], v[54:57], v[62:65], v[2:5]
	s_waitcnt vmcnt(10)
	v_mfma_f32_16x16x32_f16 v[30:33], v[50:53], v[68:71], v[30:33]
	v_mfma_f32_16x16x32_f16 v[6:9], v[54:57], v[68:71], v[6:9]
	s_waitcnt vmcnt(9)
	v_mfma_f32_16x16x32_f16 v[34:37], v[50:53], v[72:75], v[34:37]
	v_mfma_f32_16x16x32_f16 v[10:13], v[54:57], v[72:75], v[10:13]
	s_waitcnt vmcnt(8)
	v_mfma_f32_16x16x32_f16 v[18:21], v[50:53], v[92:95], v[18:21]
	v_mfma_f32_16x16x32_f16 v[14:17], v[54:57], v[92:95], v[14:17]
	s_setprio 0
	ds_read_b128 v[50:53], v176
	ds_read_b128 v[54:57], v176 offset:8448
	s_setprio 1
	s_waitcnt vmcnt(7) lgkmcnt(1)
	v_mfma_f32_16x16x32_f16 v[26:29], v[50:53], v[82:85], v[26:29]
	s_waitcnt lgkmcnt(0)
	v_mfma_f32_16x16x32_f16 v[2:5], v[54:57], v[82:85], v[2:5]
	s_waitcnt vmcnt(6)
	v_mfma_f32_16x16x32_f16 v[30:33], v[50:53], v[86:89], v[30:33]
	v_mfma_f32_16x16x32_f16 v[6:9], v[54:57], v[86:89], v[6:9]
	s_waitcnt vmcnt(5)
	v_mfma_f32_16x16x32_f16 v[34:37], v[50:53], v[96:99], v[34:37]
	v_mfma_f32_16x16x32_f16 v[58:61], v[54:57], v[96:99], v[10:13]
	s_waitcnt vmcnt(4)
	v_mfma_f32_16x16x32_f16 v[18:21], v[50:53], v[104:107], v[18:21]
	v_mfma_f32_16x16x32_f16 v[50:53], v[54:57], v[104:107], v[14:17]
	s_setprio 0
	ds_read_b128 v[54:57], v177
	ds_read_b128 v[62:65], v177 offset:8448
	s_setprio 1
	s_waitcnt vmcnt(3) lgkmcnt(1)
	v_mfma_f32_16x16x32_f16 v[26:29], v[54:57], v[22:25], v[26:29]
	s_waitcnt lgkmcnt(0)
	v_mfma_f32_16x16x32_f16 v[14:17], v[62:65], v[22:25], v[2:5]
	s_waitcnt vmcnt(2)
	v_mfma_f32_16x16x32_f16 v[22:25], v[54:57], v[38:41], v[30:33]
	v_mfma_f32_16x16x32_f16 v[10:13], v[62:65], v[38:41], v[6:9]
	s_waitcnt vmcnt(1)
	v_mfma_f32_16x16x32_f16 v[30:33], v[54:57], v[42:45], v[34:37]
	v_mfma_f32_16x16x32_f16 v[6:9], v[62:65], v[42:45], v[58:61]
	s_waitcnt vmcnt(0)
	v_mfma_f32_16x16x32_f16 v[34:37], v[54:57], v[46:49], v[18:21]
	v_mfma_f32_16x16x32_f16 v[2:5], v[62:65], v[46:49], v[50:53]
	s_setprio 0
	s_nop 1
	v_mul_u32_u24_e32 v52, 0x50, v0
	ds_read_b128 v[18:21], v52
	s_lshl_b64 s[2:3], s[2:3], 15
	v_or_b32_e32 v0, s2, v66
	v_mov_b32_e32 v1, s3
	v_lshl_add_u64 v[50:51], s[24:25], 0, v[0:1]
	ds_read_b128 v[38:41], v52 offset:16
	ds_read_b128 v[42:45], v52 offset:32
	ds_read_b128 v[46:49], v52 offset:48
	s_waitcnt lgkmcnt(3)
	global_store_dwordx4 v[50:51], v[18:21], off sc0 sc1
	s_nop 1
	v_add_co_u32_e32 v18, vcc, s29, v50
	s_nop 1
	v_addc_co_u32_e32 v19, vcc, 0, v51, vcc
	s_waitcnt lgkmcnt(2)
	global_store_dwordx4 v[18:19], v[38:41], off sc0 sc1
	v_or_b32_e32 v18, 0x4000, v0
	v_mov_b32_e32 v19, s3
	v_lshl_add_u64 v[20:21], s[24:25], 0, v[18:19]
	s_waitcnt lgkmcnt(1)
	global_store_dwordx4 v[20:21], v[42:45], off sc0 sc1
	v_mul_f32_e32 v20, 0xbfb8aa3b, v26
	v_exp_f32_e32 v38, v20
	v_add_co_u32_e32 v20, vcc, s33, v50
	v_or_b32_e32 v39, 0x200, v81
	s_nop 0
	v_addc_co_u32_e32 v21, vcc, 0, v51, vcc
	s_waitcnt lgkmcnt(0)
	global_store_dwordx4 v[20:21], v[46:49], off sc0 sc1
	v_add_f32_e32 v20, 1.0, v38
	v_rcp_f32_e32 v20, v20
	v_mul_f32_e32 v21, 0xbfb8aa3b, v27
	v_mul_f32_e32 v38, 0xbfb8aa3b, v28
	v_exp_f32_e32 v21, v21
	v_exp_f32_e32 v38, v38
	v_fma_mixlo_f16 v40, v26, v20, 0
	v_mul_f32_e32 v26, 0xbfb8aa3b, v29
	v_add_f32_e32 v20, 1.0, v21
	v_add_f32_e32 v21, 1.0, v38
	v_exp_f32_e32 v38, v26
	v_rcp_f32_e32 v20, v20
	v_rcp_f32_e32 v21, v21
	v_mov_b32_e32 v26, v27
	v_mov_b32_e32 v27, v28
	v_add_f32_e32 v28, 1.0, v38
	v_rcp_f32_e32 v28, v28
	v_pk_mul_f32 v[20:21], v[26:27], v[20:21]
	v_or_b32_e32 v27, v39, v67
	v_cvt_pk_f16_f32 v21, v20, v21
	v_fma_mixlo_f16 v26, v29, v28, 0
	v_pack_b32_f16 v20, v40, v21
	v_alignbit_b32 v21, v26, v21, 16
	v_mul_f32_e32 v26, 0xbfb8aa3b, v22
	v_exp_f32_e32 v26, v26
	v_mad_u32_u24 v27, v27, s4, v80
	ds_write_b64 v27, v[20:21]
	v_mul_f32_e32 v21, 0xbfb8aa3b, v23
	v_add_f32_e32 v20, 1.0, v26
	v_rcp_f32_e32 v20, v20
	v_mul_f32_e32 v26, 0xbfb8aa3b, v24
	v_exp_f32_e32 v21, v21
	v_exp_f32_e32 v26, v26
	v_fma_mixlo_f16 v28, v22, v20, 0
	v_mul_f32_e32 v22, 0xbfb8aa3b, v25
	v_add_f32_e32 v20, 1.0, v21
	v_add_f32_e32 v21, 1.0, v26
	v_exp_f32_e32 v26, v22
	v_rcp_f32_e32 v20, v20
	v_rcp_f32_e32 v21, v21
	v_mov_b32_e32 v22, v23
	v_mov_b32_e32 v23, v24
	v_add_f32_e32 v24, 1.0, v26
	v_rcp_f32_e32 v24, v24
	v_pk_mul_f32 v[20:21], v[22:23], v[20:21]
	v_or_b32_e32 v23, v116, v39
	v_cvt_pk_f16_f32 v21, v20, v21
	v_fma_mixlo_f16 v22, v25, v24, 0
	v_pack_b32_f16 v20, v28, v21
	v_alignbit_b32 v21, v22, v21, 16
	v_mul_f32_e32 v22, 0xbfb8aa3b, v30
	v_exp_f32_e32 v22, v22
	v_mad_u32_u24 v24, v23, s4, v80
	ds_write_b64 v24, v[20:21]
	v_mul_f32_e32 v21, 0xbfb8aa3b, v31
	v_add_f32_e32 v20, 1.0, v22
	v_mul_f32_e32 v22, 0xbfb8aa3b, v32
	v_rcp_f32_e32 v20, v20
	v_exp_f32_e32 v21, v21
	v_exp_f32_e32 v22, v22
	v_mov_b32_e32 v23, v32
	v_fma_mixlo_f16 v25, v30, v20, 0
	v_add_f32_e32 v20, 1.0, v21
	v_add_f32_e32 v21, 1.0, v22
	v_mul_f32_e32 v22, 0xbfb8aa3b, v33
	v_exp_f32_e32 v26, v22
	v_rcp_f32_e32 v20, v20
	v_rcp_f32_e32 v21, v21
	v_mov_b32_e32 v22, v31
	v_add_f32_e32 v26, 1.0, v26
	v_rcp_f32_e32 v26, v26
	v_pk_mul_f32 v[20:21], v[22:23], v[20:21]
	v_or_b32_e32 v23, v117, v39
	v_cvt_pk_f16_f32 v21, v20, v21
	v_fma_mixlo_f16 v22, v33, v26, 0
	v_pack_b32_f16 v20, v25, v21
	v_alignbit_b32 v21, v22, v21, 16
	v_mul_f32_e32 v22, 0xbfb8aa3b, v34
	v_exp_f32_e32 v22, v22
	v_mad_u32_u24 v25, v23, s4, v80
	ds_write_b64 v25, v[20:21]
	v_mul_f32_e32 v21, 0xbfb8aa3b, v35
	v_add_f32_e32 v20, 1.0, v22
	v_mul_f32_e32 v22, 0xbfb8aa3b, v36
	v_rcp_f32_e32 v20, v20
	v_exp_f32_e32 v21, v21
	v_exp_f32_e32 v22, v22
	v_mov_b32_e32 v23, v36
	v_fma_mixlo_f16 v26, v34, v20, 0
	v_add_f32_e32 v20, 1.0, v21
	v_add_f32_e32 v21, 1.0, v22
	v_mul_f32_e32 v22, 0xbfb8aa3b, v37
	v_exp_f32_e32 v28, v22
	v_rcp_f32_e32 v20, v20
	v_rcp_f32_e32 v21, v21
	v_mov_b32_e32 v22, v35
	v_add_f32_e32 v28, 1.0, v28
	v_rcp_f32_e32 v28, v28
	v_pk_mul_f32 v[20:21], v[22:23], v[20:21]
	v_or_b32_e32 v23, v118, v39
	v_cvt_pk_f16_f32 v21, v20, v21
	v_fma_mixlo_f16 v22, v37, v28, 0
	v_pack_b32_f16 v20, v26, v21
	v_alignbit_b32 v21, v22, v21, 16
	v_mul_f32_e32 v22, 0xbfb8aa3b, v14
	v_exp_f32_e32 v22, v22
	v_mad_u32_u24 v23, v23, s4, v80
	ds_write_b64 v23, v[20:21]
	v_mul_f32_e32 v21, 0xbfb8aa3b, v15
	v_add_f32_e32 v20, 1.0, v22
	v_rcp_f32_e32 v20, v20
	v_exp_f32_e32 v21, v21
	v_mul_f32_e32 v22, 0xbfb8aa3b, v16
	v_exp_f32_e32 v22, v22
	v_fma_mixlo_f16 v26, v14, v20, 0
	v_add_f32_e32 v14, 1.0, v21
	v_rcp_f32_e32 v20, v14
	v_add_f32_e32 v14, 1.0, v22
	v_rcp_f32_e32 v21, v14
	v_mov_b32_e32 v14, v15
	v_mul_f32_e32 v15, 0xbfb8aa3b, v17
	v_exp_f32_e32 v22, v15
	v_mov_b32_e32 v15, v16
	v_pk_mul_f32 v[14:15], v[14:15], v[20:21]
	v_mul_f32_e32 v20, 0xbfb8aa3b, v10
	v_cvt_pk_f16_f32 v15, v14, v15
	v_add_f32_e32 v14, 1.0, v22
	v_rcp_f32_e32 v16, v14
	v_exp_f32_e32 v20, v20
	v_pack_b32_f16 v14, v26, v15
	v_lshl_add_u64 v[0:1], s[0:1], 0, v[0:1]
	v_fma_mixlo_f16 v16, v17, v16, 0
	v_alignbit_b32 v15, v16, v15, 16
	ds_write_b64 v27, v[14:15] offset:32
	v_add_f32_e32 v14, 1.0, v20
	v_mul_f32_e32 v15, 0xbfb8aa3b, v11
	v_rcp_f32_e32 v14, v14
	v_exp_f32_e32 v15, v15
	v_mul_f32_e32 v16, 0xbfb8aa3b, v12
	v_exp_f32_e32 v16, v16
	v_fma_mixlo_f16 v17, v10, v14, 0
	v_add_f32_e32 v10, 1.0, v15
	v_rcp_f32_e32 v14, v10
	v_add_f32_e32 v10, 1.0, v16
	v_rcp_f32_e32 v15, v10
	v_mov_b32_e32 v10, v11
	v_mul_f32_e32 v11, 0xbfb8aa3b, v13
	v_exp_f32_e32 v16, v11
	v_mov_b32_e32 v11, v12
	v_pk_mul_f32 v[10:11], v[10:11], v[14:15]
	v_mul_f32_e32 v14, 0xbfb8aa3b, v6
	v_cvt_pk_f16_f32 v11, v10, v11
	v_add_f32_e32 v10, 1.0, v16
	v_rcp_f32_e32 v12, v10
	v_exp_f32_e32 v14, v14
	v_pack_b32_f16 v10, v17, v11
	v_fma_mixlo_f16 v12, v13, v12, 0
	v_alignbit_b32 v11, v12, v11, 16
	ds_write_b64 v24, v[10:11] offset:32
	v_add_f32_e32 v10, 1.0, v14
	v_mul_f32_e32 v11, 0xbfb8aa3b, v7
	v_rcp_f32_e32 v10, v10
	v_exp_f32_e32 v11, v11
	v_mul_f32_e32 v12, 0xbfb8aa3b, v8
	v_exp_f32_e32 v12, v12
	v_fma_mixlo_f16 v13, v6, v10, 0
	v_add_f32_e32 v6, 1.0, v11
	v_rcp_f32_e32 v10, v6
	v_add_f32_e32 v6, 1.0, v12
	v_rcp_f32_e32 v11, v6
	v_mov_b32_e32 v6, v7
	v_mul_f32_e32 v7, 0xbfb8aa3b, v9
	v_exp_f32_e32 v12, v7
	v_mov_b32_e32 v7, v8
	v_pk_mul_f32 v[6:7], v[6:7], v[10:11]
	v_mul_f32_e32 v10, 0xbfb8aa3b, v2
	v_cvt_pk_f16_f32 v7, v6, v7
	v_add_f32_e32 v6, 1.0, v12
	v_rcp_f32_e32 v8, v6
	v_exp_f32_e32 v10, v10
	v_pack_b32_f16 v6, v13, v7
	v_fma_mixlo_f16 v8, v9, v8, 0
	v_alignbit_b32 v7, v8, v7, 16
	ds_write_b64 v25, v[6:7] offset:32
	v_add_f32_e32 v6, 1.0, v10
	v_mul_f32_e32 v7, 0xbfb8aa3b, v3
	v_rcp_f32_e32 v6, v6
	v_exp_f32_e32 v7, v7
	v_mul_f32_e32 v8, 0xbfb8aa3b, v4
	v_exp_f32_e32 v8, v8
	v_fma_mixlo_f16 v9, v2, v6, 0
	v_add_f32_e32 v2, 1.0, v7
	v_mul_f32_e32 v7, 0xbfb8aa3b, v5
	v_rcp_f32_e32 v6, v2
	v_add_f32_e32 v2, 1.0, v8
	v_exp_f32_e32 v8, v7
	v_rcp_f32_e32 v7, v2
	v_mov_b32_e32 v2, v3
	v_mov_b32_e32 v3, v4
	v_add_f32_e32 v4, 1.0, v8
	v_rcp_f32_e32 v4, v4
	v_pk_mul_f32 v[2:3], v[2:3], v[6:7]
	v_fma_mixlo_f16 v4, v5, v4, 0
	v_cvt_pk_f16_f32 v3, v2, v3
	v_pack_b32_f16 v2, v9, v3
	v_alignbit_b32 v3, v4, v3, 16
	ds_write_b64 v23, v[2:3] offset:32
	s_waitcnt lgkmcnt(0)
	s_barrier
	ds_read_b128 v[2:5], v52 offset:40960
	ds_read_b128 v[6:9], v52 offset:40976
	ds_read_b128 v[10:13], v52 offset:40992
	ds_read_b128 v[14:17], v52 offset:41008
	s_waitcnt lgkmcnt(3)
	global_store_dwordx4 v[0:1], v[2:5], off sc0 sc1
	s_nop 1
	v_add_co_u32_e32 v2, vcc, 0x2000, v0
	s_nop 1
	v_addc_co_u32_e32 v3, vcc, 0, v1, vcc
	v_add_co_u32_e32 v0, vcc, 0x6000, v0
	s_waitcnt lgkmcnt(2)
	global_store_dwordx4 v[2:3], v[6:9], off sc0 sc1
	v_lshl_add_u64 v[2:3], s[0:1], 0, v[18:19]
	v_addc_co_u32_e32 v1, vcc, 0, v1, vcc
	s_waitcnt lgkmcnt(1)
	global_store_dwordx4 v[2:3], v[10:13], off sc0 sc1
	s_waitcnt lgkmcnt(0)
	global_store_dwordx4 v[0:1], v[14:17], off sc0 sc1
	s_endpgm
	.p2align	8

amdhsa.kernels:
  - .agpr_count:     0
    .args:
      - .actual_access:  read_only
        .address_space:  global
        .offset:         0
        .size:           8
        .value_kind:     global_buffer
      - .actual_access:  write_only
        .address_space:  global
        .offset:         8
        .size:           8
        .value_kind:     global_buffer
      - .offset:         16
        .size:           4
        .value_kind:     by_value
      - .offset:         20
        .size:           4
        .value_kind:     by_value
      - .actual_access:  read_only
        .address_space:  global
        .offset:         24
        .size:           8
        .value_kind:     global_buffer
      - .actual_access:  write_only
        .address_space:  global
        .offset:         32
        .size:           8
        .value_kind:     global_buffer
      - .offset:         40
        .size:           4
        .value_kind:     by_value
      - .offset:         44
        .size:           4
        .value_kind:     by_value
      - .actual_access:  read_only
        .address_space:  global
        .offset:         48
        .size:           8
        .value_kind:     global_buffer
      - .actual_access:  write_only
        .address_space:  global
        .offset:         56
        .size:           8
        .value_kind:     global_buffer
      - .offset:         64
        .size:           4
        .value_kind:     by_value
      - .offset:         68
        .size:           4
        .value_kind:     by_value
      - .actual_access:  read_only
        .address_space:  global
        .offset:         72
        .size:           8
        .value_kind:     global_buffer
      - .actual_access:  write_only
        .address_space:  global
        .offset:         80
        .size:           8
        .value_kind:     global_buffer
      - .offset:         88
        .size:           4
        .value_kind:     by_value
      - .actual_access:  read_only
        .address_space:  global
        .offset:         96
        .size:           8
        .value_kind:     global_buffer
      - .actual_access:  write_only
        .address_space:  global
        .offset:         104
        .size:           8
        .value_kind:     global_buffer
      - .offset:         112
        .size:           4
        .value_kind:     by_value
      - .offset:         120
        .size:           4
        .value_kind:     hidden_block_count_x
      - .offset:         124
        .size:           4
        .value_kind:     hidden_block_count_y
      - .offset:         128
        .size:           4
        .value_kind:     hidden_block_count_z
      - .offset:         132
        .size:           2
        .value_kind:     hidden_group_size_x
      - .offset:         134
        .size:           2
        .value_kind:     hidden_group_size_y
      - .offset:         136
        .size:           2
        .value_kind:     hidden_group_size_z
      - .offset:         138
        .size:           2
        .value_kind:     hidden_remainder_x
      - .offset:         140
        .size:           2
        .value_kind:     hidden_remainder_y
      - .offset:         142
        .size:           2
        .value_kind:     hidden_remainder_z
      - .offset:         160
        .size:           8
        .value_kind:     hidden_global_offset_x
      - .offset:         168
        .size:           8
        .value_kind:     hidden_global_offset_y
      - .offset:         176
        .size:           8
        .value_kind:     hidden_global_offset_z
      - .offset:         184
        .size:           2
        .value_kind:     hidden_grid_dims
    .group_segment_fixed_size: 0
    .kernarg_segment_align: 8
    .kernarg_segment_size: 376
    .language:       OpenCL C
    .language_version:
      - 2
      - 0
    .max_flat_workgroup_size: 1024
    .name:           _Z5k_swzPKfPDF16_iiS0_S1_iiS0_S1_iiS0_PfiS0_S1_i
    .private_segment_fixed_size: 0
    .sgpr_count:     32
    .sgpr_spill_count: 0
    .symbol:         _Z5k_swzPKfPDF16_iiS0_S1_iiS0_S1_iiS0_PfiS0_S1_i.kd
    .uniform_work_group_size: 1
    .uses_dynamic_stack: false
    .vgpr_count:     14
    .vgpr_spill_count: 0
    .wavefront_size: 64
  - .agpr_count:     0
    .args:
      - .actual_access:  read_only
        .address_space:  global
        .offset:         0
        .size:           8
        .value_kind:     global_buffer
      - .actual_access:  read_only
        .address_space:  global
        .offset:         8
        .size:           8
        .value_kind:     global_buffer
      - .actual_access:  write_only
        .address_space:  global
        .offset:         16
        .size:           8
        .value_kind:     global_buffer
      - .actual_access:  read_only
        .address_space:  global
        .offset:         24
        .size:           8
        .value_kind:     global_buffer
      - .actual_access:  read_only
        .address_space:  global
        .offset:         32
        .size:           8
        .value_kind:     global_buffer
      - .actual_access:  read_only
        .address_space:  global
        .offset:         40
        .size:           8
        .value_kind:     global_buffer
      - .actual_access:  write_only
        .address_space:  global
        .offset:         48
        .size:           8
        .value_kind:     global_buffer
    .group_segment_fixed_size: 98816
    .kernarg_segment_align: 8
    .kernarg_segment_size: 56
    .language:       OpenCL C
    .language_version:
      - 2
      - 0
    .max_flat_workgroup_size: 512
    .name:           _Z10k_ka_firstPKfPKiPfS0_S0_PKDF16_PDF16_
    .private_segment_fixed_size: 0
    .sgpr_count:     59
    .sgpr_spill_count: 0
    .symbol:         _Z10k_ka_firstPKfPKiPfS0_S0_PKDF16_PDF16_.kd
    .uniform_work_group_size: 1
    .uses_dynamic_stack: false
    .vgpr_count:     174
    .vgpr_spill_count: 0
    .wavefront_size: 64
  - .agpr_count:     0
    .args:
      - .actual_access:  read_only
        .address_space:  global
        .offset:         0
        .size:           8
        .value_kind:     global_buffer
      - .actual_access:  read_only
        .address_space:  global
        .offset:         8
        .size:           8
        .value_kind:     global_buffer
      - .actual_access:  read_only
        .address_space:  global
        .offset:         16
        .size:           8
        .value_kind:     global_buffer
      - .actual_access:  read_only
        .address_space:  global
        .offset:         24
        .size:           8
        .value_kind:     global_buffer
      - .actual_access:  read_only
        .address_space:  global
        .offset:         32
        .size:           8
        .value_kind:     global_buffer
      - .actual_access:  read_only
        .address_space:  global
        .offset:         40
        .size:           8
        .value_kind:     global_buffer
      - .actual_access:  write_only
        .address_space:  global
        .offset:         48
        .size:           8
        .value_kind:     global_buffer
      - .actual_access:  write_only
        .address_space:  global
        .offset:         56
        .size:           8
        .value_kind:     global_buffer
      - .actual_access:  write_only
        .address_space:  global
        .offset:         64
        .size:           8
        .value_kind:     global_buffer
      - .actual_access:  read_only
        .address_space:  global
        .offset:         72
        .size:           8
        .value_kind:     global_buffer
      - .actual_access:  write_only
        .address_space:  global
        .offset:         80
        .size:           8
        .value_kind:     global_buffer
      - .actual_access:  write_only
        .address_space:  global
        .offset:         88
        .size:           8
        .value_kind:     global_buffer
    .group_segment_fixed_size: 47616
    .kernarg_segment_align: 8
    .kernarg_segment_size: 96
    .language:       OpenCL C
    .language_version:
      - 2
      - 0
    .max_flat_workgroup_size: 512
    .name:           _Z12k_conv_xprojPKDF16_PKfS2_S0_S0_S2_PDF16_S3_PfS2_S3_S4_
    .private_segment_fixed_size: 0
    .sgpr_count:     32
    .sgpr_spill_count: 0
    .symbol:         _Z12k_conv_xprojPKDF16_PKfS2_S0_S0_S2_PDF16_S3_PfS2_S3_S4_.kd
    .uniform_work_group_size: 1
    .uses_dynamic_stack: false
    .vgpr_count:     164
    .vgpr_spill_count: 0
    .wavefront_size: 64
  - .agpr_count:     0
    .args:
      - .actual_access:  read_only
        .address_space:  global
        .offset:         0
        .size:           8
        .value_kind:     global_buffer
      - .actual_access:  read_only
        .address_space:  global
        .offset:         8
        .size:           8
        .value_kind:     global_buffer
      - .actual_access:  read_only
        .address_space:  global
        .offset:         16
        .size:           8
        .value_kind:     global_buffer
      - .actual_access:  write_only
        .address_space:  global
        .offset:         24
        .size:           8
        .value_kind:     global_buffer
    .group_segment_fixed_size: 16384
    .kernarg_segment_align: 8
    .kernarg_segment_size: 32
    .language:       OpenCL C
    .language_version:
      - 2
      - 0
    .max_flat_workgroup_size: 512
    .name:           _Z11k_scan_combPKDF16_PKfS2_PDF16_
    .private_segment_fixed_size: 0
    .sgpr_count:     18
    .sgpr_spill_count: 0
    .symbol:         _Z11k_scan_combPKDF16_PKfS2_PDF16_.kd
    .uniform_work_group_size: 1
    .uses_dynamic_stack: false
    .vgpr_count:     120
    .vgpr_spill_count: 0
    .wavefront_size: 64
  - .agpr_count:     0
    .args:
      - .actual_access:  read_only
        .address_space:  global
        .offset:         0
        .size:           8
        .value_kind:     global_buffer
      - .actual_access:  read_only
        .address_space:  global
        .offset:         8
        .size:           8
        .value_kind:     global_buffer
      - .actual_access:  read_only
        .address_space:  global
        .offset:         16
        .size:           8
        .value_kind:     global_buffer
      - .actual_access:  read_only
        .address_space:  global
        .offset:         24
        .size:           8
        .value_kind:     global_buffer
      - .actual_access:  write_only
        .address_space:  global
        .offset:         32
        .size:           8
        .value_kind:     global_buffer
    .group_segment_fixed_size: 32
    .kernarg_segment_align: 8
    .kernarg_segment_size: 40
    .language:       OpenCL C
    .language_version:
      - 2
      - 0
    .max_flat_workgroup_size: 256
    .name:           _Z6k_headPKfS0_S0_S0_Pf
    .private_segment_fixed_size: 0
    .sgpr_count:     86
    .sgpr_spill_count: 0
    .symbol:         _Z6k_headPKfS0_S0_S0_Pf.kd
    .uniform_work_group_size: 1
    .uses_dynamic_stack: false
    .vgpr_count:     92
    .vgpr_spill_count: 0
    .wavefront_size: 64
  - .agpr_count:     0
    .args:
      - .actual_access:  read_only
        .address_space:  global
        .offset:         0
        .size:           8
        .value_kind:     global_buffer
      - .actual_access:  read_only
        .address_space:  global
        .offset:         8
        .size:           8
        .value_kind:     global_buffer
      - .actual_access:  read_only
        .address_space:  global
        .offset:         16
        .size:           8
        .value_kind:     global_buffer
      - .actual_access:  read_only
        .address_space:  global
        .offset:         24
        .size:           8
        .value_kind:     global_buffer
      - .actual_access:  read_only
        .address_space:  global
        .offset:         32
        .size:           8
        .value_kind:     global_buffer
      - .actual_access:  read_only
        .address_space:  global
        .offset:         40
        .size:           8
        .value_kind:     global_buffer
      - .actual_access:  read_only
        .address_space:  global
        .offset:         48
        .size:           8
        .value_kind:     global_buffer
      - .address_space:  global
        .offset:         56
        .size:           8
        .value_kind:     global_buffer
      - .actual_access:  read_only
        .address_space:  global
        .offset:         64
        .size:           8
        .value_kind:     global_buffer
      - .actual_access:  read_only
        .address_space:  global
        .offset:         72
        .size:           8
        .value_kind:     global_buffer
      - .actual_access:  read_only
        .address_space:  global
        .offset:         80
        .size:           8
        .value_kind:     global_buffer
      - .address_space:  global
        .offset:         88
        .size:           8
        .value_kind:     global_buffer
      - .actual_access:  read_only
        .address_space:  global
        .offset:         96
        .size:           8
        .value_kind:     global_buffer
      - .actual_access:  read_only
        .address_space:  global
        .offset:         104
        .size:           8
        .value_kind:     global_buffer
      - .actual_access:  read_only
        .address_space:  global
        .offset:         112
        .size:           8
        .value_kind:     global_buffer
    .group_segment_fixed_size: 98816
    .kernarg_segment_align: 8
    .kernarg_segment_size: 120
    .language:       OpenCL C
    .language_version:
      - 2
      - 0
    .max_flat_workgroup_size: 512
    .name:           _Z4k_k2ILb0EEvPKDF16_S1_PKfS3_S3_S1_S1_PfS3_S3_S1_PDF16_PKiS4_S4_
    .private_segment_fixed_size: 0
    .sgpr_count:     106
    .sgpr_spill_count: 0
    .symbol:         _Z4k_k2ILb0EEvPKDF16_S1_PKfS3_S3_S1_S1_PfS3_S3_S1_PDF16_PKiS4_S4_.kd
    .uniform_work_group_size: 1
    .uses_dynamic_stack: false
    .vgpr_count:     232
    .vgpr_spill_count: 0
    .wavefront_size: 64
  - .agpr_count:     0
    .args:
      - .actual_access:  read_only
        .address_space:  global
        .offset:         0
        .size:           8
        .value_kind:     global_buffer
      - .actual_access:  read_only
        .address_space:  global
        .offset:         8
        .size:           8
        .value_kind:     global_buffer
      - .actual_access:  read_only
        .address_space:  global
        .offset:         16
        .size:           8
        .value_kind:     global_buffer
      - .actual_access:  read_only
        .address_space:  global
        .offset:         24
        .size:           8
        .value_kind:     global_buffer
      - .actual_access:  read_only
        .address_space:  global
        .offset:         32
        .size:           8
        .value_kind:     global_buffer
      - .actual_access:  read_only
        .address_space:  global
        .offset:         40
        .size:           8
        .value_kind:     global_buffer
      - .actual_access:  read_only
        .address_space:  global
        .offset:         48
        .size:           8
        .value_kind:     global_buffer
      - .actual_access:  read_only
        .address_space:  global
        .offset:         56
        .size:           8
        .value_kind:     global_buffer
      - .actual_access:  read_only
        .address_space:  global
        .offset:         64
        .size:           8
        .value_kind:     global_buffer
      - .actual_access:  read_only
        .address_space:  global
        .offset:         72
        .size:           8
        .value_kind:     global_buffer
      - .actual_access:  read_only
        .address_space:  global
        .offset:         80
        .size:           8
        .value_kind:     global_buffer
      - .actual_access:  read_only
        .address_space:  global
        .offset:         88
        .size:           8
        .value_kind:     global_buffer
      - .actual_access:  read_only
        .address_space:  global
        .offset:         96
        .size:           8
        .value_kind:     global_buffer
      - .actual_access:  write_only
        .address_space:  global
        .offset:         104
        .size:           8
        .value_kind:     global_buffer
      - .actual_access:  write_only
        .address_space:  global
        .offset:         112
        .size:           8
        .value_kind:     global_buffer
    .group_segment_fixed_size: 98816
    .kernarg_segment_align: 8
    .kernarg_segment_size: 120
    .language:       OpenCL C
    .language_version:
      - 2
      - 0
    .max_flat_workgroup_size: 512
    .name:           _Z4k_k2ILb1EEvPKDF16_S1_PKfS3_S3_S1_S1_PfS3_S3_S1_PDF16_PKiS4_S4_
    .private_segment_fixed_size: 0
    .sgpr_count:     44
    .sgpr_spill_count: 0
    .symbol:         _Z4k_k2ILb1EEvPKDF16_S1_PKfS3_S3_S1_S1_PfS3_S3_S1_PDF16_PKiS4_S4_.kd
    .uniform_work_group_size: 1
    .uses_dynamic_stack: false
    .vgpr_count:     196
    .vgpr_spill_count: 0
    .wavefront_size: 64
